# DPP instead of LDS round trips, part 2: 126 ds_bpermute_b32 with a provable lane^1/2/4/8 index in the row-wise passes (odd-layer c/qk norms, even-layer K norm and merge, norm2 router softmax) replaced
# baseline (speedup 1.0000x reference)
; __device__ __forceinline__ float wave_sum(float v) {
; #pragma unroll
;     for (int o = 1; o < 64; o <<= 1) v += __shfl_xor(v, o);
;     return v;
; __device__ __forceinline__ void odd_c_phase(Frame& F, KArgs a, int j) {
;     ...
;         for (int k = 0; k < RB; ++k) {
;             const int r = rw[k]; const int b = r / TPS, t = r - b * TPS; const bool lat = t < SEQ;
;             const float sq = wave_sum((cq[k][0] * cq[k][0] + cq[k][1] * cq[k][1]) + (cq[k][2] * cq[k][2] + cq[k][3] * cq[k][3]));
;             const float skv = wave_sum(ckv[k][0] * ckv[k][0] + ckv[k][1] * ckv[k][1]);
;             const float skr = wave_sum(kr[k] * kr[k]);
;             const float rq = rsqrtf(sq * (1.f / 256.f) + EPS), rkv = rsqrtf(skv * (1.f / 128.f) + EPS), rkr = rsqrtf(skr * (1.f / 32.f) + EPS);
;             bf16_t* cn = CN + (size_t)r * CNW;
;             float kv = kr[k] * rkr * gkr;
;             const float partner = __shfl_xor(kv, 8);
;             if (lat) { const int pos = (lane & 16) ? (t & 63) : (t >> 6); const f32x2 cs = R32[pos * 8 + (lane & 7)];
;                 kv = (lane & 8) ? (kv * cs.x + partner * cs.y) : (kv * cs.x - partner * cs.y); }
;             const float other = __shfl_down(kv, 1);
.LBB0_397:
	s_or_b64 exec, exec, s[14:15]
	s_waitcnt vmcnt(7)
	v_pk_mul_f32 v[38:39], v[20:21], v[20:21]
	v_pk_mul_f32 v[52:53], v[18:19], v[18:19]
	v_mov_b32_e32 v55, v39
	v_mov_b32_e32 v54, v52
	v_pk_mov_b32 v[38:39], v[52:53], v[38:39] op_sel:[1,0]
	s_waitcnt vmcnt(6)
	v_mul_f32_e32 v56, v51, v51
	v_pk_add_f32 v[38:39], v[38:39], v[54:55]
	s_nop 1
	v_mov_b32_dpp v54, v56 quad_perm:[1,0,3,2] row_mask:0xf bank_mask:0xf
	v_add_f32_e32 v38, v38, v39
	s_nop 1
	v_mov_b32_dpp v39, v38 quad_perm:[1,0,3,2] row_mask:0xf bank_mask:0xf
	s_mul_hi_i32 s10, s22, 0x3e0f83e1
	s_lshr_b32 s11, s10, 31
	s_ashr_i32 s10, s10, 11
	s_add_i32 s10, s10, s11
	s_waitcnt lgkmcnt(0)
	v_add_f32_e32 v38, v38, v39
	s_nop 1
	v_mov_b32_dpp v39, v38 quad_perm:[2,3,0,1] row_mask:0xf bank_mask:0xf
	s_mulk_i32 s10, 0x2100
	s_sub_i32 s14, s22, s10
	s_mov_b32 s10, 0x3d000000
	s_brev_b32 s11, 60
	s_waitcnt lgkmcnt(0)
	v_add_f32_e32 v38, v38, v39
	s_nop 1
	v_mov_b32_dpp v39, v38 row_shl:4 row_mask:0xf bank_mask:0x5
	v_mov_b32_dpp v39, v38 row_shr:4 row_mask:0xf bank_mask:0xa
	s_cmpk_gt_i32 s14, 0x1fff
	s_waitcnt lgkmcnt(0)
	v_add_f32_e32 v38, v38, v39
	s_nop 1
	v_mov_b32_dpp v39, v38 row_shl:8 row_mask:0xf bank_mask:0x3
	v_mov_b32_dpp v39, v38 row_shr:8 row_mask:0xf bank_mask:0xc
	s_waitcnt lgkmcnt(0)
	v_add_f32_e32 v38, v38, v39
	ds_bpermute_b32 v39, v43, v38
	s_waitcnt lgkmcnt(0)
	v_add_f32_e32 v52, v38, v39
	v_mul_f32_e32 v38, v37, v37
	v_pk_fma_f32 v[38:39], v[36:37], v[36:37], v[38:39] op_sel_hi:[1,1,0]
	s_nop 1
	v_mov_b32_dpp v55, v38 quad_perm:[1,0,3,2] row_mask:0xf bank_mask:0xf
	v_mov_b32_e32 v57, v38
	ds_bpermute_b32 v53, v44, v52
	s_waitcnt lgkmcnt(0)
	v_pk_add_f32 v[38:39], v[56:57], v[54:55]
	s_nop 1
	v_mov_b32_dpp v55, v39 quad_perm:[2,3,0,1] row_mask:0xf bank_mask:0xf
	s_nop 1
	v_mov_b32_dpp v54, v38 quad_perm:[2,3,0,1] row_mask:0xf bank_mask:0xf
	s_waitcnt lgkmcnt(0)
	v_pk_add_f32 v[38:39], v[38:39], v[54:55]
	s_nop 1
	v_mov_b32_dpp v55, v39 row_shl:4 row_mask:0xf bank_mask:0x5
	v_mov_b32_dpp v55, v39 row_shr:4 row_mask:0xf bank_mask:0xa
	s_nop 1
	v_mov_b32_dpp v54, v38 row_shl:4 row_mask:0xf bank_mask:0x5
	v_mov_b32_dpp v54, v38 row_shr:4 row_mask:0xf bank_mask:0xa
	s_waitcnt lgkmcnt(0)
	v_pk_add_f32 v[38:39], v[38:39], v[54:55]
	s_nop 1
	v_mov_b32_dpp v55, v39 row_shl:8 row_mask:0xf bank_mask:0x3
	v_mov_b32_dpp v55, v39 row_shr:8 row_mask:0xf bank_mask:0xc
	s_nop 1
	v_mov_b32_dpp v54, v38 row_shl:8 row_mask:0xf bank_mask:0x3
	v_mov_b32_dpp v54, v38 row_shr:8 row_mask:0xf bank_mask:0xc
	s_waitcnt lgkmcnt(0)
	v_pk_add_f32 v[38:39], v[38:39], v[54:55]
	ds_bpermute_b32 v55, v43, v39
	ds_bpermute_b32 v54, v43, v38
	s_waitcnt lgkmcnt(0)
	v_pk_add_f32 v[38:39], v[38:39], v[54:55]
	ds_bpermute_b32 v55, v44, v39
	ds_bpermute_b32 v54, v44, v38
	s_waitcnt lgkmcnt(0)
	v_pk_add_f32 v[38:39], v[38:39], v[54:55]
	s_nop 0
	v_pk_fma_f32 v[38:39], v[38:39], s[10:11], v[196:197] op_sel_hi:[1,1,0]
	s_nop 0
	v_cmp_gt_f32_e64 s[10:11], s95, v38
	v_mul_f32_e32 v54, 0x4b800000, v38
	v_cmp_gt_f32_e32 vcc, s95, v39
	v_cndmask_b32_e64 v38, v38, v54, s[10:11]
	v_rsq_f32_e32 v38, v38
	s_nop 0
	v_mul_f32_e32 v54, 0x45800000, v38
	v_cndmask_b32_e64 v38, v38, v54, s[10:11]
	v_mul_f32_e32 v38, v51, v38
	v_mul_f32_e32 v38, v23, v38
	s_nop 1
	v_mov_b32_dpp v51, v38 row_shl:8 row_mask:0xf bank_mask:0x3
	v_mov_b32_dpp v51, v38 row_shr:8 row_mask:0xf bank_mask:0xc
	s_cbranch_scc1 .LBB0_399
	s_and_b32 s10, s14, 63
	s_ashr_i32 s11, s14, 6
	v_mov_b32_e32 v54, s10
	v_mov_b32_e32 v55, s11
	v_cndmask_b32_e64 v54, v54, v55, s[6:7]
	v_lshl_or_b32 v54, v54, 3, v46
	v_ashrrev_i32_e32 v55, 31, v54
	v_lshl_add_u64 v[54:55], v[54:55], 3, s[26:27]
	global_load_dwordx2 v[54:55], v[54:55], off
	s_waitcnt vmcnt(0) lgkmcnt(0)
	v_mul_f32_e32 v51, v55, v51
	v_cndmask_b32_e64 v51, v51, -v51, s[8:9]
	v_fmac_f32_e32 v51, v38, v54
	v_mov_b32_e32 v38, v51

; __device__ __forceinline__ float wave_sum(float v) {
; #pragma unroll
;     for (int o = 1; o < 64; o <<= 1) v += __shfl_xor(v, o);
;     return v;
; __device__ __forceinline__ void odd_c_phase(Frame& F, KArgs a, int j) {
;     ...
;         for (int k = 0; k < RB; ++k) {
;             const int r = rw[k]; const int b = r / TPS, t = r - b * TPS; const bool lat = t < SEQ;
;             const float sq = wave_sum((cq[k][0] * cq[k][0] + cq[k][1] * cq[k][1]) + (cq[k][2] * cq[k][2] + cq[k][3] * cq[k][3]));
;             const float skv = wave_sum(ckv[k][0] * ckv[k][0] + ckv[k][1] * ckv[k][1]);
;             const float skr = wave_sum(kr[k] * kr[k]);
;             const float rq = rsqrtf(sq * (1.f / 256.f) + EPS), rkv = rsqrtf(skv * (1.f / 128.f) + EPS), rkr = rsqrtf(skr * (1.f / 32.f) + EPS);
;             bf16_t* cn = CN + (size_t)r * CNW;
;             float kv = kr[k] * rkr * gkr;
;             const float partner = __shfl_xor(kv, 8);
;             if (lat) { const int pos = (lane & 16) ? (t & 63) : (t >> 6); const f32x2 cs = R32[pos * 8 + (lane & 7)];
;                 kv = (lane & 8) ? (kv * cs.x + partner * cs.y) : (kv * cs.x - partner * cs.y); }
;             const float other = __shfl_down(kv, 1);
.LBB0_401:
	s_or_b64 exec, exec, s[10:11]
	s_waitcnt vmcnt(8)
	v_pk_mul_f32 v[18:19], v[16:17], v[16:17]
	v_pk_mul_f32 v[36:37], v[14:15], v[14:15]
	s_waitcnt lgkmcnt(0)
	v_mov_b32_e32 v39, v19
	v_mov_b32_e32 v38, v36
	v_pk_mov_b32 v[18:19], v[36:37], v[18:19] op_sel:[1,0]
	s_waitcnt vmcnt(7)
	v_mul_f32_e32 v52, v50, v50
	v_pk_add_f32 v[18:19], v[18:19], v[38:39]
	s_nop 1
	v_mov_b32_dpp v38, v52 quad_perm:[1,0,3,2] row_mask:0xf bank_mask:0xf
	v_add_f32_e32 v18, v18, v19
	s_nop 1
	v_mov_b32_dpp v19, v18 quad_perm:[1,0,3,2] row_mask:0xf bank_mask:0xf
	s_mul_hi_i32 s10, s50, 0x3e0f83e1
	s_lshr_b32 s11, s10, 31
	s_ashr_i32 s10, s10, 11
	s_add_i32 s10, s10, s11
	s_waitcnt lgkmcnt(0)
	v_add_f32_e32 v18, v18, v19
	s_nop 1
	v_mov_b32_dpp v19, v18 quad_perm:[2,3,0,1] row_mask:0xf bank_mask:0xf
	s_mulk_i32 s10, 0x2100
	s_sub_i32 s14, s50, s10
	s_mov_b32 s10, 0x3d000000
	s_brev_b32 s11, 60
	s_waitcnt lgkmcnt(0)
	v_add_f32_e32 v18, v18, v19
	s_nop 1
	v_mov_b32_dpp v19, v18 row_shl:4 row_mask:0xf bank_mask:0x5
	v_mov_b32_dpp v19, v18 row_shr:4 row_mask:0xf bank_mask:0xa
	s_cmpk_gt_i32 s14, 0x1fff
	s_waitcnt lgkmcnt(0)
	v_add_f32_e32 v18, v18, v19
	s_nop 1
	v_mov_b32_dpp v19, v18 row_shl:8 row_mask:0xf bank_mask:0x3
	v_mov_b32_dpp v19, v18 row_shr:8 row_mask:0xf bank_mask:0xc
	s_waitcnt lgkmcnt(0)
	v_add_f32_e32 v18, v18, v19
	ds_bpermute_b32 v19, v43, v18
	s_waitcnt lgkmcnt(0)
	v_add_f32_e32 v36, v18, v19
	v_mul_f32_e32 v18, v35, v35
	v_pk_fma_f32 v[18:19], v[34:35], v[34:35], v[18:19] op_sel_hi:[1,1,0]
	s_nop 1
	v_mov_b32_dpp v39, v18 quad_perm:[1,0,3,2] row_mask:0xf bank_mask:0xf
	v_mov_b32_e32 v53, v18
	ds_bpermute_b32 v37, v44, v36
	s_waitcnt lgkmcnt(0)
	v_pk_add_f32 v[18:19], v[52:53], v[38:39]
	s_nop 1
	v_mov_b32_dpp v39, v19 quad_perm:[2,3,0,1] row_mask:0xf bank_mask:0xf
	s_nop 1
	v_mov_b32_dpp v38, v18 quad_perm:[2,3,0,1] row_mask:0xf bank_mask:0xf
	s_waitcnt lgkmcnt(0)
	v_pk_add_f32 v[18:19], v[18:19], v[38:39]
	s_nop 1
	v_mov_b32_dpp v39, v19 row_shl:4 row_mask:0xf bank_mask:0x5
	v_mov_b32_dpp v39, v19 row_shr:4 row_mask:0xf bank_mask:0xa
	s_nop 1
	v_mov_b32_dpp v38, v18 row_shl:4 row_mask:0xf bank_mask:0x5
	v_mov_b32_dpp v38, v18 row_shr:4 row_mask:0xf bank_mask:0xa
	s_waitcnt lgkmcnt(0)
	v_pk_add_f32 v[18:19], v[18:19], v[38:39]
	s_nop 1
	v_mov_b32_dpp v39, v19 row_shl:8 row_mask:0xf bank_mask:0x3
	v_mov_b32_dpp v39, v19 row_shr:8 row_mask:0xf bank_mask:0xc
	s_nop 1
	v_mov_b32_dpp v38, v18 row_shl:8 row_mask:0xf bank_mask:0x3
	v_mov_b32_dpp v38, v18 row_shr:8 row_mask:0xf bank_mask:0xc
	s_waitcnt lgkmcnt(0)
	v_pk_add_f32 v[18:19], v[18:19], v[38:39]
	ds_bpermute_b32 v39, v43, v19
	ds_bpermute_b32 v38, v43, v18
	s_waitcnt lgkmcnt(0)
	v_pk_add_f32 v[18:19], v[18:19], v[38:39]
	ds_bpermute_b32 v39, v44, v19
	ds_bpermute_b32 v38, v44, v18
	s_waitcnt lgkmcnt(0)
	v_pk_add_f32 v[18:19], v[18:19], v[38:39]
	s_nop 0
	v_pk_fma_f32 v[18:19], v[18:19], s[10:11], v[196:197] op_sel_hi:[1,1,0]
	s_nop 0
	v_cmp_gt_f32_e32 vcc, s95, v18
	v_mul_f32_e32 v38, 0x4b800000, v18
	v_cmp_gt_f32_e64 s[10:11], s95, v19
	v_cndmask_b32_e32 v18, v18, v38, vcc
	v_rsq_f32_e32 v18, v18
	s_nop 0
	v_mul_f32_e32 v38, 0x45800000, v18
	v_cndmask_b32_e32 v18, v18, v38, vcc
	v_mul_f32_e32 v18, v50, v18
	v_mul_f32_e32 v18, v23, v18
	s_nop 1
	v_mov_b32_dpp v38, v18 row_shl:8 row_mask:0xf bank_mask:0x3
	v_mov_b32_dpp v38, v18 row_shr:8 row_mask:0xf bank_mask:0xc
	s_cbranch_scc1 .LBB0_403
	s_and_b32 s15, s14, 63
	s_ashr_i32 s14, s14, 6
	v_mov_b32_e32 v39, s15
	v_mov_b32_e32 v50, s14
	v_cndmask_b32_e64 v39, v39, v50, s[6:7]
	v_lshl_or_b32 v50, v39, 3, v46
	v_ashrrev_i32_e32 v51, 31, v50
	v_lshl_add_u64 v[50:51], v[50:51], 3, s[26:27]
	global_load_dwordx2 v[50:51], v[50:51], off
	s_waitcnt vmcnt(0) lgkmcnt(0)
	v_mul_f32_e32 v38, v51, v38
	v_cndmask_b32_e64 v38, v38, -v38, s[8:9]
	v_fmac_f32_e32 v38, v18, v50
	v_mov_b32_e32 v18, v38

; __device__ __forceinline__ float wave_sum(float v) {
; #pragma unroll
;     for (int o = 1; o < 64; o <<= 1) v += __shfl_xor(v, o);
;     return v;
; __device__ __forceinline__ void odd_c_phase(Frame& F, KArgs a, int j) {
;     ...
;         for (int k = 0; k < RB; ++k) {
;             const int r = rw[k]; const int b = r / TPS, t = r - b * TPS; const bool lat = t < SEQ;
;             const float sq = wave_sum((cq[k][0] * cq[k][0] + cq[k][1] * cq[k][1]) + (cq[k][2] * cq[k][2] + cq[k][3] * cq[k][3]));
;             const float skv = wave_sum(ckv[k][0] * ckv[k][0] + ckv[k][1] * ckv[k][1]);
;             const float skr = wave_sum(kr[k] * kr[k]);
;             const float rq = rsqrtf(sq * (1.f / 256.f) + EPS), rkv = rsqrtf(skv * (1.f / 128.f) + EPS), rkr = rsqrtf(skr * (1.f / 32.f) + EPS);
;             bf16_t* cn = CN + (size_t)r * CNW;
;             float kv = kr[k] * rkr * gkr;
;             const float partner = __shfl_xor(kv, 8);
;             if (lat) { const int pos = (lane & 16) ? (t & 63) : (t >> 6); const f32x2 cs = R32[pos * 8 + (lane & 7)];
;                 kv = (lane & 8) ? (kv * cs.x + partner * cs.y) : (kv * cs.x - partner * cs.y); }
;             const float other = __shfl_down(kv, 1);
.LBB0_407:
	s_waitcnt vmcnt(6)
	v_pk_mul_f32 v[14:15], v[12:13], v[12:13]
	v_pk_mul_f32 v[16:17], v[10:11], v[10:11]
	v_mov_b32_e32 v19, v15
	v_mov_b32_e32 v18, v16
	v_pk_mov_b32 v[14:15], v[16:17], v[14:15] op_sel:[1,0]
	s_waitcnt vmcnt(5)
	v_mul_f32_e32 v34, v49, v49
	v_pk_add_f32 v[14:15], v[14:15], v[18:19]
	s_nop 1
	v_mov_b32_dpp v18, v34 quad_perm:[1,0,3,2] row_mask:0xf bank_mask:0xf
	v_add_f32_e32 v14, v14, v15
	s_nop 1
	v_mov_b32_dpp v15, v14 quad_perm:[1,0,3,2] row_mask:0xf bank_mask:0xf
	s_mul_hi_i32 s10, s44, 0x3e0f83e1
	s_lshr_b32 s11, s10, 31
	s_ashr_i32 s10, s10, 11
	s_add_i32 s10, s10, s11
	s_waitcnt lgkmcnt(0)
	v_add_f32_e32 v14, v14, v15
	s_nop 1
	v_mov_b32_dpp v15, v14 quad_perm:[2,3,0,1] row_mask:0xf bank_mask:0xf
	s_mulk_i32 s10, 0x2100
	s_sub_i32 s14, s44, s10
	s_mov_b32 s10, 0x3d000000
	s_brev_b32 s11, 60
	s_waitcnt lgkmcnt(0)
	v_add_f32_e32 v14, v14, v15
	s_nop 1
	v_mov_b32_dpp v15, v14 row_shl:4 row_mask:0xf bank_mask:0x5
	v_mov_b32_dpp v15, v14 row_shr:4 row_mask:0xf bank_mask:0xa
	s_cmpk_gt_i32 s14, 0x1fff
	s_waitcnt lgkmcnt(0)
	v_add_f32_e32 v14, v14, v15
	s_nop 1
	v_mov_b32_dpp v15, v14 row_shl:8 row_mask:0xf bank_mask:0x3
	v_mov_b32_dpp v15, v14 row_shr:8 row_mask:0xf bank_mask:0xc
	s_waitcnt lgkmcnt(0)
	v_add_f32_e32 v14, v14, v15
	ds_bpermute_b32 v15, v43, v14
	s_waitcnt lgkmcnt(0)
	v_add_f32_e32 v16, v14, v15
	v_mul_f32_e32 v14, v33, v33
	v_pk_fma_f32 v[14:15], v[32:33], v[32:33], v[14:15] op_sel_hi:[1,1,0]
	s_nop 1
	v_mov_b32_dpp v19, v14 quad_perm:[1,0,3,2] row_mask:0xf bank_mask:0xf
	v_mov_b32_e32 v35, v14
	ds_bpermute_b32 v17, v44, v16
	s_waitcnt lgkmcnt(0)
	v_pk_add_f32 v[14:15], v[34:35], v[18:19]
	s_nop 1
	v_mov_b32_dpp v19, v15 quad_perm:[2,3,0,1] row_mask:0xf bank_mask:0xf
	s_nop 1
	v_mov_b32_dpp v18, v14 quad_perm:[2,3,0,1] row_mask:0xf bank_mask:0xf
	s_waitcnt lgkmcnt(0)
	v_pk_add_f32 v[14:15], v[14:15], v[18:19]
	s_nop 1
	v_mov_b32_dpp v19, v15 row_shl:4 row_mask:0xf bank_mask:0x5
	v_mov_b32_dpp v19, v15 row_shr:4 row_mask:0xf bank_mask:0xa
	s_nop 1
	v_mov_b32_dpp v18, v14 row_shl:4 row_mask:0xf bank_mask:0x5
	v_mov_b32_dpp v18, v14 row_shr:4 row_mask:0xf bank_mask:0xa
	s_waitcnt lgkmcnt(0)
	v_pk_add_f32 v[14:15], v[14:15], v[18:19]
	s_nop 1
	v_mov_b32_dpp v19, v15 row_shl:8 row_mask:0xf bank_mask:0x3
	v_mov_b32_dpp v19, v15 row_shr:8 row_mask:0xf bank_mask:0xc
	s_nop 1
	v_mov_b32_dpp v18, v14 row_shl:8 row_mask:0xf bank_mask:0x3
	v_mov_b32_dpp v18, v14 row_shr:8 row_mask:0xf bank_mask:0xc
	s_waitcnt lgkmcnt(0)
	v_pk_add_f32 v[14:15], v[14:15], v[18:19]
	ds_bpermute_b32 v19, v43, v15
	ds_bpermute_b32 v18, v43, v14
	s_waitcnt lgkmcnt(0)
	v_pk_add_f32 v[14:15], v[14:15], v[18:19]
	ds_bpermute_b32 v19, v44, v15
	ds_bpermute_b32 v18, v44, v14
	s_waitcnt lgkmcnt(0)
	v_pk_add_f32 v[14:15], v[14:15], v[18:19]
	s_nop 0
	v_pk_fma_f32 v[14:15], v[14:15], s[10:11], v[196:197] op_sel_hi:[1,1,0]
	s_nop 0
	v_cmp_gt_f32_e32 vcc, s95, v14
	v_mul_f32_e32 v18, 0x4b800000, v14
	v_cmp_gt_f32_e64 s[10:11], s95, v15
	v_cndmask_b32_e32 v14, v14, v18, vcc
	v_rsq_f32_e32 v14, v14
	s_nop 0
	v_mul_f32_e32 v18, 0x45800000, v14
	v_cndmask_b32_e32 v14, v14, v18, vcc
	v_mul_f32_e32 v14, v49, v14
	v_mul_f32_e32 v14, v23, v14
	s_nop 1
	v_mov_b32_dpp v18, v14 row_shl:8 row_mask:0xf bank_mask:0x3
	v_mov_b32_dpp v18, v14 row_shr:8 row_mask:0xf bank_mask:0xc
	s_cbranch_scc1 .LBB0_409
	s_and_b32 s15, s14, 63
	s_ashr_i32 s14, s14, 6
	v_mov_b32_e32 v19, s15
	v_mov_b32_e32 v34, s14
	v_cndmask_b32_e64 v19, v19, v34, s[6:7]
	v_lshl_or_b32 v34, v19, 3, v46
	v_ashrrev_i32_e32 v35, 31, v34
	v_lshl_add_u64 v[34:35], v[34:35], 3, s[26:27]
	global_load_dwordx2 v[34:35], v[34:35], off
	s_waitcnt vmcnt(0) lgkmcnt(0)
	v_mul_f32_e32 v18, v35, v18
	v_cndmask_b32_e64 v18, v18, -v18, s[8:9]
	v_fmac_f32_e32 v18, v14, v34
	v_mov_b32_e32 v14, v18

; __device__ __forceinline__ float wave_sum(float v) {
; #pragma unroll
;     for (int o = 1; o < 64; o <<= 1) v += __shfl_xor(v, o);
;     return v;
; __device__ __forceinline__ void odd_c_phase(Frame& F, KArgs a, int j) {
;     ...
;         for (int k = 0; k < RB; ++k) {
;             const int r = rw[k]; const int b = r / TPS, t = r - b * TPS; const bool lat = t < SEQ;
;             const float sq = wave_sum((cq[k][0] * cq[k][0] + cq[k][1] * cq[k][1]) + (cq[k][2] * cq[k][2] + cq[k][3] * cq[k][3]));
;             const float skv = wave_sum(ckv[k][0] * ckv[k][0] + ckv[k][1] * ckv[k][1]);
;             const float skr = wave_sum(kr[k] * kr[k]);
;             const float rq = rsqrtf(sq * (1.f / 256.f) + EPS), rkv = rsqrtf(skv * (1.f / 128.f) + EPS), rkr = rsqrtf(skr * (1.f / 32.f) + EPS);
;             bf16_t* cn = CN + (size_t)r * CNW;
;             float kv = kr[k] * rkr * gkr;
;             const float partner = __shfl_xor(kv, 8);
;             if (lat) { const int pos = (lane & 16) ? (t & 63) : (t >> 6); const f32x2 cs = R32[pos * 8 + (lane & 7)];
;                 kv = (lane & 8) ? (kv * cs.x + partner * cs.y) : (kv * cs.x - partner * cs.y); }
;             const float other = __shfl_down(kv, 1);
.LBB0_413:
	s_waitcnt vmcnt(4)
	v_pk_mul_f32 v[10:11], v[8:9], v[8:9]
	v_pk_mul_f32 v[12:13], v[6:7], v[6:7]
	v_mov_b32_e32 v15, v11
	v_mov_b32_e32 v14, v12
	v_pk_mov_b32 v[10:11], v[12:13], v[10:11] op_sel:[1,0]
	s_waitcnt vmcnt(3)
	v_mul_f32_e32 v16, v48, v48
	v_pk_add_f32 v[10:11], v[10:11], v[14:15]
	s_nop 1
	v_mov_b32_dpp v14, v16 quad_perm:[1,0,3,2] row_mask:0xf bank_mask:0xf
	v_add_f32_e32 v10, v10, v11
	s_nop 1
	v_mov_b32_dpp v11, v10 quad_perm:[1,0,3,2] row_mask:0xf bank_mask:0xf
	s_mul_hi_i32 s10, s36, 0x3e0f83e1
	s_lshr_b32 s11, s10, 31
	s_ashr_i32 s10, s10, 11
	s_add_i32 s10, s10, s11
	s_waitcnt lgkmcnt(0)
	v_add_f32_e32 v10, v10, v11
	s_nop 1
	v_mov_b32_dpp v11, v10 quad_perm:[2,3,0,1] row_mask:0xf bank_mask:0xf
	s_mulk_i32 s10, 0x2100
	s_sub_i32 s14, s36, s10
	s_mov_b32 s10, 0x3d000000
	s_brev_b32 s11, 60
	s_waitcnt lgkmcnt(0)
	v_add_f32_e32 v10, v10, v11
	s_nop 1
	v_mov_b32_dpp v11, v10 row_shl:4 row_mask:0xf bank_mask:0x5
	v_mov_b32_dpp v11, v10 row_shr:4 row_mask:0xf bank_mask:0xa
	s_cmpk_gt_i32 s14, 0x1fff
	s_waitcnt lgkmcnt(0)
	v_add_f32_e32 v10, v10, v11
	s_nop 1
	v_mov_b32_dpp v11, v10 row_shl:8 row_mask:0xf bank_mask:0x3
	v_mov_b32_dpp v11, v10 row_shr:8 row_mask:0xf bank_mask:0xc
	s_waitcnt lgkmcnt(0)
	v_add_f32_e32 v10, v10, v11
	ds_bpermute_b32 v11, v43, v10
	s_waitcnt lgkmcnt(0)
	v_add_f32_e32 v12, v10, v11
	v_mul_f32_e32 v10, v31, v31
	v_pk_fma_f32 v[10:11], v[30:31], v[30:31], v[10:11] op_sel_hi:[1,1,0]
	s_nop 1
	v_mov_b32_dpp v15, v10 quad_perm:[1,0,3,2] row_mask:0xf bank_mask:0xf
	v_mov_b32_e32 v17, v10
	ds_bpermute_b32 v13, v44, v12
	s_waitcnt lgkmcnt(0)
	v_pk_add_f32 v[10:11], v[16:17], v[14:15]
	s_nop 1
	v_mov_b32_dpp v15, v11 quad_perm:[2,3,0,1] row_mask:0xf bank_mask:0xf
	s_nop 1
	v_mov_b32_dpp v14, v10 quad_perm:[2,3,0,1] row_mask:0xf bank_mask:0xf
	s_waitcnt lgkmcnt(0)
	v_pk_add_f32 v[10:11], v[10:11], v[14:15]
	s_nop 1
	v_mov_b32_dpp v15, v11 row_shl:4 row_mask:0xf bank_mask:0x5
	v_mov_b32_dpp v15, v11 row_shr:4 row_mask:0xf bank_mask:0xa
	s_nop 1
	v_mov_b32_dpp v14, v10 row_shl:4 row_mask:0xf bank_mask:0x5
	v_mov_b32_dpp v14, v10 row_shr:4 row_mask:0xf bank_mask:0xa
	s_waitcnt lgkmcnt(0)
	v_pk_add_f32 v[10:11], v[10:11], v[14:15]
	s_nop 1
	v_mov_b32_dpp v15, v11 row_shl:8 row_mask:0xf bank_mask:0x3
	v_mov_b32_dpp v15, v11 row_shr:8 row_mask:0xf bank_mask:0xc
	s_nop 1
	v_mov_b32_dpp v14, v10 row_shl:8 row_mask:0xf bank_mask:0x3
	v_mov_b32_dpp v14, v10 row_shr:8 row_mask:0xf bank_mask:0xc
	s_waitcnt lgkmcnt(0)
	v_pk_add_f32 v[10:11], v[10:11], v[14:15]
	ds_bpermute_b32 v15, v43, v11
	ds_bpermute_b32 v14, v43, v10
	s_waitcnt lgkmcnt(0)
	v_pk_add_f32 v[10:11], v[10:11], v[14:15]
	ds_bpermute_b32 v15, v44, v11
	ds_bpermute_b32 v14, v44, v10
	s_waitcnt lgkmcnt(0)
	v_pk_add_f32 v[10:11], v[10:11], v[14:15]
	s_nop 0
	v_pk_fma_f32 v[10:11], v[10:11], s[10:11], v[196:197] op_sel_hi:[1,1,0]
	s_nop 0
	v_cmp_gt_f32_e32 vcc, s95, v10
	v_mul_f32_e32 v14, 0x4b800000, v10
	v_cmp_gt_f32_e64 s[10:11], s95, v11
	v_cndmask_b32_e32 v10, v10, v14, vcc
	v_rsq_f32_e32 v10, v10
	s_nop 0
	v_mul_f32_e32 v14, 0x45800000, v10
	v_cndmask_b32_e32 v10, v10, v14, vcc
	v_mul_f32_e32 v10, v48, v10
	v_mul_f32_e32 v10, v23, v10
	s_nop 1
	v_mov_b32_dpp v14, v10 row_shl:8 row_mask:0xf bank_mask:0x3
	v_mov_b32_dpp v14, v10 row_shr:8 row_mask:0xf bank_mask:0xc
	s_cbranch_scc1 .LBB0_415
	s_and_b32 s15, s14, 63
	s_ashr_i32 s14, s14, 6
	v_mov_b32_e32 v15, s15
	v_mov_b32_e32 v16, s14
	v_cndmask_b32_e64 v15, v15, v16, s[6:7]
	v_lshl_or_b32 v16, v15, 3, v46
	v_ashrrev_i32_e32 v17, 31, v16
	v_lshl_add_u64 v[16:17], v[16:17], 3, s[26:27]
	global_load_dwordx2 v[16:17], v[16:17], off
	s_waitcnt vmcnt(0) lgkmcnt(0)
	v_mul_f32_e32 v14, v17, v14
	v_cndmask_b32_e64 v14, v14, -v14, s[8:9]
	v_fmac_f32_e32 v14, v10, v16
	v_mov_b32_e32 v10, v14

; __device__ __forceinline__ unsigned cvtpk(float lo, float hi) { f32x2 v = {lo, hi}; bf16x2_t b = __builtin_convertvector(v, bf16x2_t); return __builtin_bit_cast(unsigned, b); }
; __device__ __forceinline__ float bf_lo(unsigned w) { return __uint_as_float(w << 16); }
; __device__ __forceinline__ float bf_hi(unsigned w) { return __uint_as_float(w & 0xffff0000u); }
; __device__ __forceinline__ void odd_qk_phase(Frame& F, KArgs a, int j) {
;     ...
;     for (int r0 = F.gw + ((NR - 1 - F.gw) / (RB * F.NGW)) * (RB * F.NGW); r0 >= 0; r0 -= RB * F.NGW) {
;         u32x4 ka[RB], kb[RB]; bool ok[RB]; bf16_t* pp[RB];
; #pragma unroll
;         for (int k = 0; k < RB; ++k) { int r = r0 + k * F.NGW; ok[k] = r < NR; if (!ok[k]) r = r0;
;             pp[k] = KN + (size_t)r * 1024 + hd * 64 + q4 * 16; ka[k] = *(const u32x4*)pp[k]; kb[k] = *(const u32x4*)(pp[k] + 8); }
; #pragma unroll
;         for (int k = 0; k < RB; ++k) {
;             float x[16];
; #pragma unroll
;             for (int i = 0; i < 4; ++i) { x[2 * i] = bf_lo(ka[k][i]); x[2 * i + 1] = bf_hi(ka[k][i]); x[8 + 2 * i] = bf_lo(kb[k][i]); x[8 + 2 * i + 1] = bf_hi(kb[k][i]); }
;             float sn = 0.f;
; #pragma unroll
;             for (int i = 0; i < 16; ++i) sn += x[i] * x[i];
;             sn += __shfl_xor(sn, 1); sn += __shfl_xor(sn, 2);
;             const float rn = rsqrtf(sn * (1.f / 64.f) + EPS);
;             u32x4 u1, u2;
; #pragma unroll
;             for (int i = 0; i < 4; ++i) { u1[i] = cvtpk(x[2 * i] * rn * gkn[2 * i], x[2 * i + 1] * rn * gkn[2 * i + 1]); u2[i] = cvtpk(x[8 + 2 * i] * rn * gkn[8 + 2 * i], x[8 + 2 * i + 1] * rn * gkn[8 + 2 * i + 1]); }
;             if (ok[k]) { *(u32x4*)pp[k] = u1; *(u32x4*)(pp[k] + 8) = u2; }
.LBB0_577:
	s_lshl_b64 s[4:5], s[38:39], 11
	v_lshl_add_u64 v[50:51], v[42:43], 0, s[4:5]
	global_load_dwordx4 v[56:59], v[50:51], off
	global_load_dwordx4 v[64:67], v[50:51], off offset:16
	s_add_i32 s6, s17, s38
	s_cmp_lt_i32 s6, 0x10800
	s_cselect_b64 s[14:15], -1, 0
	s_and_b64 s[4:5], s[14:15], exec
	s_cselect_b32 s4, s6, s38
	s_ashr_i32 s5, s4, 31
	s_add_i32 s25, s24, s38
	s_lshl_b64 s[4:5], s[4:5], 11
	s_cmp_lt_i32 s25, 0x10800
	s_cselect_b64 s[6:7], -1, 0
	v_lshl_add_u64 v[48:49], v[42:43], 0, s[4:5]
	s_and_b64 s[4:5], s[6:7], exec
	s_cselect_b32 s4, s25, s38
	s_mul_i32 s5, s3, 24
	s_add_i32 s25, s5, s38
	s_ashr_i32 s5, s4, 31
	s_lshl_b64 s[4:5], s[4:5], 11
	s_cmp_lt_i32 s25, 0x10800
	v_lshl_add_u64 v[46:47], v[42:43], 0, s[4:5]
	s_cselect_b64 s[4:5], -1, 0
	s_and_b64 s[28:29], s[4:5], exec
	s_cselect_b32 s28, s25, s38
	s_ashr_i32 s29, s28, 31
	s_lshl_b64 s[28:29], s[28:29], 11
	v_lshl_add_u64 v[44:45], v[42:43], 0, s[28:29]
	s_waitcnt lgkmcnt(0)
	global_load_dwordx4 v[34:37], v[48:49], off offset:16
	global_load_dwordx4 v[38:41], v[48:49], off
	global_load_dwordx4 v[26:29], v[46:47], off offset:16
	global_load_dwordx4 v[30:33], v[46:47], off
	global_load_dwordx4 v[18:21], v[44:45], off offset:16
	global_load_dwordx4 v[22:25], v[44:45], off
	s_cmp_gt_u32 s38, 0x107ff
	s_waitcnt vmcnt(7)
	v_lshlrev_b32_e32 v52, 16, v56
	v_and_b32_e32 v53, 0xffff0000, v56
	v_lshlrev_b32_e32 v54, 16, v57
	v_and_b32_e32 v55, 0xffff0000, v57
	v_pk_mul_f32 v[70:71], v[52:53], v[52:53]
	v_pk_mul_f32 v[72:73], v[54:55], v[54:55]
	v_add_f32_e32 v70, v70, v71
	v_lshlrev_b32_e32 v56, 16, v58
	v_and_b32_e32 v57, 0xffff0000, v58
	v_add_f32_e32 v70, v72, v70
	v_pk_mul_f32 v[74:75], v[56:57], v[56:57]
	v_add_f32_e32 v70, v73, v70
	v_lshlrev_b32_e32 v58, 16, v59
	v_and_b32_e32 v59, 0xffff0000, v59
	v_add_f32_e32 v70, v74, v70
	v_pk_mul_f32 v[76:77], v[58:59], v[58:59]
	v_add_f32_e32 v70, v75, v70
	s_waitcnt vmcnt(6)
	v_lshlrev_b32_e32 v60, 16, v64
	v_and_b32_e32 v61, 0xffff0000, v64
	v_add_f32_e32 v70, v76, v70
	v_pk_mul_f32 v[78:79], v[60:61], v[60:61]
	v_add_f32_e32 v70, v77, v70
	v_lshlrev_b32_e32 v62, 16, v65
	v_and_b32_e32 v63, 0xffff0000, v65
	v_add_f32_e32 v70, v78, v70
	v_pk_mul_f32 v[80:81], v[62:63], v[62:63]
	v_add_f32_e32 v70, v79, v70
	v_lshlrev_b32_e32 v64, 16, v66
	v_and_b32_e32 v65, 0xffff0000, v66
	v_add_f32_e32 v70, v80, v70
	v_pk_mul_f32 v[82:83], v[64:65], v[64:65]
	v_add_f32_e32 v70, v81, v70
	v_lshlrev_b32_e32 v66, 16, v67
	v_and_b32_e32 v67, 0xffff0000, v67
	v_add_f32_e32 v70, v82, v70
	v_pk_mul_f32 v[84:85], v[66:67], v[66:67]
	v_add_f32_e32 v70, v83, v70
	v_add_f32_e32 v70, v84, v70
	v_add_f32_e32 v70, v85, v70
	ds_bpermute_b32 v71, v68, v70
	s_waitcnt lgkmcnt(0)
	v_add_f32_e32 v70, v70, v71
	s_nop 1
	v_mov_b32_dpp v71, v70 quad_perm:[2,3,0,1] row_mask:0xf bank_mask:0xf
	s_cbranch_scc1 .LBB0_579
	s_waitcnt lgkmcnt(0)
	v_add_f32_e32 v70, v70, v71
	v_fmamk_f32 v70, v70, 0x3c800000, v196
	v_mul_f32_e32 v71, 0x4b800000, v70
	v_cmp_gt_f32_e32 vcc, s95, v70
	s_nop 1
	v_cndmask_b32_e32 v70, v70, v71, vcc
	v_rsq_f32_e32 v70, v70
	s_nop 0
	v_mul_f32_e32 v71, 0x45800000, v70
	v_cndmask_b32_e32 v70, v70, v71, vcc
	v_pk_mul_f32 v[52:53], v[70:71], v[52:53] op_sel_hi:[0,1]
	v_pk_mul_f32 v[54:55], v[70:71], v[54:55] op_sel_hi:[0,1]
	v_pk_mul_f32 v[60:61], v[70:71], v[60:61] op_sel_hi:[0,1]
	v_pk_mul_f32 v[62:63], v[70:71], v[62:63] op_sel_hi:[0,1]
	v_pk_mul_f32 v[52:53], v[14:15], v[52:53]
	v_pk_mul_f32 v[54:55], v[16:17], v[54:55]
	v_pk_mul_f32 v[60:61], v[6:7], v[60:61]
	v_pk_mul_f32 v[62:63], v[8:9], v[62:63]
	v_cvt_pk_bf16_f32 v52, v52, v53
	v_cvt_pk_bf16_f32 v53, v54, v55
	v_pk_mul_f32 v[54:55], v[70:71], v[56:57] op_sel_hi:[0,1]
	v_pk_mul_f32 v[56:57], v[70:71], v[58:59] op_sel_hi:[0,1]
	v_cvt_pk_bf16_f32 v60, v60, v61
	v_cvt_pk_bf16_f32 v61, v62, v63
	v_pk_mul_f32 v[62:63], v[70:71], v[64:65] op_sel_hi:[0,1]
	v_pk_mul_f32 v[64:65], v[70:71], v[66:67] op_sel_hi:[0,1]
	v_pk_mul_f32 v[54:55], v[10:11], v[54:55]
	v_pk_mul_f32 v[56:57], v[12:13], v[56:57]
	v_pk_mul_f32 v[62:63], v[2:3], v[62:63]
	v_pk_mul_f32 v[64:65], v[4:5], v[64:65]
	v_cvt_pk_bf16_f32 v54, v54, v55
	v_cvt_pk_bf16_f32 v55, v56, v57
	v_cvt_pk_bf16_f32 v62, v62, v63
	v_cvt_pk_bf16_f32 v63, v64, v65
	global_store_dwordx4 v[50:51], v[52:55], off
	global_store_dwordx4 v[50:51], v[60:63], off offset:16
; __device__ __forceinline__ unsigned cvtpk(float lo, float hi) { f32x2 v = {lo, hi}; bf16x2_t b = __builtin_convertvector(v, bf16x2_t); return __builtin_bit_cast(unsigned, b); }
; __device__ __forceinline__ float bf_lo(unsigned w) { return __uint_as_float(w << 16); }
; __device__ __forceinline__ float bf_hi(unsigned w) { return __uint_as_float(w & 0xffff0000u); }
; __device__ __forceinline__ void odd_qk_phase(Frame& F, KArgs a, int j) {
;     ...
;         for (int k = 0; k < RB; ++k) {
;             float x[16];
; #pragma unroll
;             for (int i = 0; i < 4; ++i) { x[2 * i] = bf_lo(ka[k][i]); x[2 * i + 1] = bf_hi(ka[k][i]); x[8 + 2 * i] = bf_lo(kb[k][i]); x[8 + 2 * i + 1] = bf_hi(kb[k][i]); }
;             float sn = 0.f;
; #pragma unroll
;             for (int i = 0; i < 16; ++i) sn += x[i] * x[i];
;             sn += __shfl_xor(sn, 1); sn += __shfl_xor(sn, 2);
;             const float rn = rsqrtf(sn * (1.f / 64.f) + EPS);
;             u32x4 u1, u2;
; #pragma unroll
;             for (int i = 0; i < 4; ++i) { u1[i] = cvtpk(x[2 * i] * rn * gkn[2 * i], x[2 * i + 1] * rn * gkn[2 * i + 1]); u2[i] = cvtpk(x[8 + 2 * i] * rn * gkn[8 + 2 * i], x[8 + 2 * i + 1] * rn * gkn[8 + 2 * i + 1]); }
;             if (ok[k]) { *(u32x4*)pp[k] = u1; *(u32x4*)(pp[k] + 8) = u2; }
.LBB0_579:
	s_waitcnt vmcnt(4)
	v_lshlrev_b32_e32 v50, 16, v38
	v_and_b32_e32 v51, 0xffff0000, v38
	v_lshlrev_b32_e32 v38, 16, v39
	v_and_b32_e32 v39, 0xffff0000, v39
	v_pk_mul_f32 v[58:59], v[50:51], v[50:51]
	v_pk_mul_f32 v[60:61], v[38:39], v[38:39]
	v_add_f32_e32 v58, v58, v59
	v_lshlrev_b32_e32 v52, 16, v34
	v_and_b32_e32 v53, 0xffff0000, v34
	v_lshlrev_b32_e32 v54, 16, v35
	v_and_b32_e32 v55, 0xffff0000, v35
	v_lshlrev_b32_e32 v34, 16, v40
	v_and_b32_e32 v35, 0xffff0000, v40
	v_add_f32_e32 v58, v60, v58
	v_pk_mul_f32 v[62:63], v[34:35], v[34:35]
	v_add_f32_e32 v58, v61, v58
	v_lshlrev_b32_e32 v40, 16, v41
	v_and_b32_e32 v41, 0xffff0000, v41
	v_add_f32_e32 v58, v62, v58
	v_pk_mul_f32 v[64:65], v[40:41], v[40:41]
	v_add_f32_e32 v58, v63, v58
	v_add_f32_e32 v58, v64, v58
	v_pk_mul_f32 v[66:67], v[52:53], v[52:53]
	v_add_f32_e32 v58, v65, v58
	v_add_f32_e32 v58, v66, v58
	s_waitcnt lgkmcnt(0)
	v_pk_mul_f32 v[70:71], v[54:55], v[54:55]
	v_add_f32_e32 v58, v67, v58
	v_lshlrev_b32_e32 v56, 16, v36
	v_and_b32_e32 v57, 0xffff0000, v36
	v_add_f32_e32 v58, v70, v58
	v_pk_mul_f32 v[72:73], v[56:57], v[56:57]
	v_add_f32_e32 v58, v71, v58
	v_lshlrev_b32_e32 v36, 16, v37
	v_and_b32_e32 v37, 0xffff0000, v37
	v_add_f32_e32 v58, v72, v58
	v_pk_mul_f32 v[74:75], v[36:37], v[36:37]
	v_add_f32_e32 v58, v73, v58
	v_add_f32_e32 v58, v74, v58
	v_add_f32_e32 v58, v75, v58
	ds_bpermute_b32 v59, v68, v58
	s_andn2_b64 vcc, exec, s[14:15]
	s_waitcnt lgkmcnt(0)
	v_add_f32_e32 v58, v58, v59
	s_nop 1
	v_mov_b32_dpp v59, v58 quad_perm:[2,3,0,1] row_mask:0xf bank_mask:0xf
	s_cbranch_vccnz .LBB0_581
	s_waitcnt lgkmcnt(0)
	v_add_f32_e32 v58, v58, v59
	v_fmamk_f32 v58, v58, 0x3c800000, v196
	v_mul_f32_e32 v59, 0x4b800000, v58
	v_cmp_gt_f32_e32 vcc, s95, v58
	s_nop 1
	v_cndmask_b32_e32 v58, v58, v59, vcc
	v_rsq_f32_e32 v58, v58
	s_nop 0
	v_mul_f32_e32 v59, 0x45800000, v58
	v_cndmask_b32_e32 v58, v58, v59, vcc
	v_pk_mul_f32 v[52:53], v[58:59], v[52:53] op_sel_hi:[0,1]
	v_pk_mul_f32 v[54:55], v[58:59], v[54:55] op_sel_hi:[0,1]
	v_pk_mul_f32 v[52:53], v[6:7], v[52:53]
	v_pk_mul_f32 v[54:55], v[8:9], v[54:55]
	v_cvt_pk_bf16_f32 v52, v52, v53
	v_cvt_pk_bf16_f32 v53, v54, v55
	v_pk_mul_f32 v[54:55], v[58:59], v[56:57] op_sel_hi:[0,1]
	v_pk_mul_f32 v[36:37], v[58:59], v[36:37] op_sel_hi:[0,1]
	v_pk_mul_f32 v[54:55], v[2:3], v[54:55]
	v_pk_mul_f32 v[36:37], v[4:5], v[36:37]
	v_cvt_pk_bf16_f32 v54, v54, v55
	v_cvt_pk_bf16_f32 v55, v36, v37
	v_pk_mul_f32 v[36:37], v[58:59], v[50:51] op_sel_hi:[0,1]
	v_pk_mul_f32 v[38:39], v[58:59], v[38:39] op_sel_hi:[0,1]
	v_pk_mul_f32 v[34:35], v[58:59], v[34:35] op_sel_hi:[0,1]
	v_pk_mul_f32 v[36:37], v[14:15], v[36:37]
	v_pk_mul_f32 v[38:39], v[16:17], v[38:39]
	v_pk_mul_f32 v[34:35], v[10:11], v[34:35]
	v_cvt_pk_bf16_f32 v36, v36, v37
	v_cvt_pk_bf16_f32 v37, v38, v39
	v_cvt_pk_bf16_f32 v38, v34, v35
	v_pk_mul_f32 v[34:35], v[58:59], v[40:41] op_sel_hi:[0,1]
	v_pk_mul_f32 v[34:35], v[12:13], v[34:35]
	s_nop 0
	v_cvt_pk_bf16_f32 v39, v34, v35
	global_store_dwordx4 v[48:49], v[36:39], off
	global_store_dwordx4 v[48:49], v[52:55], off offset:16
.LBB0_581:
	s_waitcnt vmcnt(2)
	v_lshlrev_b32_e32 v34, 16, v30
	v_and_b32_e32 v35, 0xffff0000, v30
	v_lshlrev_b32_e32 v30, 16, v31
	v_and_b32_e32 v31, 0xffff0000, v31
	v_pk_mul_f32 v[48:49], v[34:35], v[34:35]
	v_pk_mul_f32 v[50:51], v[30:31], v[30:31]
	v_add_f32_e32 v48, v48, v49
	v_lshlrev_b32_e32 v36, 16, v26
	v_and_b32_e32 v37, 0xffff0000, v26
	v_lshlrev_b32_e32 v38, 16, v27
	v_and_b32_e32 v39, 0xffff0000, v27
	v_lshlrev_b32_e32 v26, 16, v32
	v_and_b32_e32 v27, 0xffff0000, v32
	v_add_f32_e32 v48, v50, v48
	v_pk_mul_f32 v[52:53], v[26:27], v[26:27]
	v_add_f32_e32 v48, v51, v48
	v_lshlrev_b32_e32 v32, 16, v33
	v_and_b32_e32 v33, 0xffff0000, v33
	v_add_f32_e32 v48, v52, v48
	v_pk_mul_f32 v[54:55], v[32:33], v[32:33]
	v_add_f32_e32 v48, v53, v48
	v_add_f32_e32 v48, v54, v48
	v_pk_mul_f32 v[56:57], v[36:37], v[36:37]
	v_add_f32_e32 v48, v55, v48
	v_add_f32_e32 v48, v56, v48
	s_waitcnt lgkmcnt(0)
	v_pk_mul_f32 v[58:59], v[38:39], v[38:39]
	v_add_f32_e32 v48, v57, v48
	v_lshlrev_b32_e32 v40, 16, v28
	v_and_b32_e32 v41, 0xffff0000, v28
	v_add_f32_e32 v48, v58, v48
	v_pk_mul_f32 v[60:61], v[40:41], v[40:41]
	v_add_f32_e32 v48, v59, v48
	v_lshlrev_b32_e32 v28, 16, v29
	v_and_b32_e32 v29, 0xffff0000, v29
	v_add_f32_e32 v48, v60, v48
	v_pk_mul_f32 v[62:63], v[28:29], v[28:29]
	v_add_f32_e32 v48, v61, v48
	v_add_f32_e32 v48, v62, v48
	v_add_f32_e32 v48, v63, v48
	ds_bpermute_b32 v49, v68, v48
	s_andn2_b64 vcc, exec, s[6:7]
	s_waitcnt lgkmcnt(0)
	v_add_f32_e32 v48, v48, v49
	s_nop 1
	v_mov_b32_dpp v49, v48 quad_perm:[2,3,0,1] row_mask:0xf bank_mask:0xf
	s_cbranch_vccnz .LBB0_583
	s_waitcnt lgkmcnt(0)
	v_add_f32_e32 v48, v48, v49
	v_fmamk_f32 v48, v48, 0x3c800000, v196
	v_mul_f32_e32 v49, 0x4b800000, v48
	v_cmp_gt_f32_e32 vcc, s95, v48
	s_nop 1
	v_cndmask_b32_e32 v48, v48, v49, vcc
	v_rsq_f32_e32 v48, v48
	s_nop 0
	v_mul_f32_e32 v49, 0x45800000, v48
	v_cndmask_b32_e32 v48, v48, v49, vcc
	v_pk_mul_f32 v[36:37], v[48:49], v[36:37] op_sel_hi:[0,1]
	v_pk_mul_f32 v[38:39], v[48:49], v[38:39] op_sel_hi:[0,1]
	v_pk_mul_f32 v[36:37], v[6:7], v[36:37]
	v_pk_mul_f32 v[38:39], v[8:9], v[38:39]
	v_cvt_pk_bf16_f32 v36, v36, v37
	v_cvt_pk_bf16_f32 v37, v38, v39
	v_pk_mul_f32 v[38:39], v[48:49], v[40:41] op_sel_hi:[0,1]
	v_pk_mul_f32 v[28:29], v[48:49], v[28:29] op_sel_hi:[0,1]
	v_pk_mul_f32 v[38:39], v[2:3], v[38:39]
	v_pk_mul_f32 v[28:29], v[4:5], v[28:29]
	v_cvt_pk_bf16_f32 v38, v38, v39
	v_cvt_pk_bf16_f32 v39, v28, v29
	v_pk_mul_f32 v[28:29], v[48:49], v[34:35] op_sel_hi:[0,1]
	v_pk_mul_f32 v[30:31], v[48:49], v[30:31] op_sel_hi:[0,1]
	v_pk_mul_f32 v[26:27], v[48:49], v[26:27] op_sel_hi:[0,1]
	v_pk_mul_f32 v[28:29], v[14:15], v[28:29]
	v_pk_mul_f32 v[30:31], v[16:17], v[30:31]
	v_pk_mul_f32 v[26:27], v[10:11], v[26:27]
	v_cvt_pk_bf16_f32 v28, v28, v29
	v_cvt_pk_bf16_f32 v29, v30, v31
	v_cvt_pk_bf16_f32 v30, v26, v27
	v_pk_mul_f32 v[26:27], v[48:49], v[32:33] op_sel_hi:[0,1]
	v_pk_mul_f32 v[26:27], v[12:13], v[26:27]
	s_nop 0
	v_cvt_pk_bf16_f32 v31, v26, v27
	global_store_dwordx4 v[46:47], v[28:31], off
	global_store_dwordx4 v[46:47], v[36:39], off offset:16
; __device__ __forceinline__ unsigned cvtpk(float lo, float hi) { f32x2 v = {lo, hi}; bf16x2_t b = __builtin_convertvector(v, bf16x2_t); return __builtin_bit_cast(unsigned, b); }
; __device__ __forceinline__ float bf_lo(unsigned w) { return __uint_as_float(w << 16); }
; __device__ __forceinline__ float bf_hi(unsigned w) { return __uint_as_float(w & 0xffff0000u); }
; __device__ __forceinline__ void odd_qk_phase(Frame& F, KArgs a, int j) {
;     ...
;         for (int k = 0; k < RB; ++k) {
;             float x[16];
; #pragma unroll
;             for (int i = 0; i < 4; ++i) { x[2 * i] = bf_lo(ka[k][i]); x[2 * i + 1] = bf_hi(ka[k][i]); x[8 + 2 * i] = bf_lo(kb[k][i]); x[8 + 2 * i + 1] = bf_hi(kb[k][i]); }
;             float sn = 0.f;
; #pragma unroll
;             for (int i = 0; i < 16; ++i) sn += x[i] * x[i];
;             sn += __shfl_xor(sn, 1); sn += __shfl_xor(sn, 2);
;             const float rn = rsqrtf(sn * (1.f / 64.f) + EPS);
;             u32x4 u1, u2;
; #pragma unroll
;             for (int i = 0; i < 4; ++i) { u1[i] = cvtpk(x[2 * i] * rn * gkn[2 * i], x[2 * i + 1] * rn * gkn[2 * i + 1]); u2[i] = cvtpk(x[8 + 2 * i] * rn * gkn[8 + 2 * i], x[8 + 2 * i + 1] * rn * gkn[8 + 2 * i + 1]); }
;             if (ok[k]) { *(u32x4*)pp[k] = u1; *(u32x4*)(pp[k] + 8) = u2; }
.LBB0_583:
	s_waitcnt vmcnt(0)
	v_lshlrev_b32_e32 v26, 16, v22
	v_and_b32_e32 v27, 0xffff0000, v22
	v_lshlrev_b32_e32 v22, 16, v23
	v_and_b32_e32 v23, 0xffff0000, v23
	v_pk_mul_f32 v[34:35], v[26:27], v[26:27]
	v_pk_mul_f32 v[36:37], v[22:23], v[22:23]
	v_add_f32_e32 v34, v34, v35
	v_lshlrev_b32_e32 v28, 16, v18
	v_and_b32_e32 v29, 0xffff0000, v18
	v_lshlrev_b32_e32 v30, 16, v19
	v_and_b32_e32 v31, 0xffff0000, v19
	v_lshlrev_b32_e32 v18, 16, v24
	v_and_b32_e32 v19, 0xffff0000, v24
	v_add_f32_e32 v34, v36, v34
	v_pk_mul_f32 v[38:39], v[18:19], v[18:19]
	v_add_f32_e32 v34, v37, v34
	v_lshlrev_b32_e32 v24, 16, v25
	v_and_b32_e32 v25, 0xffff0000, v25
	v_add_f32_e32 v34, v38, v34
	v_pk_mul_f32 v[40:41], v[24:25], v[24:25]
	v_add_f32_e32 v34, v39, v34
	v_add_f32_e32 v34, v40, v34
	v_pk_mul_f32 v[46:47], v[28:29], v[28:29]
	v_add_f32_e32 v34, v41, v34
	v_add_f32_e32 v34, v46, v34
	s_waitcnt lgkmcnt(0)
	v_pk_mul_f32 v[48:49], v[30:31], v[30:31]
	v_add_f32_e32 v34, v47, v34
	v_lshlrev_b32_e32 v32, 16, v20
	v_and_b32_e32 v33, 0xffff0000, v20
	v_add_f32_e32 v34, v48, v34
	v_pk_mul_f32 v[50:51], v[32:33], v[32:33]
	v_add_f32_e32 v34, v49, v34
	v_lshlrev_b32_e32 v20, 16, v21
	v_and_b32_e32 v21, 0xffff0000, v21
	v_add_f32_e32 v34, v50, v34
	v_pk_mul_f32 v[52:53], v[20:21], v[20:21]
	v_add_f32_e32 v34, v51, v34
	v_add_f32_e32 v34, v52, v34
	v_add_f32_e32 v34, v53, v34
	ds_bpermute_b32 v35, v68, v34
	s_andn2_b64 vcc, exec, s[4:5]
	s_waitcnt lgkmcnt(0)
	v_add_f32_e32 v34, v34, v35
	s_nop 1
	v_mov_b32_dpp v35, v34 quad_perm:[2,3,0,1] row_mask:0xf bank_mask:0xf
	s_cbranch_vccnz .LBB0_576
	s_waitcnt lgkmcnt(0)
	v_add_f32_e32 v34, v34, v35
	v_fmamk_f32 v34, v34, 0x3c800000, v196
	v_mul_f32_e32 v35, 0x4b800000, v34
	v_cmp_gt_f32_e32 vcc, s95, v34
	s_nop 1
	v_cndmask_b32_e32 v34, v34, v35, vcc
	v_rsq_f32_e32 v34, v34
	s_nop 0
	v_mul_f32_e32 v35, 0x45800000, v34
	v_cndmask_b32_e32 v34, v34, v35, vcc
	v_pk_mul_f32 v[28:29], v[34:35], v[28:29] op_sel_hi:[0,1]
	v_pk_mul_f32 v[30:31], v[34:35], v[30:31] op_sel_hi:[0,1]
	v_pk_mul_f32 v[28:29], v[6:7], v[28:29]
	v_pk_mul_f32 v[30:31], v[8:9], v[30:31]
	v_cvt_pk_bf16_f32 v28, v28, v29
	v_cvt_pk_bf16_f32 v29, v30, v31
	v_pk_mul_f32 v[30:31], v[34:35], v[32:33] op_sel_hi:[0,1]
	v_pk_mul_f32 v[20:21], v[34:35], v[20:21] op_sel_hi:[0,1]
	v_pk_mul_f32 v[30:31], v[2:3], v[30:31]
	v_pk_mul_f32 v[20:21], v[4:5], v[20:21]
	v_cvt_pk_bf16_f32 v30, v30, v31
	v_cvt_pk_bf16_f32 v31, v20, v21
	v_pk_mul_f32 v[20:21], v[34:35], v[26:27] op_sel_hi:[0,1]
	v_pk_mul_f32 v[22:23], v[34:35], v[22:23] op_sel_hi:[0,1]
	v_pk_mul_f32 v[18:19], v[34:35], v[18:19] op_sel_hi:[0,1]
	v_pk_mul_f32 v[20:21], v[14:15], v[20:21]
	v_pk_mul_f32 v[22:23], v[16:17], v[22:23]
	v_pk_mul_f32 v[18:19], v[10:11], v[18:19]
	v_cvt_pk_bf16_f32 v20, v20, v21
	v_cvt_pk_bf16_f32 v21, v22, v23
	v_cvt_pk_bf16_f32 v22, v18, v19
	v_pk_mul_f32 v[18:19], v[34:35], v[24:25] op_sel_hi:[0,1]
	v_pk_mul_f32 v[18:19], v[12:13], v[18:19]
	s_nop 0
	v_cvt_pk_bf16_f32 v23, v18, v19
	global_store_dwordx4 v[44:45], v[20:23], off
	global_store_dwordx4 v[44:45], v[28:31], off offset:16
	s_branch .LBB0_576

; __device__ __forceinline__ float bf_lo(unsigned w) { return __uint_as_float(w << 16); }
; __device__ __forceinline__ float bf_hi(unsigned w) { return __uint_as_float(w & 0xffff0000u); }
; __device__ __forceinline__ void even_qk_phase(Frame& F, KArgs a, int j) {
;     ...
;     for (int r0 = F.gw + ((NR - 1 - F.gw) / (RB * F.NGW)) * (RB * F.NGW); r0 >= 0; r0 -= RB * F.NGW) {
;         u32x4 w1[RB], w2[RB]; bool ok[RB]; int tt[RB]; bf16_t* rowp[RB];
; #pragma unroll
;         for (int k = 0; k < RB; ++k) {
;             int r = r0 + k * F.NGW; ok[k] = r < NR; if (!ok[k]) r = r0;
;             const int b = r / TPS; tt[k] = r - b * TPS; rowp[k] = QK + (size_t)r * QKW + hc * 64;
;             w1[k] = *(const u32x4*)(rowp[k] + d1); w2[k] = *(const u32x4*)(rowp[k] + d2);
;         }
; #pragma unroll
;         for (int k = 0; k < RB; ++k) {
;             const int t = tt[k]; const bool lat = t < SEQ; const int pos = (q4 >> 1) ? (t & 63) : (t >> 6);
;             float x1[8], x2[8];
; #pragma unroll
;             for (int i = 0; i < 4; ++i) { x1[2 * i] = bf_lo(w1[k][i]); x1[2 * i + 1] = bf_hi(w1[k][i]); x2[2 * i] = bf_lo(w2[k][i]); x2[2 * i + 1] = bf_hi(w2[k][i]); }
;             float ss = 0.f;
; #pragma unroll
;             for (int i = 0; i < 8; ++i) ss += x1[i] * x1[i] + x2[i] * x2[i];
;             ss += __shfl_xor(ss, 1); ss += __shfl_xor(ss, 2);
;             const float rstd = rsqrtf(ss * (1.f / 64.f) + EPS);
;             float o1[8], o2[8];
; #pragma unroll
;             for (int i = 0; i < 8; ++i) {
;                 const float a1 = x1[i] * rstd * g1[i], a2 = x2[i] * rstd * g2[i];
;                 float c = 1.f, s_ = 0.f;
;                 if (lat) { const f32x2 cs = R64[pos * 16 + (q4 & 1) * 8 + i]; c = cs.x; s_ = cs.y; }
;                 o1[i] = a1 * c - a2 * s_; o2[i] = a2 * c + a1 * s_;
;             }
;             if (hact && ok[k]) { u32x4 u1, u2;
.LBB0_811:
	s_waitcnt vmcnt(0)
	v_mad_u64_u32 v[52:53], s[8:9], s17, v234, v[42:43]
	global_load_dwordx4 v[68:71], v[52:53], off
	global_load_dwordx4 v[72:75], v[52:53], off offset:32
	s_mul_hi_u32 s8, s17, 0x3e0f83e1
	s_lshr_b32 s8, s8, 11
	s_mulk_i32 s8, 0xdf00
	s_add_i32 s14, s24, s17
	s_add_i32 s38, s17, s8
	s_cmp_gt_i32 s14, 0x107ff
	s_cselect_b64 s[40:41], -1, 0
	s_and_b64 s[8:9], s[40:41], exec
	s_cselect_b32 s31, s17, s14
	s_add_i32 s14, s25, s17
	s_cmp_gt_i32 s14, 0x107ff
	s_cselect_b64 s[36:37], -1, 0
	v_mad_i64_i32 v[50:51], s[8:9], s31, v234, v[42:43]
	s_and_b64 s[8:9], s[36:37], exec
	s_mul_i32 s8, s93, 24
	s_cselect_b32 s30, s17, s14
	s_add_i32 s14, s8, s17
	s_cmp_gt_i32 s14, 0x107ff
	s_cselect_b64 s[28:29], -1, 0
	s_and_b64 s[8:9], s[28:29], exec
	s_cselect_b32 s16, s17, s14
	v_mad_i64_i32 v[48:49], s[8:9], s30, v234, v[42:43]
	v_mad_i64_i32 v[46:47], s[8:9], s16, v234, v[42:43]
	global_load_dwordx4 v[38:41], v[50:51], off
	global_load_dwordx4 v[34:37], v[50:51], off offset:32
	global_load_dwordx4 v[30:33], v[48:49], off
	global_load_dwordx4 v[26:29], v[48:49], off offset:32
	global_load_dwordx4 v[22:25], v[46:47], off
	global_load_dwordx4 v[18:21], v[46:47], off offset:32
	s_cmpk_lt_u32 s38, 0x2000
	s_cselect_b64 s[14:15], -1, 0
	s_lshr_b32 s8, s38, 6
	s_and_b32 s9, s38, 63
	s_cmpk_gt_u32 s38, 0x1fff
	s_waitcnt vmcnt(7)
	v_lshlrev_b32_e32 v67, 16, v71
	s_waitcnt vmcnt(6)
	v_lshlrev_b32_e32 v56, 16, v72
	v_and_b32_e32 v57, 0xffff0000, v72
	v_and_b32_e32 v63, 0xffff0000, v71
	v_lshlrev_b32_e32 v54, 16, v68
	v_and_b32_e32 v55, 0xffff0000, v68
	v_and_b32_e32 v58, 0xffff0000, v69
	v_lshlrev_b32_e32 v59, 16, v69
	v_and_b32_e32 v60, 0xffff0000, v73
	v_lshlrev_b32_e32 v61, 16, v73
	v_and_b32_e32 v68, 0xffff0000, v70
	v_lshlrev_b32_e32 v69, 16, v70
	v_pk_mul_f32 v[70:71], v[56:57], v[56:57]
	v_lshlrev_b32_e32 v65, 16, v75
	v_and_b32_e32 v62, 0xffff0000, v75
	v_and_b32_e32 v72, 0xffff0000, v74
	v_lshlrev_b32_e32 v73, 16, v74
	v_pk_mul_f32 v[74:75], v[60:61], v[60:61]
	v_pk_fma_f32 v[70:71], v[54:55], v[54:55], v[70:71]
	v_pk_fma_f32 v[74:75], v[58:59], v[58:59], v[74:75]
	v_add_f32_e32 v5, v70, v71
	v_pk_mul_f32 v[76:77], v[72:73], v[72:73]
	v_add_f32_e32 v5, v75, v5
	v_mov_b32_e32 v64, v62
	v_pk_fma_f32 v[76:77], v[68:69], v[68:69], v[76:77]
	v_add_f32_e32 v5, v74, v5
	v_mov_b32_e32 v66, v63
	v_pk_mul_f32 v[78:79], v[64:65], v[64:65]
	v_add_f32_e32 v5, v77, v5
	v_pk_fma_f32 v[78:79], v[66:67], v[66:67], v[78:79]
	v_add_f32_e32 v5, v76, v5
	v_add_f32_e32 v5, v79, v5
	v_add_f32_e32 v5, v78, v5
	s_waitcnt lgkmcnt(0)
	ds_bpermute_b32 v9, v88, v5
	v_mov_b32_e32 v64, s9
	v_mov_b32_e32 v66, s8
	v_cndmask_b32_e64 v64, v64, v66, s[6:7]
	v_lshl_or_b32 v194, v64, 4, v1
	s_waitcnt lgkmcnt(0)
	v_add_f32_e32 v5, v5, v9
	s_nop 1
	v_mov_b32_dpp v9, v5 quad_perm:[2,3,0,1] row_mask:0xf bank_mask:0xf
	v_mov_b32_e32 v75, 0
	v_mov_b32_e32 v74, 1.0
	v_mov_b32_e32 v70, 1.0
	v_mov_b32_e32 v71, 0
	s_cbranch_scc1 .LBB0_813
	v_lshl_add_u64 v[70:71], v[194:195], 3, s[22:23]
	global_load_dwordx2 v[70:71], v[70:71], off

; __device__ __forceinline__ float bf_lo(unsigned w) { return __uint_as_float(w << 16); }
; __device__ __forceinline__ float bf_hi(unsigned w) { return __uint_as_float(w & 0xffff0000u); }
; __device__ __forceinline__ void even_qk_phase(Frame& F, KArgs a, int j) {
;     ...
;         for (int k = 0; k < RB; ++k) {
;             const int t = tt[k]; const bool lat = t < SEQ; const int pos = (q4 >> 1) ? (t & 63) : (t >> 6);
;             float x1[8], x2[8];
; #pragma unroll
;             for (int i = 0; i < 4; ++i) { x1[2 * i] = bf_lo(w1[k][i]); x1[2 * i + 1] = bf_hi(w1[k][i]); x2[2 * i] = bf_lo(w2[k][i]); x2[2 * i + 1] = bf_hi(w2[k][i]); }
;             float ss = 0.f;
; #pragma unroll
;             for (int i = 0; i < 8; ++i) ss += x1[i] * x1[i] + x2[i] * x2[i];
;             ss += __shfl_xor(ss, 1); ss += __shfl_xor(ss, 2);
;             const float rstd = rsqrtf(ss * (1.f / 64.f) + EPS);
;             float o1[8], o2[8];
; #pragma unroll
;             for (int i = 0; i < 8; ++i) {
;                 const float a1 = x1[i] * rstd * g1[i], a2 = x2[i] * rstd * g2[i];
;                 float c = 1.f, s_ = 0.f;
;                 if (lat) { const f32x2 cs = R64[pos * 16 + (q4 & 1) * 8 + i]; c = cs.x; s_ = cs.y; }
.LBB0_829:
	s_or_b64 exec, exec, s[8:9]
	s_waitcnt vmcnt(4)
	v_lshlrev_b32_e32 v54, 16, v34
	v_and_b32_e32 v55, 0xffff0000, v34
	v_lshlrev_b32_e32 v52, 16, v38
	v_and_b32_e32 v53, 0xffff0000, v38
	v_pk_mul_f32 v[62:63], v[54:55], v[54:55]
	v_and_b32_e32 v34, 0xffff0000, v35
	v_lshlrev_b32_e32 v35, 16, v35
	v_pk_fma_f32 v[64:65], v[52:53], v[52:53], v[62:63]
	v_and_b32_e32 v38, 0xffff0000, v39
	v_lshlrev_b32_e32 v39, 16, v39
	v_pk_mul_f32 v[62:63], v[34:35], v[34:35]
	v_lshlrev_b32_e32 v61, 16, v41
	v_and_b32_e32 v57, 0xffff0000, v41
	v_pk_fma_f32 v[66:67], v[38:39], v[38:39], v[62:63]
	v_and_b32_e32 v62, 0xffff0000, v40
	v_lshlrev_b32_e32 v63, 16, v40
	v_and_b32_e32 v40, 0xffff0000, v36
	v_lshlrev_b32_e32 v41, 16, v36
	v_add_f32_e32 v5, v64, v65
	v_lshlrev_b32_e32 v59, 16, v37
	v_and_b32_e32 v56, 0xffff0000, v37
	v_pk_mul_f32 v[36:37], v[40:41], v[40:41]
	v_add_f32_e32 v5, v67, v5
	v_pk_fma_f32 v[36:37], v[62:63], v[62:63], v[36:37]
	v_mov_b32_e32 v58, v56
	v_add_f32_e32 v5, v66, v5
	v_mov_b32_e32 v60, v57
	v_pk_mul_f32 v[68:69], v[58:59], v[58:59]
	v_add_f32_e32 v5, v37, v5
	v_pk_fma_f32 v[68:69], v[60:61], v[60:61], v[68:69]
	v_add_f32_e32 v5, v36, v5
	v_add_f32_e32 v5, v69, v5
	v_add_f32_e32 v5, v68, v5
	s_mul_hi_i32 s8, s31, 0x3e0f83e1
	s_waitcnt lgkmcnt(0)
	ds_bpermute_b32 v9, v88, v5
	s_lshr_b32 s9, s8, 31
	s_ashr_i32 s8, s8, 11
	s_add_i32 s8, s8, s9
	s_mulk_i32 s8, 0x2100
	s_sub_i32 s8, s31, s8
	s_cmpk_lt_i32 s8, 0x2000
	s_waitcnt lgkmcnt(0)
	v_add_f32_e32 v5, v5, v9
	s_cselect_b64 s[14:15], -1, 0
	s_ashr_i32 s9, s8, 6
	s_and_b32 s31, s8, 63
	s_nop 1
	v_mov_b32_dpp v9, v5 quad_perm:[2,3,0,1] row_mask:0xf bank_mask:0xf
	v_mov_b32_e32 v36, s31
	v_mov_b32_e32 v37, s9
	v_cndmask_b32_e64 v36, v36, v37, s[6:7]
	s_waitcnt vmcnt(0)
	v_lshl_or_b32 v70, v36, 4, v1
	s_cmpk_gt_i32 s8, 0x1fff
	v_mov_b32_e32 v65, 0
	v_mov_b32_e32 v64, 1.0
	v_ashrrev_i32_e32 v71, 31, v70
	v_mov_b32_e32 v36, 1.0
	v_mov_b32_e32 v37, 0
	s_cbranch_scc1 .LBB0_831
	v_lshl_add_u64 v[36:37], v[70:71], 3, s[22:23]
	global_load_dwordx2 v[36:37], v[36:37], off

; __device__ __forceinline__ float bf_lo(unsigned w) { return __uint_as_float(w << 16); }
; __device__ __forceinline__ float bf_hi(unsigned w) { return __uint_as_float(w & 0xffff0000u); }
; __device__ __forceinline__ void even_qk_phase(Frame& F, KArgs a, int j) {
;     ...
;         for (int k = 0; k < RB; ++k) {
;             const int t = tt[k]; const bool lat = t < SEQ; const int pos = (q4 >> 1) ? (t & 63) : (t >> 6);
;             float x1[8], x2[8];
; #pragma unroll
;             for (int i = 0; i < 4; ++i) { x1[2 * i] = bf_lo(w1[k][i]); x1[2 * i + 1] = bf_hi(w1[k][i]); x2[2 * i] = bf_lo(w2[k][i]); x2[2 * i + 1] = bf_hi(w2[k][i]); }
;             float ss = 0.f;
; #pragma unroll
;             for (int i = 0; i < 8; ++i) ss += x1[i] * x1[i] + x2[i] * x2[i];
;             ss += __shfl_xor(ss, 1); ss += __shfl_xor(ss, 2);
;             const float rstd = rsqrtf(ss * (1.f / 64.f) + EPS);
;             float o1[8], o2[8];
; #pragma unroll
;             for (int i = 0; i < 8; ++i) {
;                 const float a1 = x1[i] * rstd * g1[i], a2 = x2[i] * rstd * g2[i];
;                 float c = 1.f, s_ = 0.f;
;                 if (lat) { const f32x2 cs = R64[pos * 16 + (q4 & 1) * 8 + i]; c = cs.x; s_ = cs.y; }
.LBB0_845:
	s_or_b64 exec, exec, s[8:9]
	s_waitcnt vmcnt(0)
	v_lshlrev_b32_e32 v36, 16, v26
	v_and_b32_e32 v37, 0xffff0000, v26
	v_lshlrev_b32_e32 v34, 16, v30
	v_and_b32_e32 v35, 0xffff0000, v30
	v_pk_mul_f32 v[52:53], v[36:37], v[36:37]
	v_and_b32_e32 v26, 0xffff0000, v27
	v_lshlrev_b32_e32 v27, 16, v27
	v_pk_fma_f32 v[54:55], v[34:35], v[34:35], v[52:53]
	v_and_b32_e32 v30, 0xffff0000, v31
	v_lshlrev_b32_e32 v31, 16, v31
	v_pk_mul_f32 v[52:53], v[26:27], v[26:27]
	v_lshlrev_b32_e32 v51, 16, v33
	v_and_b32_e32 v39, 0xffff0000, v33
	v_pk_fma_f32 v[56:57], v[30:31], v[30:31], v[52:53]
	v_and_b32_e32 v52, 0xffff0000, v32
	v_lshlrev_b32_e32 v53, 16, v32
	v_and_b32_e32 v32, 0xffff0000, v28
	v_lshlrev_b32_e32 v33, 16, v28
	v_add_f32_e32 v5, v54, v55
	v_lshlrev_b32_e32 v41, 16, v29
	v_and_b32_e32 v38, 0xffff0000, v29
	v_pk_mul_f32 v[28:29], v[32:33], v[32:33]
	v_add_f32_e32 v5, v57, v5
	v_pk_fma_f32 v[28:29], v[52:53], v[52:53], v[28:29]
	v_mov_b32_e32 v40, v38
	v_add_f32_e32 v5, v56, v5
	v_mov_b32_e32 v50, v39
	v_pk_mul_f32 v[58:59], v[40:41], v[40:41]
	v_add_f32_e32 v5, v29, v5
	v_pk_fma_f32 v[58:59], v[50:51], v[50:51], v[58:59]
	v_add_f32_e32 v5, v28, v5
	v_add_f32_e32 v5, v59, v5
	v_add_f32_e32 v5, v58, v5
	s_mul_hi_i32 s8, s30, 0x3e0f83e1
	s_waitcnt lgkmcnt(0)
	ds_bpermute_b32 v9, v88, v5
	s_lshr_b32 s9, s8, 31
	s_ashr_i32 s8, s8, 11
	s_add_i32 s8, s8, s9
	s_mulk_i32 s8, 0x2100
	s_sub_i32 s8, s30, s8
	s_cmpk_lt_i32 s8, 0x2000
	s_waitcnt lgkmcnt(0)
	v_add_f32_e32 v5, v5, v9
	s_cselect_b64 s[14:15], -1, 0
	s_ashr_i32 s9, s8, 6
	s_and_b32 s30, s8, 63
	s_nop 1
	v_mov_b32_dpp v9, v5 quad_perm:[2,3,0,1] row_mask:0xf bank_mask:0xf
	v_mov_b32_e32 v28, s30
	v_mov_b32_e32 v29, s9
	v_cndmask_b32_e64 v28, v28, v29, s[6:7]
	v_lshl_or_b32 v60, v28, 4, v1
	s_cmpk_gt_i32 s8, 0x1fff
	v_mov_b32_e32 v55, 0
	v_mov_b32_e32 v54, 1.0
	v_ashrrev_i32_e32 v61, 31, v60
	v_mov_b32_e32 v28, 1.0
	v_mov_b32_e32 v29, 0
	s_cbranch_scc1 .LBB0_847
	v_lshl_add_u64 v[28:29], v[60:61], 3, s[22:23]
	global_load_dwordx2 v[28:29], v[28:29], off

; __device__ __forceinline__ float bf_lo(unsigned w) { return __uint_as_float(w << 16); }
; __device__ __forceinline__ float bf_hi(unsigned w) { return __uint_as_float(w & 0xffff0000u); }
; __device__ __forceinline__ void even_qk_phase(Frame& F, KArgs a, int j) {
;     ...
;         for (int k = 0; k < RB; ++k) {
;             const int t = tt[k]; const bool lat = t < SEQ; const int pos = (q4 >> 1) ? (t & 63) : (t >> 6);
;             float x1[8], x2[8];
; #pragma unroll
;             for (int i = 0; i < 4; ++i) { x1[2 * i] = bf_lo(w1[k][i]); x1[2 * i + 1] = bf_hi(w1[k][i]); x2[2 * i] = bf_lo(w2[k][i]); x2[2 * i + 1] = bf_hi(w2[k][i]); }
;             float ss = 0.f;
; #pragma unroll
;             for (int i = 0; i < 8; ++i) ss += x1[i] * x1[i] + x2[i] * x2[i];
;             ss += __shfl_xor(ss, 1); ss += __shfl_xor(ss, 2);
;             const float rstd = rsqrtf(ss * (1.f / 64.f) + EPS);
;             float o1[8], o2[8];
; #pragma unroll
;             for (int i = 0; i < 8; ++i) {
;                 const float a1 = x1[i] * rstd * g1[i], a2 = x2[i] * rstd * g2[i];
;                 float c = 1.f, s_ = 0.f;
;                 if (lat) { const f32x2 cs = R64[pos * 16 + (q4 & 1) * 8 + i]; c = cs.x; s_ = cs.y; }
.LBB0_861:
	s_or_b64 exec, exec, s[8:9]
	s_waitcnt vmcnt(0)
	v_lshlrev_b32_e32 v28, 16, v18
	v_and_b32_e32 v29, 0xffff0000, v18
	v_lshlrev_b32_e32 v26, 16, v22
	v_and_b32_e32 v27, 0xffff0000, v22
	v_pk_mul_f32 v[36:37], v[28:29], v[28:29]
	v_and_b32_e32 v18, 0xffff0000, v19
	v_lshlrev_b32_e32 v19, 16, v19
	v_pk_fma_f32 v[38:39], v[26:27], v[26:27], v[36:37]
	v_and_b32_e32 v22, 0xffff0000, v23
	v_lshlrev_b32_e32 v23, 16, v23
	v_pk_mul_f32 v[36:37], v[18:19], v[18:19]
	v_lshlrev_b32_e32 v35, 16, v25
	v_and_b32_e32 v31, 0xffff0000, v25
	v_pk_fma_f32 v[40:41], v[22:23], v[22:23], v[36:37]
	v_and_b32_e32 v36, 0xffff0000, v24
	v_lshlrev_b32_e32 v37, 16, v24
	v_and_b32_e32 v24, 0xffff0000, v20
	v_lshlrev_b32_e32 v25, 16, v20
	v_add_f32_e32 v5, v38, v39
	v_lshlrev_b32_e32 v33, 16, v21
	v_and_b32_e32 v30, 0xffff0000, v21
	v_pk_mul_f32 v[20:21], v[24:25], v[24:25]
	v_add_f32_e32 v5, v41, v5
	v_pk_fma_f32 v[20:21], v[36:37], v[36:37], v[20:21]
	v_mov_b32_e32 v32, v30
	v_add_f32_e32 v5, v40, v5
	v_mov_b32_e32 v34, v31
	v_pk_mul_f32 v[48:49], v[32:33], v[32:33]
	v_add_f32_e32 v5, v21, v5
	v_pk_fma_f32 v[48:49], v[34:35], v[34:35], v[48:49]
	v_add_f32_e32 v5, v20, v5
	v_add_f32_e32 v5, v49, v5
	v_add_f32_e32 v5, v48, v5
	s_mul_hi_i32 s8, s16, 0x3e0f83e1
	s_waitcnt lgkmcnt(0)
	ds_bpermute_b32 v9, v88, v5
	s_lshr_b32 s9, s8, 31
	s_ashr_i32 s8, s8, 11
	s_add_i32 s8, s8, s9
	s_mulk_i32 s8, 0x2100
	s_sub_i32 s8, s16, s8
	s_cmpk_lt_i32 s8, 0x2000
	s_waitcnt lgkmcnt(0)
	v_add_f32_e32 v5, v5, v9
	s_cselect_b64 s[14:15], -1, 0
	s_ashr_i32 s9, s8, 6
	s_and_b32 s16, s8, 63
	s_nop 1
	v_mov_b32_dpp v9, v5 quad_perm:[2,3,0,1] row_mask:0xf bank_mask:0xf
	v_mov_b32_e32 v20, s16
	v_mov_b32_e32 v21, s9
	v_cndmask_b32_e64 v20, v20, v21, s[6:7]
	v_lshl_or_b32 v50, v20, 4, v1
	s_cmpk_gt_i32 s8, 0x1fff
	v_mov_b32_e32 v39, 0
	v_mov_b32_e32 v38, 1.0
	v_ashrrev_i32_e32 v51, 31, v50
	v_mov_b32_e32 v20, 1.0
	v_mov_b32_e32 v21, 0
	s_cbranch_scc1 .LBB0_863
	v_lshl_add_u64 v[20:21], v[50:51], 3, s[22:23]
	global_load_dwordx2 v[20:21], v[20:21], off

; __device__ __forceinline__ const float* IN(KArgs a, int i) { return (const float*)a->in[i]; }
; #define a launder(kargs)
; __device__ __forceinline__ float wave_sum(float v) {
; #pragma unroll
;     for (int o = 1; o < 64; o <<= 1) v += __shfl_xor(v, o);
;     return v;
; __device__ __forceinline__ void even_merge_phase(Frame& F, KArgs a, int j, int layer) {
;     ...
;     const float lam_init = 0.8f - 0.6f * expf(-0.3f * (float)layer);
;     const float* lv = IN(a, I_DLAM) + j * 256;
;     const float s01 = wave_sum(lv[F.lane] * lv[64 + F.lane]), s23 = wave_sum(lv[128 + F.lane] * lv[192 + F.lane]);
;     const float lam = expf(s01) - expf(s23) + lam_init;
;     const float* sub = IN(a, I_ASUB) + j * 128;
;     const int lane = F.lane, hd = lane >> 4, sb = lane & 15;
;     float gsub[8];
; #pragma unroll
;     for (int i = 0; i < 8; ++i) gsub[i] = sub[sb * 8 + i] * (1.f - lam_init);
;     constexpr int RB = 4;
;     for (int r0 = F.gw; r0 < NR; r0 += RB * F.NGW) {
;         u32x4 w1[RB], w2[RB]; bool ok[RB]; int rw[RB];
; #pragma unroll
;         for (int k = 0; k < RB; ++k) { int r = r0 + k * F.NGW; ok[k] = r < NR; if (!ok[k]) r = r0; rw[k] = r;
;             const bf16_t* p1 = OB + (size_t)r * 1024 + (hd * 2) * 128 + sb * 8; w1[k] = *(const u32x4*)p1; w2[k] = *(const u32x4*)(p1 + 128); }
.LBB0_1052:
	s_or_b64 exec, exec, s[4:5]
	s_mov_b64 s[10:11], s[0:1]
	v_mov_b32_e32 v1, v202
	s_waitcnt lgkmcnt(0)
	s_barrier
	v_readlane_b32 s12, v255, 37
	v_readfirstlane_b32 s3, v1
	s_ashr_i32 s4, s3, 6
	s_mov_b32 s3, s93
	s_mov_b32 s64, s2
	s_lshl_b32 s2, s2, 3
	s_add_i32 s8, s2, s4
	s_load_dwordx4 s[4:7], s[10:11], 0x50
	v_readlane_b32 s13, v255, 38
	s_lshl_b32 s38, s12, 8
	s_lshl_b64 s[12:13], s[38:39], 2
	v_and_b32_e32 v2, 63, v1
	s_waitcnt lgkmcnt(0)
	s_add_u32 s4, s4, s12
	s_addc_u32 s5, s5, s13
	v_lshlrev_b32_e32 v5, 2, v2
	global_load_dword v3, v5, s[4:5]
	global_load_dword v4, v5, s[4:5] offset:256
	global_load_dword v8, v5, s[4:5] offset:512
	s_nop 0
	global_load_dword v5, v5, s[4:5] offset:768
	v_cmp_lt_i32_e32 vcc, v233, v227
	s_cmp_gt_i32 s8, 0x107ff
	v_readlane_b32 s4, v255, 33
	v_cndmask_b32_e32 v7, v225, v233, vcc
	v_lshlrev_b32_e32 v42, 2, v7
	s_waitcnt vmcnt(2)
	v_mul_f32_e32 v6, v3, v4
	ds_bpermute_b32 v6, v42, v6
	s_waitcnt vmcnt(0)
	v_mul_f32_e32 v9, v8, v5
	ds_bpermute_b32 v9, v42, v9
	s_waitcnt lgkmcnt(0)
	v_fmac_f32_e32 v6, v3, v4
	v_xor_b32_e32 v3, 2, v225
	v_cmp_lt_i32_e32 vcc, v3, v227
	v_xor_b32_e32 v4, 4, v225
	s_waitcnt lgkmcnt(0)
	v_fmac_f32_e32 v9, v8, v5
	v_cndmask_b32_e32 v3, v225, v3, vcc
	v_lshlrev_b32_e32 v43, 2, v3
	s_nop 1
	v_mov_b32_dpp v3, v6 quad_perm:[2,3,0,1] row_mask:0xf bank_mask:0xf
	v_cmp_lt_i32_e32 vcc, v4, v227
	s_nop 1
	v_mov_b32_dpp v5, v9 quad_perm:[2,3,0,1] row_mask:0xf bank_mask:0xf
	s_waitcnt lgkmcnt(0)
	v_add_f32_e32 v3, v6, v3
	v_cndmask_b32_e32 v4, v225, v4, vcc
	v_lshlrev_b32_e32 v44, 2, v4
	s_nop 1
	v_mov_b32_dpp v4, v3 row_shl:4 row_mask:0xf bank_mask:0x5
	v_mov_b32_dpp v4, v3 row_shr:4 row_mask:0xf bank_mask:0xa
	s_waitcnt lgkmcnt(0)
	v_add_f32_e32 v5, v9, v5
	s_nop 1
	v_mov_b32_dpp v8, v5 row_shl:4 row_mask:0xf bank_mask:0x5
	v_mov_b32_dpp v8, v5 row_shr:4 row_mask:0xf bank_mask:0xa
	s_waitcnt lgkmcnt(0)
	v_add_f32_e32 v3, v3, v4
	v_xor_b32_e32 v4, 8, v225
	v_cmp_lt_i32_e32 vcc, v4, v227
	s_waitcnt lgkmcnt(0)
	v_add_f32_e32 v5, v5, v8
	v_cndmask_b32_e32 v4, v225, v4, vcc
	v_lshlrev_b32_e32 v45, 2, v4
	s_nop 1
	v_mov_b32_dpp v4, v3 row_shl:8 row_mask:0xf bank_mask:0x3
	v_mov_b32_dpp v4, v3 row_shr:8 row_mask:0xf bank_mask:0xc
	s_nop 1
	v_mov_b32_dpp v8, v5 row_shl:8 row_mask:0xf bank_mask:0x3
	v_mov_b32_dpp v8, v5 row_shr:8 row_mask:0xf bank_mask:0xc
	s_waitcnt lgkmcnt(0)
	v_add_f32_e32 v3, v3, v4
	v_xor_b32_e32 v4, 16, v225
	v_cmp_lt_i32_e32 vcc, v4, v227
	s_waitcnt lgkmcnt(0)
	v_add_f32_e32 v5, v5, v8
	v_cndmask_b32_e32 v4, v225, v4, vcc
	v_lshlrev_b32_e32 v6, 2, v4
	ds_bpermute_b32 v4, v6, v3
	ds_bpermute_b32 v6, v6, v5
	s_waitcnt lgkmcnt(0)
	v_add_f32_e32 v3, v3, v4
	v_xor_b32_e32 v4, 32, v225
	v_cmp_lt_i32_e32 vcc, v4, v227
	s_waitcnt lgkmcnt(0)
	v_add_f32_e32 v5, v5, v6
	v_cndmask_b32_e32 v4, v225, v4, vcc
	v_lshlrev_b32_e32 v7, 2, v4
	ds_bpermute_b32 v4, v7, v3
	ds_bpermute_b32 v6, v7, v5
	s_cbranch_scc1 .LBB0_1061
	v_cvt_f32_u32_e32 v7, s4
	s_mov_b32 s9, 0x3fb8aa3b
	s_mov_b32 s12, 0xc2ce8ed0
	s_mov_b32 s13, 0x42b17218
	v_mul_f32_e32 v7, 0xbe99999a, v7
	v_mul_f32_e32 v8, 0x3fb8aa3b, v7
	v_fma_f32 v9, v7, s9, -v8
	v_rndne_f32_e32 v10, v8
	v_fmac_f32_e32 v9, 0x32a5705f, v7
	v_sub_f32_e32 v8, v8, v10
	v_add_f32_e32 v8, v8, v9
	v_exp_f32_e32 v8, v8
	v_cvt_i32_f32_e32 v9, v10
	v_cmp_ngt_f32_e32 vcc, s12, v7
	v_mov_b32_e32 v18, 0x7f800000
	s_lshl_b32 s2, s3, 3
	v_ldexp_f32 v8, v8, v9
	v_cndmask_b32_e32 v8, 0, v8, vcc
	v_cmp_nlt_f32_e32 vcc, s13, v7
	s_lshl_b64 s[4:5], s[20:21], 2
	s_add_u32 s4, s6, s4
	v_cndmask_b32_e32 v7, v18, v8, vcc
	v_mov_b32_e32 v8, 0x3f4ccccd
	v_fmamk_f32 v7, v7, 0xbf19999a, v8
	v_lshlrev_b32_e32 v8, 3, v2
	v_and_b32_e32 v17, 0x78, v8
	s_addc_u32 s5, s7, s5
	v_lshlrev_b32_e32 v12, 2, v17
	global_load_dwordx4 v[8:11], v12, s[4:5] offset:16
	s_nop 0
	global_load_dwordx4 v[12:15], v12, s[4:5]
	s_waitcnt lgkmcnt(0)
	v_add_f32_e32 v3, v3, v4
	v_sub_f32_e32 v16, 1.0, v7
	v_mul_f32_e32 v4, 0x3fb8aa3b, v3
	v_cmp_ngt_f32_e32 vcc, s12, v3
	s_load_dwordx2 s[4:5], s[10:11], 0xd0
	v_lshrrev_b32_e32 v2, 4, v2
	v_lshlrev_b32_e32 v194, 8, v2
	v_lshlrev_b32_e32 v2, 9, v2
	s_mov_b64 s[6:7], 0x258b2300
	s_lshl_b32 s14, s3, 4
	s_waitcnt vmcnt(1)
	v_pk_mul_f32 v[30:31], v[16:17], v[8:9] op_sel_hi:[0,1]
	v_fma_f32 v8, v3, s9, -v4
	v_rndne_f32_e32 v9, v4
	v_fmac_f32_e32 v8, 0x32a5705f, v3
	v_sub_f32_e32 v4, v4, v9
	v_add_f32_e32 v4, v4, v8
	v_exp_f32_e32 v4, v4
	v_cvt_i32_f32_e32 v8, v9
	s_waitcnt vmcnt(0)
	v_pk_mul_f32 v[26:27], v[16:17], v[12:13] op_sel_hi:[0,1]
	v_pk_mul_f32 v[28:29], v[16:17], v[14:15] op_sel_hi:[0,1]
	v_pk_mul_f32 v[32:33], v[16:17], v[10:11] op_sel_hi:[0,1]
	v_ldexp_f32 v4, v4, v8
	v_cndmask_b32_e32 v4, 0, v4, vcc
	v_cmp_nlt_f32_e32 vcc, s13, v3
	s_nop 1
	v_cndmask_b32_e32 v3, v18, v4, vcc
	s_waitcnt lgkmcnt(0)
	v_add_f32_e32 v4, v5, v6
	v_mul_f32_e32 v5, 0x3fb8aa3b, v4
	v_fma_f32 v6, v4, s9, -v5
	v_rndne_f32_e32 v8, v5
	v_fmac_f32_e32 v6, 0x32a5705f, v4
	v_sub_f32_e32 v5, v5, v8
	v_add_f32_e32 v5, v5, v6
	v_exp_f32_e32 v5, v5
	v_cvt_i32_f32_e32 v6, v8
	v_cmp_ngt_f32_e32 vcc, s12, v4
	v_ldexp_f32 v5, v5, v6
	s_nop 0
	v_cndmask_b32_e32 v5, 0, v5, vcc
	v_cmp_nlt_f32_e32 vcc, s13, v4
	s_nop 1
	v_cndmask_b32_e32 v4, v18, v5, vcc
	v_sub_f32_e32 v3, v3, v4
	v_add_f32_e32 v34, v7, v3
	v_mov_b32_e32 v3, v195
	v_lshl_add_u64 v[2:3], s[4:5], 0, v[2:3]
	v_lshlrev_b32_e32 v4, 1, v17
	v_mov_b32_e32 v5, v195
	v_lshl_add_u64 v[2:3], v[2:3], 0, v[4:5]
	v_lshl_add_u64 v[36:37], v[2:3], 0, s[6:7]
	v_lshl_add_u64 v[2:3], s[4:5], 0, v[194:195]
	v_lshl_add_u64 v[2:3], v[2:3], 0, v[4:5]
	s_mov_b64 s[4:5], 0x81ee300
	v_lshl_add_u64 v[38:39], v[2:3], 0, s[4:5]
	v_mov_b32_e32 v35, v34
	s_branch .LBB0_1055

; __device__ __forceinline__ unsigned cvtpk(float lo, float hi) { f32x2 v = {lo, hi}; bf16x2_t b = __builtin_convertvector(v, bf16x2_t); return __builtin_bit_cast(unsigned, b); }
; __device__ __forceinline__ float bf_lo(unsigned w) { return __uint_as_float(w << 16); }
; __device__ __forceinline__ float bf_hi(unsigned w) { return __uint_as_float(w & 0xffff0000u); }
; __device__ __forceinline__ void even_merge_phase(Frame& F, KArgs a, int j, int layer) {
;     ...
;     for (int r0 = F.gw; r0 < NR; r0 += RB * F.NGW) {
;         u32x4 w1[RB], w2[RB]; bool ok[RB]; int rw[RB];
; #pragma unroll
;         for (int k = 0; k < RB; ++k) { int r = r0 + k * F.NGW; ok[k] = r < NR; if (!ok[k]) r = r0; rw[k] = r;
;             const bf16_t* p1 = OB + (size_t)r * 1024 + (hd * 2) * 128 + sb * 8; w1[k] = *(const u32x4*)p1; w2[k] = *(const u32x4*)(p1 + 128); }
; #pragma unroll
;         for (int k = 0; k < RB; ++k) {
;             float v[8]; float ss = 0.f;
; #pragma unroll
;             for (int i = 0; i < 4; ++i) { v[2 * i] = bf_lo(w1[k][i]) - lam * bf_lo(w2[k][i]); v[2 * i + 1] = bf_hi(w1[k][i]) - lam * bf_hi(w2[k][i]); }
; #pragma unroll
;             for (int i = 0; i < 8; ++i) ss += v[i] * v[i];
;             ss += __shfl_xor(ss, 1); ss += __shfl_xor(ss, 2); ss += __shfl_xor(ss, 4); ss += __shfl_xor(ss, 8);
;             const float rstd = rsqrtf(ss * (1.f / 128.f) + EPS);
;             u32x4 u;
; #pragma unroll
;             for (int i = 0; i < 4; ++i) u[i] = cvtpk(v[2 * i] * rstd * gsub[2 * i], v[2 * i + 1] * rstd * gsub[2 * i + 1]);
;             if (ok[k]) *(u32x4*)(H + (size_t)rw[k] * 1024 + hd * 128 + sb * 8) = u;
.LBB0_1055:
	s_ashr_i32 s9, s8, 31
	s_lshl_b64 s[20:21], s[8:9], 11
	v_lshl_add_u64 v[2:3], v[36:37], 0, s[20:21]
	global_load_dwordx4 v[46:49], v[2:3], off
	global_load_dwordx4 v[50:53], v[2:3], off offset:256
	s_add_i32 s9, s8, s2
	s_cmp_lt_i32 s9, 0x10800
	s_cselect_b32 s4, s9, s8
	s_ashr_i32 s5, s4, 31
	s_lshl_b64 s[18:19], s[4:5], 11
	v_lshl_add_u64 v[2:3], v[36:37], 0, s[18:19]
	global_load_dwordx4 v[22:25], v[2:3], off
	global_load_dwordx4 v[18:21], v[2:3], off offset:256
	s_add_i32 s6, s14, s8
	s_cmp_lt_i32 s6, 0x10800
	s_cselect_b64 s[12:13], -1, 0
	s_and_b64 s[4:5], s[12:13], exec
	s_cselect_b32 s4, s6, s8
	s_ashr_i32 s5, s4, 31
	s_lshl_b64 s[10:11], s[4:5], 11
	s_mul_i32 s4, s3, 24
	s_add_i32 s15, s4, s8
	s_cmp_lt_i32 s15, 0x10800
	s_cselect_b64 s[6:7], -1, 0
	s_and_b64 s[4:5], s[6:7], exec
	s_cselect_b32 s4, s15, s8
	s_ashr_i32 s5, s4, 31
	s_lshl_b64 s[4:5], s[4:5], 11
	v_lshl_add_u64 v[2:3], v[36:37], 0, s[10:11]
	global_load_dwordx4 v[14:17], v[2:3], off
	global_load_dwordx4 v[10:13], v[2:3], off offset:256
	v_lshl_add_u64 v[2:3], v[36:37], 0, s[4:5]
	s_waitcnt lgkmcnt(0)
	global_load_dwordx4 v[6:9], v[2:3], off
	s_nop 0
	global_load_dwordx4 v[2:5], v[2:3], off offset:256
	s_cmp_gt_i32 s9, 0x107ff
	s_waitcnt vmcnt(7)
	v_lshlrev_b32_e32 v40, 16, v49
	v_and_b32_e32 v41, 0xffff0000, v49
	v_lshlrev_b32_e32 v56, 16, v48
	v_and_b32_e32 v57, 0xffff0000, v48
	s_waitcnt vmcnt(6)
	v_lshlrev_b32_e32 v48, 16, v52
	v_and_b32_e32 v49, 0xffff0000, v52
	v_pk_fma_f32 v[48:49], v[34:35], v[48:49], v[56:57] neg_lo:[1,0,0] neg_hi:[1,0,0]
	v_lshlrev_b32_e32 v56, 16, v47
	v_and_b32_e32 v57, 0xffff0000, v47
	v_lshlrev_b32_e32 v60, 16, v46
	v_and_b32_e32 v61, 0xffff0000, v46
	v_lshlrev_b32_e32 v46, 16, v50
	v_and_b32_e32 v47, 0xffff0000, v50
	v_lshlrev_b32_e32 v58, 16, v51
	v_and_b32_e32 v59, 0xffff0000, v51
	v_pk_fma_f32 v[46:47], v[34:35], v[46:47], v[60:61] neg_lo:[1,0,0] neg_hi:[1,0,0]
	v_pk_fma_f32 v[56:57], v[34:35], v[58:59], v[56:57] neg_lo:[1,0,0] neg_hi:[1,0,0]
	v_pk_mul_f32 v[50:51], v[46:47], v[46:47]
	v_pk_mul_f32 v[58:59], v[56:57], v[56:57]
	v_add_f32_e32 v50, v50, v51
	v_add_f32_e32 v50, v58, v50
	v_lshlrev_b32_e32 v54, 16, v53
	v_and_b32_e32 v55, 0xffff0000, v53
	v_pk_mul_f32 v[52:53], v[48:49], v[48:49]
	v_add_f32_e32 v50, v59, v50
	v_pk_fma_f32 v[40:41], v[34:35], v[54:55], v[40:41] neg_lo:[1,0,0] neg_hi:[1,0,0]
	v_add_f32_e32 v50, v52, v50
	v_pk_mul_f32 v[54:55], v[40:41], v[40:41]
	v_add_f32_e32 v50, v53, v50
	v_add_f32_e32 v50, v54, v50
	v_add_f32_e32 v50, v55, v50
	ds_bpermute_b32 v51, v42, v50
	s_waitcnt lgkmcnt(0)
	v_add_f32_e32 v50, v50, v51
	s_nop 1
	v_mov_b32_dpp v51, v50 quad_perm:[2,3,0,1] row_mask:0xf bank_mask:0xf
	s_waitcnt lgkmcnt(0)
	v_add_f32_e32 v50, v50, v51
	s_nop 1
	v_mov_b32_dpp v51, v50 row_shl:4 row_mask:0xf bank_mask:0x5
	v_mov_b32_dpp v51, v50 row_shr:4 row_mask:0xf bank_mask:0xa
	s_waitcnt lgkmcnt(0)
	v_add_f32_e32 v50, v50, v51
	s_nop 1
	v_mov_b32_dpp v51, v50 row_shl:8 row_mask:0xf bank_mask:0x3
	v_mov_b32_dpp v51, v50 row_shr:8 row_mask:0xf bank_mask:0xc
	s_waitcnt lgkmcnt(0)
	v_add_f32_e32 v50, v50, v51
	v_fmamk_f32 v50, v50, 0x3c000000, v196
	v_cmp_gt_f32_e32 vcc, s95, v50
	v_mul_f32_e32 v51, 0x4b800000, v50
	s_nop 0
	v_cndmask_b32_e32 v50, v50, v51, vcc
	v_rsq_f32_e32 v50, v50
	s_nop 0
	v_mul_f32_e32 v51, 0x45800000, v50
	v_cndmask_b32_e32 v50, v50, v51, vcc
	v_pk_mul_f32 v[46:47], v[46:47], v[50:51] op_sel_hi:[1,0]
	v_pk_mul_f32 v[52:53], v[56:57], v[50:51] op_sel_hi:[1,0]
	v_pk_mul_f32 v[48:49], v[48:49], v[50:51] op_sel_hi:[1,0]
	v_pk_mul_f32 v[40:41], v[40:41], v[50:51] op_sel_hi:[1,0]
	v_pk_mul_f32 v[46:47], v[26:27], v[46:47]
	v_pk_mul_f32 v[52:53], v[28:29], v[52:53]
	v_pk_mul_f32 v[48:49], v[30:31], v[48:49]
	v_pk_mul_f32 v[40:41], v[32:33], v[40:41]
	v_cvt_pk_bf16_f32 v46, v46, v47
	v_cvt_pk_bf16_f32 v47, v52, v53
	v_cvt_pk_bf16_f32 v48, v48, v49
	v_cvt_pk_bf16_f32 v49, v40, v41
	v_lshl_add_u64 v[40:41], v[38:39], 0, s[20:21]
	global_store_dwordx4 v[40:41], v[46:49], off
	s_waitcnt vmcnt(6)
	v_lshlrev_b32_e32 v40, 16, v22
	v_and_b32_e32 v41, 0xffff0000, v22
	s_waitcnt vmcnt(5)
	v_lshlrev_b32_e32 v46, 16, v18
	v_and_b32_e32 v47, 0xffff0000, v18
	v_lshlrev_b32_e32 v22, 16, v23
	v_and_b32_e32 v23, 0xffff0000, v23
	v_lshlrev_b32_e32 v18, 16, v19
	v_and_b32_e32 v19, 0xffff0000, v19
	v_pk_fma_f32 v[40:41], v[34:35], v[46:47], v[40:41] neg_lo:[1,0,0] neg_hi:[1,0,0]
	v_pk_fma_f32 v[18:19], v[34:35], v[18:19], v[22:23] neg_lo:[1,0,0] neg_hi:[1,0,0]
	v_lshlrev_b32_e32 v22, 16, v24
	v_and_b32_e32 v23, 0xffff0000, v24
	v_lshlrev_b32_e32 v46, 16, v20
	v_and_b32_e32 v47, 0xffff0000, v20
	v_lshlrev_b32_e32 v24, 16, v25
	v_and_b32_e32 v25, 0xffff0000, v25
	v_lshlrev_b32_e32 v20, 16, v21
	v_and_b32_e32 v21, 0xffff0000, v21
	v_pk_fma_f32 v[20:21], v[34:35], v[20:21], v[24:25] neg_lo:[1,0,0] neg_hi:[1,0,0]
	v_pk_mul_f32 v[24:25], v[40:41], v[40:41]
	v_pk_fma_f32 v[22:23], v[34:35], v[46:47], v[22:23] neg_lo:[1,0,0] neg_hi:[1,0,0]
	v_pk_mul_f32 v[46:47], v[18:19], v[18:19]
	v_add_f32_e32 v24, v24, v25
	v_add_f32_e32 v24, v46, v24
	v_pk_mul_f32 v[48:49], v[22:23], v[22:23]
	v_add_f32_e32 v24, v47, v24
	v_add_f32_e32 v24, v48, v24
	v_pk_mul_f32 v[50:51], v[20:21], v[20:21]
	v_add_f32_e32 v24, v49, v24
	v_add_f32_e32 v24, v50, v24
	v_add_f32_e32 v24, v51, v24
	ds_bpermute_b32 v25, v42, v24
	s_waitcnt lgkmcnt(0)
	v_add_f32_e32 v24, v24, v25
	s_nop 1
	v_mov_b32_dpp v25, v24 quad_perm:[2,3,0,1] row_mask:0xf bank_mask:0xf
	s_waitcnt lgkmcnt(0)
	v_add_f32_e32 v24, v24, v25
	s_nop 1
	v_mov_b32_dpp v25, v24 row_shl:4 row_mask:0xf bank_mask:0x5
	v_mov_b32_dpp v25, v24 row_shr:4 row_mask:0xf bank_mask:0xa
	s_waitcnt lgkmcnt(0)
	v_add_f32_e32 v24, v24, v25
	s_nop 1
	v_mov_b32_dpp v25, v24 row_shl:8 row_mask:0xf bank_mask:0x3
	v_mov_b32_dpp v25, v24 row_shr:8 row_mask:0xf bank_mask:0xc
	s_cbranch_scc1 .LBB0_1057
	s_waitcnt lgkmcnt(0)
	v_add_f32_e32 v24, v24, v25
	v_fmamk_f32 v24, v24, 0x3c000000, v196
	v_mul_f32_e32 v25, 0x4b800000, v24
	v_cmp_gt_f32_e32 vcc, s95, v24
	s_nop 1
	v_cndmask_b32_e32 v24, v24, v25, vcc
	v_rsq_f32_e32 v24, v24
	s_nop 0
	v_mul_f32_e32 v25, 0x45800000, v24
	v_cndmask_b32_e32 v24, v24, v25, vcc
	v_pk_mul_f32 v[18:19], v[18:19], v[24:25] op_sel_hi:[1,0]
	v_pk_mul_f32 v[40:41], v[40:41], v[24:25] op_sel_hi:[1,0]
	v_pk_mul_f32 v[18:19], v[28:29], v[18:19]
	v_pk_mul_f32 v[40:41], v[26:27], v[40:41]
	v_cvt_pk_bf16_f32 v47, v18, v19
	v_pk_mul_f32 v[18:19], v[22:23], v[24:25] op_sel_hi:[1,0]
	v_cvt_pk_bf16_f32 v46, v40, v41
	v_pk_mul_f32 v[18:19], v[30:31], v[18:19]
	s_nop 0
	v_cvt_pk_bf16_f32 v48, v18, v19
	v_pk_mul_f32 v[18:19], v[20:21], v[24:25] op_sel_hi:[1,0]
	s_nop 0
	v_pk_mul_f32 v[18:19], v[32:33], v[18:19]
	s_nop 0
	v_cvt_pk_bf16_f32 v49, v18, v19
	v_lshl_add_u64 v[18:19], v[38:39], 0, s[18:19]
	global_store_dwordx4 v[18:19], v[46:49], off
; __device__ __forceinline__ unsigned cvtpk(float lo, float hi) { f32x2 v = {lo, hi}; bf16x2_t b = __builtin_convertvector(v, bf16x2_t); return __builtin_bit_cast(unsigned, b); }
; __device__ __forceinline__ float bf_lo(unsigned w) { return __uint_as_float(w << 16); }
; __device__ __forceinline__ float bf_hi(unsigned w) { return __uint_as_float(w & 0xffff0000u); }
; __device__ __forceinline__ void even_merge_phase(Frame& F, KArgs a, int j, int layer) {
;     ...
;         for (int k = 0; k < RB; ++k) {
;             float v[8]; float ss = 0.f;
; #pragma unroll
;             for (int i = 0; i < 4; ++i) { v[2 * i] = bf_lo(w1[k][i]) - lam * bf_lo(w2[k][i]); v[2 * i + 1] = bf_hi(w1[k][i]) - lam * bf_hi(w2[k][i]); }
; #pragma unroll
;             for (int i = 0; i < 8; ++i) ss += v[i] * v[i];
;             ss += __shfl_xor(ss, 1); ss += __shfl_xor(ss, 2); ss += __shfl_xor(ss, 4); ss += __shfl_xor(ss, 8);
;             const float rstd = rsqrtf(ss * (1.f / 128.f) + EPS);
;             u32x4 u;
; #pragma unroll
;             for (int i = 0; i < 4; ++i) u[i] = cvtpk(v[2 * i] * rstd * gsub[2 * i], v[2 * i + 1] * rstd * gsub[2 * i + 1]);
;             if (ok[k]) *(u32x4*)(H + (size_t)rw[k] * 1024 + hd * 128 + sb * 8) = u;
.LBB0_1057:
	s_waitcnt vmcnt(4)
	v_lshlrev_b32_e32 v18, 16, v14
	v_and_b32_e32 v19, 0xffff0000, v14
	s_waitcnt vmcnt(3)
	v_lshlrev_b32_e32 v20, 16, v10
	v_and_b32_e32 v21, 0xffff0000, v10
	v_lshlrev_b32_e32 v14, 16, v15
	v_and_b32_e32 v15, 0xffff0000, v15
	v_lshlrev_b32_e32 v10, 16, v11
	v_and_b32_e32 v11, 0xffff0000, v11
	v_pk_fma_f32 v[18:19], v[34:35], v[20:21], v[18:19] neg_lo:[1,0,0] neg_hi:[1,0,0]
	v_pk_fma_f32 v[10:11], v[34:35], v[10:11], v[14:15] neg_lo:[1,0,0] neg_hi:[1,0,0]
	v_lshlrev_b32_e32 v14, 16, v16
	v_and_b32_e32 v15, 0xffff0000, v16
	v_lshlrev_b32_e32 v20, 16, v12
	v_and_b32_e32 v21, 0xffff0000, v12
	v_lshlrev_b32_e32 v16, 16, v17
	v_and_b32_e32 v17, 0xffff0000, v17
	v_lshlrev_b32_e32 v12, 16, v13
	v_and_b32_e32 v13, 0xffff0000, v13
	v_pk_fma_f32 v[12:13], v[34:35], v[12:13], v[16:17] neg_lo:[1,0,0] neg_hi:[1,0,0]
	v_pk_mul_f32 v[16:17], v[18:19], v[18:19]
	v_pk_fma_f32 v[14:15], v[34:35], v[20:21], v[14:15] neg_lo:[1,0,0] neg_hi:[1,0,0]
	v_pk_mul_f32 v[20:21], v[10:11], v[10:11]
	v_add_f32_e32 v16, v16, v17
	v_add_f32_e32 v16, v20, v16
	v_pk_mul_f32 v[22:23], v[14:15], v[14:15]
	v_add_f32_e32 v16, v21, v16
	v_add_f32_e32 v16, v22, v16
	s_waitcnt lgkmcnt(0)
	v_pk_mul_f32 v[24:25], v[12:13], v[12:13]
	v_add_f32_e32 v16, v23, v16
	v_add_f32_e32 v16, v24, v16
	v_add_f32_e32 v16, v25, v16
	ds_bpermute_b32 v17, v42, v16
	s_andn2_b64 vcc, exec, s[12:13]
	s_waitcnt lgkmcnt(0)
	v_add_f32_e32 v16, v16, v17
	s_nop 1
	v_mov_b32_dpp v17, v16 quad_perm:[2,3,0,1] row_mask:0xf bank_mask:0xf
	s_waitcnt lgkmcnt(0)
	v_add_f32_e32 v16, v16, v17
	s_nop 1
	v_mov_b32_dpp v17, v16 row_shl:4 row_mask:0xf bank_mask:0x5
	v_mov_b32_dpp v17, v16 row_shr:4 row_mask:0xf bank_mask:0xa
	s_waitcnt lgkmcnt(0)
	v_add_f32_e32 v16, v16, v17
	s_nop 1
	v_mov_b32_dpp v17, v16 row_shl:8 row_mask:0xf bank_mask:0x3
	v_mov_b32_dpp v17, v16 row_shr:8 row_mask:0xf bank_mask:0xc
	s_cbranch_vccnz .LBB0_1059
	s_waitcnt lgkmcnt(0)
	v_add_f32_e32 v16, v16, v17
	v_fmamk_f32 v16, v16, 0x3c000000, v196
	v_mul_f32_e32 v17, 0x4b800000, v16
	v_cmp_gt_f32_e32 vcc, s95, v16
	s_nop 1
	v_cndmask_b32_e32 v16, v16, v17, vcc
	v_rsq_f32_e32 v16, v16
	s_nop 0
	v_mul_f32_e32 v17, 0x45800000, v16
	v_cndmask_b32_e32 v20, v16, v17, vcc
	v_pk_mul_f32 v[16:17], v[18:19], v[20:21] op_sel_hi:[1,0]
	v_pk_mul_f32 v[10:11], v[10:11], v[20:21] op_sel_hi:[1,0]
	v_pk_mul_f32 v[16:17], v[26:27], v[16:17]
	v_pk_mul_f32 v[10:11], v[28:29], v[10:11]
	v_cvt_pk_bf16_f32 v16, v16, v17
	v_cvt_pk_bf16_f32 v17, v10, v11
	v_pk_mul_f32 v[10:11], v[14:15], v[20:21] op_sel_hi:[1,0]
	s_nop 0
	v_pk_mul_f32 v[10:11], v[30:31], v[10:11]
	s_nop 0
	v_cvt_pk_bf16_f32 v18, v10, v11
	v_pk_mul_f32 v[10:11], v[12:13], v[20:21] op_sel_hi:[1,0]
	s_nop 0
	v_pk_mul_f32 v[10:11], v[32:33], v[10:11]
	s_nop 0
	v_cvt_pk_bf16_f32 v19, v10, v11
	v_lshl_add_u64 v[10:11], v[38:39], 0, s[10:11]
	global_store_dwordx4 v[10:11], v[16:19], off
.LBB0_1059:
	s_waitcnt vmcnt(2)
	v_lshlrev_b32_e32 v10, 16, v6
	v_and_b32_e32 v11, 0xffff0000, v6
	s_waitcnt vmcnt(1)
	v_lshlrev_b32_e32 v12, 16, v2
	v_and_b32_e32 v13, 0xffff0000, v2
	v_lshlrev_b32_e32 v6, 16, v7
	v_and_b32_e32 v7, 0xffff0000, v7
	v_lshlrev_b32_e32 v2, 16, v3
	v_and_b32_e32 v3, 0xffff0000, v3
	v_pk_fma_f32 v[10:11], v[34:35], v[12:13], v[10:11] neg_lo:[1,0,0] neg_hi:[1,0,0]
	v_pk_fma_f32 v[2:3], v[34:35], v[2:3], v[6:7] neg_lo:[1,0,0] neg_hi:[1,0,0]
	v_lshlrev_b32_e32 v6, 16, v8
	v_and_b32_e32 v7, 0xffff0000, v8
	v_lshlrev_b32_e32 v12, 16, v4
	v_and_b32_e32 v13, 0xffff0000, v4
	v_lshlrev_b32_e32 v8, 16, v9
	v_and_b32_e32 v9, 0xffff0000, v9
	v_lshlrev_b32_e32 v4, 16, v5
	v_and_b32_e32 v5, 0xffff0000, v5
	v_pk_fma_f32 v[4:5], v[34:35], v[4:5], v[8:9] neg_lo:[1,0,0] neg_hi:[1,0,0]
	v_pk_mul_f32 v[8:9], v[10:11], v[10:11]
	v_pk_fma_f32 v[6:7], v[34:35], v[12:13], v[6:7] neg_lo:[1,0,0] neg_hi:[1,0,0]
	v_pk_mul_f32 v[12:13], v[2:3], v[2:3]
	v_add_f32_e32 v8, v8, v9
	v_add_f32_e32 v8, v12, v8
	v_pk_mul_f32 v[14:15], v[6:7], v[6:7]
	v_add_f32_e32 v8, v13, v8
	v_add_f32_e32 v8, v14, v8
	s_waitcnt lgkmcnt(0)
	v_pk_mul_f32 v[16:17], v[4:5], v[4:5]
	v_add_f32_e32 v8, v15, v8
	v_add_f32_e32 v8, v16, v8
	v_add_f32_e32 v8, v17, v8
	ds_bpermute_b32 v9, v42, v8
	s_andn2_b64 vcc, exec, s[6:7]
	s_waitcnt lgkmcnt(0)
	v_add_f32_e32 v8, v8, v9
	s_nop 1
	v_mov_b32_dpp v9, v8 quad_perm:[2,3,0,1] row_mask:0xf bank_mask:0xf
	s_waitcnt lgkmcnt(0)
	v_add_f32_e32 v8, v8, v9
	s_nop 1
	v_mov_b32_dpp v9, v8 row_shl:4 row_mask:0xf bank_mask:0x5
	v_mov_b32_dpp v9, v8 row_shr:4 row_mask:0xf bank_mask:0xa
	s_waitcnt lgkmcnt(0)
	v_add_f32_e32 v8, v8, v9
	s_nop 1
	v_mov_b32_dpp v9, v8 row_shl:8 row_mask:0xf bank_mask:0x3
	v_mov_b32_dpp v9, v8 row_shr:8 row_mask:0xf bank_mask:0xc
	s_cbranch_vccnz .LBB0_1054
	s_waitcnt lgkmcnt(0)
	v_add_f32_e32 v8, v8, v9
	v_fmamk_f32 v8, v8, 0x3c000000, v196
	v_mul_f32_e32 v9, 0x4b800000, v8
	v_cmp_gt_f32_e32 vcc, s95, v8
	s_nop 1
	v_cndmask_b32_e32 v8, v8, v9, vcc
	v_rsq_f32_e32 v8, v8
	s_nop 0
	v_mul_f32_e32 v9, 0x45800000, v8
	v_cndmask_b32_e32 v12, v8, v9, vcc
	v_pk_mul_f32 v[8:9], v[10:11], v[12:13] op_sel_hi:[1,0]
	v_pk_mul_f32 v[2:3], v[2:3], v[12:13] op_sel_hi:[1,0]
	v_pk_mul_f32 v[8:9], v[26:27], v[8:9]
	v_pk_mul_f32 v[2:3], v[28:29], v[2:3]
	v_cvt_pk_bf16_f32 v8, v8, v9
	v_cvt_pk_bf16_f32 v9, v2, v3
	v_pk_mul_f32 v[2:3], v[6:7], v[12:13] op_sel_hi:[1,0]
	s_nop 0
	v_pk_mul_f32 v[2:3], v[30:31], v[2:3]
	s_nop 0
	v_cvt_pk_bf16_f32 v10, v2, v3
	v_pk_mul_f32 v[2:3], v[4:5], v[12:13] op_sel_hi:[1,0]
	s_nop 0
	v_pk_mul_f32 v[2:3], v[32:33], v[2:3]
	s_nop 0
	v_cvt_pk_bf16_f32 v11, v2, v3
	v_lshl_add_u64 v[2:3], v[38:39], 0, s[4:5]
	global_store_dwordx4 v[2:3], v[8:11], off
	s_branch .LBB0_1054

; __device__ __forceinline__ float* xrow_ptr(float* xl, float* xc, int b, int t) { return (t < SEQ) ? xl + ((size_t)(b * SEQ + t)) * DM : xc + ((size_t)(b * CTXL + (t - SEQ))) * DM; }
; #define xl OUTP(launder(kargs))
; __device__ __forceinline__ void norm2_block(float* xl, float* xc, const float* MOD, const float* gn, const float* WP, bf16_t* H, float* AFF, int L, int row0, int nrows, int lane) {
;     const int r16 = lane & 15, kq = lane >> 4;
;     const int b = row0 / TPS, t0 = row0 - b * TPS; const int s_ = (t0 >= SEQ) ? 8 : b;
;     if (L == 3 && t0 >= SEQ) return;
;     const int rl = (r16 < nrows) ? r16 : r16 - nrows;
;     const float* xr = xrow_ptr(xl, xc, b, t0 + rl) + 4 * kq;
;     const float* wp = WP + s_ * 16384 + (kq * 16 + r16) * 4;
;     f32x4 acc = {0.f, 0.f, 0.f, 0.f}; float sq = 0.f;
;     f32x4 xa[8], wb[8];
; #pragma unroll
;     for (int q = 0; q < 8; ++q) { xa[q] = *(const f32x4*)(xr + 16 * q); wb[q] = *(const f32x4*)(wp + 256 * q); }
; #pragma unroll
;     for (int g = 0; g < 8; ++g) {
;         f32x4 xn[8], wn[8];
;         if (g < 7) {
; #pragma unroll
;             for (int q = 0; q < 8; ++q) { xn[q] = *(const f32x4*)(xr + 16 * (8 * (g + 1) + q)); wn[q] = *(const f32x4*)(wp + 256 * (8 * (g + 1) + q)); } }
; #pragma unroll
;         for (int q = 0; q < 8; ++q) {
;             sq += (xa[q][0] * xa[q][0] + xa[q][1] * xa[q][1]) + (xa[q][2] * xa[q][2] + xa[q][3] * xa[q][3]);
; #pragma unroll
;             for (int i = 0; i < 4; ++i) acc = __builtin_amdgcn_mfma_f32_16x16x4f32(xa[q][i], wb[q][i], acc, 0, 0, 0); }
.LBB0_1191:
	s_add_i32 s20, s18, -7
	s_mul_hi_i32 s19, s20, 0x3e0f83e1
	s_lshr_b32 s21, s19, 31
	s_ashr_i32 s19, s19, 11
	s_add_i32 s21, s19, s21
	s_mul_i32 s26, s21, 0xffffdf00
	s_add_i32 s19, s20, s26
	s_cmpk_gt_i32 s19, 0x1fff
	s_cselect_b64 s[22:23], -1, 0
	s_and_b64 s[24:25], s[36:37], s[22:23]
	s_and_b64 vcc, exec, s[24:25]
	s_cbranch_vccnz .LBB0_1190
	v_add_u32_e32 v3, s18, v159
	v_add3_u32 v2, v3, s26, -7
	v_cmp_lt_i32_e32 vcc, s74, v2
	s_and_saveexec_b64 s[24:25], vcc
	s_xor_b64 s[24:25], exec, s[24:25]
	s_lshl_b32 s27, s21, 13
	v_subrev_u32_e32 v2, s27, v3
	v_add_u32_e32 v2, 0xffffdff9, v2
	s_or_saveexec_b64 s[24:25], s[24:25]
	v_mov_b64_e32 v[4:5], s[6:7]
	s_xor_b64 exec, exec, s[24:25]
	s_lshl_b32 s27, s43, 3
	s_sub_i32 s27, s27, s42
	s_add_i32 s26, s27, s26
	s_add_i32 s26, s26, 0x10800
	v_or_b32_e32 v2, s26, v159
	v_lshl_add_u32 v2, s21, 13, v2
	v_mov_b64_e32 v[4:5], s[8:9]
	s_or_b64 exec, exec, s[24:25]
	s_and_b64 s[22:23], s[22:23], exec
	v_ashrrev_i32_e32 v3, 31, v2
	s_cselect_b32 s24, 8, s21
	v_lshlrev_b64 v[2:3], 12, v[2:3]
	v_lshl_add_u64 v[2:3], v[4:5], 0, v[2:3]
	v_lshlrev_b32_e32 v194, 2, v142
	s_lshl_b32 s22, s24, 14
	v_lshl_add_u64 v[152:153], v[2:3], 0, v[194:195]
	s_ashr_i32 s23, s22, 31
	v_lshl_add_u64 v[154:155], s[22:23], 2, v[144:145]
	global_load_dwordx4 v[122:125], v[152:153], off
	global_load_dwordx4 v[128:131], v[154:155], off
	global_load_dwordx4 v[114:117], v[152:153], off offset:64
	global_load_dwordx4 v[118:121], v[154:155], off offset:1024
	global_load_dwordx4 v[102:105], v[152:153], off offset:128
	global_load_dwordx4 v[106:109], v[154:155], off offset:2048
	global_load_dwordx4 v[86:89], v[152:153], off offset:192
	global_load_dwordx4 v[90:93], v[154:155], off offset:3072
	global_load_dwordx4 v[66:69], v[152:153], off offset:256
	s_movk_i32 s22, 0x1000
	v_add_co_u32_e32 v2, vcc, s22, v154
	s_movk_i32 s22, 0x2000
	s_nop 0
	v_addc_co_u32_e32 v3, vcc, 0, v155, vcc
	v_add_co_u32_e32 v4, vcc, s22, v154
	s_movk_i32 s22, 0x3000
	s_nop 0
	v_addc_co_u32_e32 v5, vcc, 0, v155, vcc
	global_load_dwordx4 v[74:77], v[4:5], off offset:-4096
	global_load_dwordx4 v[50:53], v[152:153], off offset:320
	global_load_dwordx4 v[54:57], v[2:3], off offset:1024
	global_load_dwordx4 v[34:37], v[152:153], off offset:384
	global_load_dwordx4 v[38:41], v[2:3], off offset:2048
	global_load_dwordx4 v[18:21], v[152:153], off offset:448
	global_load_dwordx4 v[22:25], v[2:3], off offset:3072
	global_load_dwordx4 v[98:101], v[152:153], off offset:512
	global_load_dwordx4 v[110:113], v[4:5], off
	global_load_dwordx4 v[82:85], v[152:153], off offset:576
	global_load_dwordx4 v[94:97], v[4:5], off offset:1024
	global_load_dwordx4 v[70:73], v[152:153], off offset:640
	global_load_dwordx4 v[78:81], v[4:5], off offset:2048
	global_load_dwordx4 v[58:61], v[152:153], off offset:704
	global_load_dwordx4 v[62:65], v[4:5], off offset:3072
	global_load_dwordx4 v[42:45], v[152:153], off offset:768
	v_add_co_u32_e32 v6, vcc, s22, v154
	s_movk_i32 s22, 0x6000
	s_nop 0
	v_addc_co_u32_e32 v7, vcc, 0, v155, vcc
	v_add_co_u32_e32 v126, vcc, s80, v154
	s_waitcnt vmcnt(24)
	v_mul_f32_e32 v132, v123, v123
	v_mul_f32_e32 v133, v125, v125
	v_fmac_f32_e32 v132, v122, v122
	v_fmac_f32_e32 v133, v124, v124
	v_add_f32_e32 v136, v132, v133
	s_waitcnt vmcnt(23)
	v_mfma_f32_16x16x4_f32 v[132:135], v122, v128, 0
	s_waitcnt vmcnt(22)
	v_mul_f32_e32 v128, v115, v115
	v_fmac_f32_e32 v128, v114, v114
	v_addc_co_u32_e32 v127, vcc, 0, v155, vcc
	global_load_dwordx4 v[46:49], v[126:127], off offset:-4096
	global_load_dwordx4 v[26:29], v[152:153], off offset:832
	global_load_dwordx4 v[30:33], v[6:7], off offset:1024
	global_load_dwordx4 v[10:13], v[152:153], off offset:896
	global_load_dwordx4 v[14:17], v[6:7], off offset:2048
	global_load_dwordx4 v[2:5], v[152:153], off offset:960
	s_nop 0
	global_load_dwordx4 v[6:9], v[6:7], off offset:3072
	v_mfma_f32_16x16x4_f32 v[132:135], v123, v129, v[132:135]
	v_mul_f32_e32 v129, v117, v117
	v_fmac_f32_e32 v129, v116, v116
	v_add_f32_e32 v128, v128, v129
	v_mfma_f32_16x16x4_f32 v[132:135], v124, v130, v[132:135]
	v_mfma_f32_16x16x4_f32 v[122:125], v125, v131, v[132:135]
	s_waitcnt vmcnt(28)
	v_mfma_f32_16x16x4_f32 v[122:125], v114, v118, v[122:125]
	v_add_f32_e32 v118, v136, v128
	v_mfma_f32_16x16x4_f32 v[122:125], v115, v119, v[122:125]
	s_waitcnt vmcnt(27)
	v_mul_f32_e32 v119, v103, v103
	v_fmac_f32_e32 v119, v102, v102
	v_mfma_f32_16x16x4_f32 v[122:125], v116, v120, v[122:125]
	v_mul_f32_e32 v120, v105, v105
	v_fmac_f32_e32 v120, v104, v104
	v_add_f32_e32 v119, v119, v120
	v_mfma_f32_16x16x4_f32 v[114:117], v117, v121, v[122:125]
	s_waitcnt vmcnt(26)
	v_mfma_f32_16x16x4_f32 v[114:117], v102, v106, v[114:117]
	v_add_f32_e32 v106, v118, v119
	v_mfma_f32_16x16x4_f32 v[114:117], v103, v107, v[114:117]
	s_waitcnt vmcnt(25)
	v_mul_f32_e32 v107, v87, v87
	v_fmac_f32_e32 v107, v86, v86
	v_mfma_f32_16x16x4_f32 v[114:117], v104, v108, v[114:117]
	v_mul_f32_e32 v108, v89, v89
	v_fmac_f32_e32 v108, v88, v88
	v_add_f32_e32 v107, v107, v108
	v_mfma_f32_16x16x4_f32 v[102:105], v105, v109, v[114:117]
	s_waitcnt vmcnt(24)
	v_mfma_f32_16x16x4_f32 v[102:105], v86, v90, v[102:105]
	v_add_f32_e32 v90, v106, v107
	v_mfma_f32_16x16x4_f32 v[102:105], v87, v91, v[102:105]
	s_waitcnt vmcnt(23)
	v_mul_f32_e32 v91, v67, v67
	v_fmac_f32_e32 v91, v66, v66
	v_mfma_f32_16x16x4_f32 v[102:105], v88, v92, v[102:105]
	v_mul_f32_e32 v92, v69, v69
	v_fmac_f32_e32 v92, v68, v68
	v_add_f32_e32 v91, v91, v92
	v_mfma_f32_16x16x4_f32 v[86:89], v89, v93, v[102:105]
	s_waitcnt vmcnt(22)
	v_mfma_f32_16x16x4_f32 v[86:89], v66, v74, v[86:89]
	v_add_f32_e32 v74, v90, v91
	v_mfma_f32_16x16x4_f32 v[86:89], v67, v75, v[86:89]
	s_waitcnt vmcnt(21)
; __device__ __forceinline__ void norm2_block(float* xl, float* xc, const float* MOD, const float* gn, const float* WP, bf16_t* H, float* AFF, int L, int row0, int nrows, int lane) {
;     ...
;     for (int q = 0; q < 8; ++q) { xa[q] = *(const f32x4*)(xr + 16 * q); wb[q] = *(const f32x4*)(wp + 256 * q); }
; #pragma unroll
;     for (int g = 0; g < 8; ++g) {
;         f32x4 xn[8], wn[8];
;         if (g < 7) {
; #pragma unroll
;             for (int q = 0; q < 8; ++q) { xn[q] = *(const f32x4*)(xr + 16 * (8 * (g + 1) + q)); wn[q] = *(const f32x4*)(wp + 256 * (8 * (g + 1) + q)); } }
; #pragma unroll
;         for (int q = 0; q < 8; ++q) {
;             sq += (xa[q][0] * xa[q][0] + xa[q][1] * xa[q][1]) + (xa[q][2] * xa[q][2] + xa[q][3] * xa[q][3]);
; #pragma unroll
;             for (int i = 0; i < 4; ++i) acc = __builtin_amdgcn_mfma_f32_16x16x4f32(xa[q][i], wb[q][i], acc, 0, 0, 0); }
;         if (g < 7) {
; #pragma unroll
;             for (int q = 0; q < 8; ++q) { xa[q] = xn[q]; wb[q] = wn[q]; } }
;     }
	v_mul_f32_e32 v75, v51, v51
	v_fmac_f32_e32 v75, v50, v50
	v_mfma_f32_16x16x4_f32 v[86:89], v68, v76, v[86:89]
	v_mul_f32_e32 v76, v53, v53
	v_fmac_f32_e32 v76, v52, v52
	v_add_f32_e32 v75, v75, v76
	v_mfma_f32_16x16x4_f32 v[66:69], v69, v77, v[86:89]
	s_waitcnt vmcnt(20)
	v_mfma_f32_16x16x4_f32 v[66:69], v50, v54, v[66:69]
	v_add_f32_e32 v54, v74, v75
	v_mfma_f32_16x16x4_f32 v[66:69], v51, v55, v[66:69]
	s_waitcnt vmcnt(19)
	v_mul_f32_e32 v55, v35, v35
	v_fmac_f32_e32 v55, v34, v34
	v_mfma_f32_16x16x4_f32 v[66:69], v52, v56, v[66:69]
	v_mul_f32_e32 v56, v37, v37
	v_fmac_f32_e32 v56, v36, v36
	v_add_f32_e32 v55, v55, v56
	v_mfma_f32_16x16x4_f32 v[50:53], v53, v57, v[66:69]
	global_load_dwordx4 v[134:137], v[152:153], off offset:1024
	global_load_dwordx4 v[138:141], v[126:127], off
	global_load_dwordx4 v[118:121], v[152:153], off offset:1088
	global_load_dwordx4 v[122:125], v[126:127], off offset:1024
	global_load_dwordx4 v[102:105], v[152:153], off offset:1152
	global_load_dwordx4 v[106:109], v[126:127], off offset:2048
	global_load_dwordx4 v[86:89], v[152:153], off offset:1216
	global_load_dwordx4 v[90:93], v[126:127], off offset:3072
	global_load_dwordx4 v[66:69], v[152:153], off offset:1280
	s_waitcnt vmcnt(24)
	v_mul_f32_e32 v126, v99, v99
	v_mul_f32_e32 v127, v101, v101
	v_fmac_f32_e32 v126, v98, v98
	v_fmac_f32_e32 v127, v100, v100
	v_add_f32_e32 v126, v126, v127
	v_mfma_f32_16x16x4_f32 v[50:53], v34, v38, v[50:53]
	v_add_f32_e32 v38, v54, v55
	v_mfma_f32_16x16x4_f32 v[50:53], v35, v39, v[50:53]
	v_mul_f32_e32 v39, v19, v19
	v_fmac_f32_e32 v39, v18, v18
	v_mfma_f32_16x16x4_f32 v[50:53], v36, v40, v[50:53]
	v_mul_f32_e32 v40, v21, v21
	v_fmac_f32_e32 v40, v20, v20
	v_add_f32_e32 v39, v39, v40
	v_add_f32_e32 v128, v38, v39
	v_mfma_f32_16x16x4_f32 v[34:37], v37, v41, v[50:53]
	v_mfma_f32_16x16x4_f32 v[34:37], v18, v22, v[34:37]
	v_add_co_u32_e32 v22, vcc, s77, v154
	v_mfma_f32_16x16x4_f32 v[34:37], v19, v23, v[34:37]
	s_nop 0
	v_addc_co_u32_e32 v23, vcc, 0, v155, vcc
	v_add_co_u32_e32 v156, vcc, s22, v154
	s_movk_i32 s22, 0x7000
	s_nop 0
	v_addc_co_u32_e32 v157, vcc, 0, v155, vcc
	v_mfma_f32_16x16x4_f32 v[34:37], v20, v24, v[34:37]
	v_mfma_f32_16x16x4_f32 v[114:117], v21, v25, v[34:37]
	global_load_dwordx4 v[74:77], v[156:157], off offset:-4096
	global_load_dwordx4 v[50:53], v[152:153], off offset:1344
	global_load_dwordx4 v[54:57], v[22:23], off offset:1024
	s_nop 5
	global_load_dwordx4 v[34:37], v[152:153], off offset:1408
	global_load_dwordx4 v[38:41], v[22:23], off offset:2048
	global_load_dwordx4 v[18:21], v[152:153], off offset:1472
	s_nop 0
	global_load_dwordx4 v[22:25], v[22:23], off offset:3072
	s_waitcnt vmcnt(30)
	v_mfma_f32_16x16x4_f32 v[114:117], v98, v110, v[114:117]
	v_add_f32_e32 v110, v128, v126
	v_mfma_f32_16x16x4_f32 v[114:117], v99, v111, v[114:117]
	s_waitcnt vmcnt(29)
	v_mul_f32_e32 v111, v83, v83
	v_fmac_f32_e32 v111, v82, v82
	v_mfma_f32_16x16x4_f32 v[114:117], v100, v112, v[114:117]
	v_mul_f32_e32 v112, v85, v85
	v_fmac_f32_e32 v112, v84, v84
	v_add_f32_e32 v111, v111, v112
	v_mfma_f32_16x16x4_f32 v[98:101], v101, v113, v[114:117]
	s_waitcnt vmcnt(28)
	v_mfma_f32_16x16x4_f32 v[98:101], v82, v94, v[98:101]
	v_add_f32_e32 v94, v110, v111
	v_mfma_f32_16x16x4_f32 v[98:101], v83, v95, v[98:101]
	s_waitcnt vmcnt(27)
	v_mul_f32_e32 v95, v71, v71
	v_fmac_f32_e32 v95, v70, v70
	v_mfma_f32_16x16x4_f32 v[98:101], v84, v96, v[98:101]
	v_mul_f32_e32 v96, v73, v73
	v_fmac_f32_e32 v96, v72, v72
	v_add_f32_e32 v95, v95, v96
	v_mfma_f32_16x16x4_f32 v[82:85], v85, v97, v[98:101]
	s_waitcnt vmcnt(26)
	v_mfma_f32_16x16x4_f32 v[82:85], v70, v78, v[82:85]
	v_add_f32_e32 v78, v94, v95
	v_mfma_f32_16x16x4_f32 v[82:85], v71, v79, v[82:85]
	s_waitcnt vmcnt(25)
	v_mul_f32_e32 v79, v59, v59
	v_fmac_f32_e32 v79, v58, v58
	v_mfma_f32_16x16x4_f32 v[82:85], v72, v80, v[82:85]
	v_mul_f32_e32 v80, v61, v61
	v_fmac_f32_e32 v80, v60, v60
	v_add_f32_e32 v79, v79, v80
	v_mfma_f32_16x16x4_f32 v[70:73], v73, v81, v[82:85]
	s_waitcnt vmcnt(24)
	v_mfma_f32_16x16x4_f32 v[70:73], v58, v62, v[70:73]
	v_add_f32_e32 v62, v78, v79
	v_mfma_f32_16x16x4_f32 v[70:73], v59, v63, v[70:73]
	s_waitcnt vmcnt(23)
	v_mul_f32_e32 v63, v43, v43
	v_fmac_f32_e32 v63, v42, v42
	v_mfma_f32_16x16x4_f32 v[70:73], v60, v64, v[70:73]
	v_mul_f32_e32 v64, v45, v45
	v_fmac_f32_e32 v64, v44, v44
	v_add_f32_e32 v63, v63, v64
	v_mfma_f32_16x16x4_f32 v[58:61], v61, v65, v[70:73]
	s_waitcnt vmcnt(22)
	v_mfma_f32_16x16x4_f32 v[58:61], v42, v46, v[58:61]
	v_add_f32_e32 v46, v62, v63
	v_mfma_f32_16x16x4_f32 v[58:61], v43, v47, v[58:61]
	s_waitcnt vmcnt(21)
	v_mul_f32_e32 v47, v27, v27
	v_fmac_f32_e32 v47, v26, v26
	v_mfma_f32_16x16x4_f32 v[58:61], v44, v48, v[58:61]
	v_mul_f32_e32 v48, v29, v29
	v_fmac_f32_e32 v48, v28, v28
	v_add_f32_e32 v47, v47, v48
	v_mfma_f32_16x16x4_f32 v[42:45], v45, v49, v[58:61]
	global_load_dwordx4 v[126:129], v[152:153], off offset:1536
	global_load_dwordx4 v[130:133], v[156:157], off
	global_load_dwordx4 v[110:113], v[152:153], off offset:1600
	global_load_dwordx4 v[114:117], v[156:157], off offset:1024
	global_load_dwordx4 v[94:97], v[152:153], off offset:1664
	global_load_dwordx4 v[98:101], v[156:157], off offset:2048
	global_load_dwordx4 v[78:81], v[152:153], off offset:1728
	global_load_dwordx4 v[82:85], v[156:157], off offset:3072
	global_load_dwordx4 v[58:61], v[152:153], off offset:1792
	s_waitcnt vmcnt(29)
	v_mfma_f32_16x16x4_f32 v[42:45], v26, v30, v[42:45]
	v_add_f32_e32 v30, v46, v47
	v_mfma_f32_16x16x4_f32 v[42:45], v27, v31, v[42:45]
	s_waitcnt vmcnt(28)
; __device__ __forceinline__ void norm2_block(float* xl, float* xc, const float* MOD, const float* gn, const float* WP, bf16_t* H, float* AFF, int L, int row0, int nrows, int lane) {
;     ...
;     for (int q = 0; q < 8; ++q) { xa[q] = *(const f32x4*)(xr + 16 * q); wb[q] = *(const f32x4*)(wp + 256 * q); }
; #pragma unroll
;     for (int g = 0; g < 8; ++g) {
;         f32x4 xn[8], wn[8];
;         if (g < 7) {
; #pragma unroll
;             for (int q = 0; q < 8; ++q) { xn[q] = *(const f32x4*)(xr + 16 * (8 * (g + 1) + q)); wn[q] = *(const f32x4*)(wp + 256 * (8 * (g + 1) + q)); } }
; #pragma unroll
;         for (int q = 0; q < 8; ++q) {
;             sq += (xa[q][0] * xa[q][0] + xa[q][1] * xa[q][1]) + (xa[q][2] * xa[q][2] + xa[q][3] * xa[q][3]);
; #pragma unroll
;             for (int i = 0; i < 4; ++i) acc = __builtin_amdgcn_mfma_f32_16x16x4f32(xa[q][i], wb[q][i], acc, 0, 0, 0); }
;         if (g < 7) {
; #pragma unroll
;             for (int q = 0; q < 8; ++q) { xa[q] = xn[q]; wb[q] = wn[q]; } }
;     }
	v_mul_f32_e32 v31, v11, v11
	v_fmac_f32_e32 v31, v10, v10
	v_mfma_f32_16x16x4_f32 v[42:45], v28, v32, v[42:45]
	v_mul_f32_e32 v32, v13, v13
	v_fmac_f32_e32 v32, v12, v12
	v_add_f32_e32 v31, v31, v32
	v_mfma_f32_16x16x4_f32 v[26:29], v29, v33, v[42:45]
	s_waitcnt vmcnt(27)
	v_mfma_f32_16x16x4_f32 v[26:29], v10, v14, v[26:29]
	v_add_f32_e32 v14, v30, v31
	v_mfma_f32_16x16x4_f32 v[26:29], v11, v15, v[26:29]
	s_waitcnt vmcnt(26)
	v_mul_f32_e32 v15, v3, v3
	v_fmac_f32_e32 v15, v2, v2
	v_mfma_f32_16x16x4_f32 v[26:29], v12, v16, v[26:29]
	v_mul_f32_e32 v16, v5, v5
	v_fmac_f32_e32 v16, v4, v4
	v_add_f32_e32 v15, v15, v16
	v_add_f32_e32 v62, v14, v15
	v_mfma_f32_16x16x4_f32 v[10:13], v13, v17, v[26:29]
	s_waitcnt vmcnt(25)
	v_mfma_f32_16x16x4_f32 v[10:13], v2, v6, v[10:13]
	v_mfma_f32_16x16x4_f32 v[10:13], v3, v7, v[10:13]
	v_mfma_f32_16x16x4_f32 v[10:13], v4, v8, v[10:13]
	v_add_co_u32_e32 v4, vcc, s22, v154
	s_mov_b32 s22, 0xb000
	v_mfma_f32_16x16x4_f32 v[10:13], v5, v9, v[10:13]
	v_addc_co_u32_e32 v5, vcc, 0, v155, vcc
	v_add_co_u32_e32 v2, vcc, s81, v154
	s_nop 1
	v_addc_co_u32_e32 v3, vcc, 0, v155, vcc
	s_waitcnt vmcnt(23)
	v_mfma_f32_16x16x4_f32 v[10:13], v134, v138, v[10:13]
	global_load_dwordx4 v[70:73], v[2:3], off offset:-4096
	global_load_dwordx4 v[42:45], v[152:153], off offset:1856
	global_load_dwordx4 v[46:49], v[4:5], off offset:1024
	global_load_dwordx4 v[26:29], v[152:153], off offset:1920
	global_load_dwordx4 v[30:33], v[4:5], off offset:2048
	global_load_dwordx4 v[6:9], v[152:153], off offset:1984
	global_load_dwordx4 v[14:17], v[4:5], off offset:3072
	v_mul_f32_e32 v4, v135, v135
	v_mul_f32_e32 v5, v137, v137
	v_fmac_f32_e32 v4, v134, v134
	v_fmac_f32_e32 v5, v136, v136
	v_add_f32_e32 v4, v4, v5
	v_add_f32_e32 v4, v62, v4
	v_mfma_f32_16x16x4_f32 v[10:13], v135, v139, v[10:13]
	s_waitcnt vmcnt(29)
	v_mul_f32_e32 v5, v119, v119
	v_mul_f32_e32 v62, v121, v121
	v_fmac_f32_e32 v5, v118, v118
	v_fmac_f32_e32 v62, v120, v120
	v_add_f32_e32 v5, v5, v62
	v_add_f32_e32 v4, v4, v5
	s_waitcnt vmcnt(27)
	v_mul_f32_e32 v5, v103, v103
	v_mfma_f32_16x16x4_f32 v[10:13], v136, v140, v[10:13]
	v_mul_f32_e32 v62, v105, v105
	v_fmac_f32_e32 v5, v102, v102
	v_fmac_f32_e32 v62, v104, v104
	v_add_f32_e32 v5, v5, v62
	v_add_f32_e32 v4, v4, v5
	s_waitcnt vmcnt(25)
	v_mul_f32_e32 v5, v87, v87
	v_mul_f32_e32 v62, v89, v89
	v_mfma_f32_16x16x4_f32 v[10:13], v137, v141, v[10:13]
	v_fmac_f32_e32 v5, v86, v86
	v_fmac_f32_e32 v62, v88, v88
	v_add_f32_e32 v5, v5, v62
	v_add_f32_e32 v4, v4, v5
	s_waitcnt vmcnt(23)
	v_mul_f32_e32 v5, v67, v67
	v_mul_f32_e32 v62, v69, v69
	v_fmac_f32_e32 v5, v66, v66
	v_mfma_f32_16x16x4_f32 v[10:13], v118, v122, v[10:13]
	v_fmac_f32_e32 v62, v68, v68
	v_add_f32_e32 v5, v5, v62
	v_add_f32_e32 v4, v4, v5
	s_waitcnt vmcnt(21)
	v_mul_f32_e32 v5, v51, v51
	v_mul_f32_e32 v62, v53, v53
	v_fmac_f32_e32 v5, v50, v50
	v_fmac_f32_e32 v62, v52, v52
	v_mfma_f32_16x16x4_f32 v[10:13], v119, v123, v[10:13]
	v_add_f32_e32 v5, v5, v62
	v_add_f32_e32 v4, v4, v5
	s_waitcnt vmcnt(19)
	v_mul_f32_e32 v5, v35, v35
	v_fmac_f32_e32 v5, v34, v34
	s_waitcnt vmcnt(15)
	v_mul_f32_e32 v138, v129, v129
	v_fmac_f32_e32 v138, v128, v128
	v_mfma_f32_16x16x4_f32 v[10:13], v120, v124, v[10:13]
	v_mfma_f32_16x16x4_f32 v[10:13], v121, v125, v[10:13]
	v_mfma_f32_16x16x4_f32 v[10:13], v102, v106, v[10:13]
	v_mfma_f32_16x16x4_f32 v[10:13], v103, v107, v[10:13]
	v_mfma_f32_16x16x4_f32 v[10:13], v104, v108, v[10:13]
	v_mfma_f32_16x16x4_f32 v[10:13], v105, v109, v[10:13]
	v_mfma_f32_16x16x4_f32 v[10:13], v86, v90, v[10:13]
	v_mfma_f32_16x16x4_f32 v[10:13], v87, v91, v[10:13]
	v_mfma_f32_16x16x4_f32 v[10:13], v88, v92, v[10:13]
	v_mfma_f32_16x16x4_f32 v[10:13], v89, v93, v[10:13]
	v_mfma_f32_16x16x4_f32 v[10:13], v66, v74, v[10:13]
	v_mfma_f32_16x16x4_f32 v[10:13], v67, v75, v[10:13]
	v_mfma_f32_16x16x4_f32 v[10:13], v68, v76, v[10:13]
	v_mfma_f32_16x16x4_f32 v[10:13], v69, v77, v[10:13]
	global_load_dwordx4 v[122:125], v[152:153], off offset:2048
	global_load_dwordx4 v[134:137], v[2:3], off
	global_load_dwordx4 v[106:109], v[152:153], off offset:2112
	global_load_dwordx4 v[118:121], v[2:3], off offset:1024
	global_load_dwordx4 v[90:93], v[152:153], off offset:2176
	global_load_dwordx4 v[102:105], v[2:3], off offset:2048
	global_load_dwordx4 v[74:77], v[152:153], off offset:2240
	global_load_dwordx4 v[86:89], v[2:3], off offset:3072
	global_load_dwordx4 v[62:65], v[152:153], off offset:2304
	v_mfma_f32_16x16x4_f32 v[10:13], v50, v54, v[10:13]
	v_mul_f32_e32 v50, v37, v37
	v_fmac_f32_e32 v50, v36, v36
	v_add_f32_e32 v5, v5, v50
	v_add_f32_e32 v4, v4, v5
	v_mul_f32_e32 v5, v19, v19
	v_fmac_f32_e32 v5, v18, v18
	v_mfma_f32_16x16x4_f32 v[10:13], v51, v55, v[10:13]
	v_mfma_f32_16x16x4_f32 v[10:13], v52, v56, v[10:13]
	v_mfma_f32_16x16x4_f32 v[10:13], v53, v57, v[10:13]
	v_mfma_f32_16x16x4_f32 v[10:13], v34, v38, v[10:13]
	v_mul_f32_e32 v34, v21, v21
	v_fmac_f32_e32 v34, v20, v20
	v_add_f32_e32 v5, v5, v34
	v_mfma_f32_16x16x4_f32 v[10:13], v35, v39, v[10:13]
	v_mfma_f32_16x16x4_f32 v[10:13], v36, v40, v[10:13]
	v_mfma_f32_16x16x4_f32 v[10:13], v37, v41, v[10:13]
	v_mfma_f32_16x16x4_f32 v[10:13], v18, v22, v[10:13]
	v_mfma_f32_16x16x4_f32 v[10:13], v19, v23, v[10:13]
	v_mfma_f32_16x16x4_f32 v[10:13], v20, v24, v[10:13]
	v_add_f32_e32 v24, v4, v5
	v_mfma_f32_16x16x4_f32 v[20:23], v21, v25, v[10:13]
	v_mul_f32_e32 v25, v127, v127
	v_fmac_f32_e32 v25, v126, v126
	v_add_f32_e32 v25, v25, v138
	v_add_f32_e32 v24, v24, v25
	s_waitcnt vmcnt(22)
	v_mul_f32_e32 v25, v111, v111
	v_fmac_f32_e32 v25, v110, v110
	s_waitcnt vmcnt(8)
; __device__ __forceinline__ void norm2_block(float* xl, float* xc, const float* MOD, const float* gn, const float* WP, bf16_t* H, float* AFF, int L, int row0, int nrows, int lane) {
;     ...
;     for (int q = 0; q < 8; ++q) { xa[q] = *(const f32x4*)(xr + 16 * q); wb[q] = *(const f32x4*)(wp + 256 * q); }
; #pragma unroll
;     for (int g = 0; g < 8; ++g) {
;         f32x4 xn[8], wn[8];
;         if (g < 7) {
; #pragma unroll
;             for (int q = 0; q < 8; ++q) { xn[q] = *(const f32x4*)(xr + 16 * (8 * (g + 1) + q)); wn[q] = *(const f32x4*)(wp + 256 * (8 * (g + 1) + q)); } }
; #pragma unroll
;         for (int q = 0; q < 8; ++q) {
;             sq += (xa[q][0] * xa[q][0] + xa[q][1] * xa[q][1]) + (xa[q][2] * xa[q][2] + xa[q][3] * xa[q][3]);
; #pragma unroll
;             for (int i = 0; i < 4; ++i) acc = __builtin_amdgcn_mfma_f32_16x16x4f32(xa[q][i], wb[q][i], acc, 0, 0, 0); }
;         if (g < 7) {
; #pragma unroll
;             for (int q = 0; q < 8; ++q) { xa[q] = xn[q]; wb[q] = wn[q]; } }
;     }
	v_mul_f32_e32 v138, v125, v125
	v_mfma_f32_16x16x4_f32 v[20:23], v126, v130, v[20:23]
	v_mul_f32_e32 v126, v113, v113
	v_fmac_f32_e32 v126, v112, v112
	v_add_f32_e32 v25, v25, v126
	v_fmac_f32_e32 v138, v124, v124
	v_add_co_u32_e32 v10, vcc, s93, v154
	v_add_f32_e32 v24, v24, v25
	v_mfma_f32_16x16x4_f32 v[20:23], v127, v131, v[20:23]
	v_addc_co_u32_e32 v11, vcc, 0, v155, vcc
	v_add_co_u32_e32 v18, vcc, s85, v154
	v_mul_f32_e32 v25, v95, v95
	s_nop 0
	v_addc_co_u32_e32 v19, vcc, 0, v155, vcc
	v_mfma_f32_16x16x4_f32 v[20:23], v128, v132, v[20:23]
	global_load_dwordx4 v[66:69], v[18:19], off offset:-4096
	global_load_dwordx4 v[50:53], v[152:153], off offset:2368
	global_load_dwordx4 v[54:57], v[10:11], off offset:1024
	global_load_dwordx4 v[34:37], v[152:153], off offset:2432
	global_load_dwordx4 v[38:41], v[10:11], off offset:2048
	global_load_dwordx4 v[2:5], v[152:153], off offset:2496
	s_nop 0
	global_load_dwordx4 v[10:13], v[10:11], off offset:3072
	v_fmac_f32_e32 v25, v94, v94
	v_mfma_f32_16x16x4_f32 v[20:23], v129, v133, v[20:23]
	v_mul_f32_e32 v133, v123, v123
	v_fmac_f32_e32 v133, v122, v122
	v_add_f32_e32 v133, v133, v138
	v_mfma_f32_16x16x4_f32 v[20:23], v110, v114, v[20:23]
	v_mul_f32_e32 v110, v97, v97
	v_fmac_f32_e32 v110, v96, v96
	v_add_f32_e32 v25, v25, v110
	v_add_f32_e32 v24, v24, v25
	v_mul_f32_e32 v25, v79, v79
	v_fmac_f32_e32 v25, v78, v78
	v_mfma_f32_16x16x4_f32 v[20:23], v111, v115, v[20:23]
	v_mfma_f32_16x16x4_f32 v[20:23], v112, v116, v[20:23]
	v_mfma_f32_16x16x4_f32 v[20:23], v113, v117, v[20:23]
	v_mfma_f32_16x16x4_f32 v[20:23], v94, v98, v[20:23]
	v_mul_f32_e32 v94, v81, v81
	v_fmac_f32_e32 v94, v80, v80
	v_add_f32_e32 v25, v25, v94
	v_add_f32_e32 v24, v24, v25
	v_mul_f32_e32 v25, v59, v59
	v_fmac_f32_e32 v25, v58, v58
	v_mfma_f32_16x16x4_f32 v[20:23], v95, v99, v[20:23]
	v_mfma_f32_16x16x4_f32 v[20:23], v96, v100, v[20:23]
	v_mfma_f32_16x16x4_f32 v[20:23], v97, v101, v[20:23]
	v_mfma_f32_16x16x4_f32 v[20:23], v78, v82, v[20:23]
	v_mul_f32_e32 v78, v61, v61
	v_fmac_f32_e32 v78, v60, v60
	v_add_f32_e32 v25, v25, v78
	v_add_f32_e32 v24, v24, v25
	v_mul_f32_e32 v25, v43, v43
	v_fmac_f32_e32 v25, v42, v42
	v_mfma_f32_16x16x4_f32 v[20:23], v79, v83, v[20:23]
	v_mfma_f32_16x16x4_f32 v[20:23], v80, v84, v[20:23]
	v_mfma_f32_16x16x4_f32 v[20:23], v81, v85, v[20:23]
	v_mfma_f32_16x16x4_f32 v[20:23], v58, v70, v[20:23]
	v_mul_f32_e32 v58, v45, v45
	v_fmac_f32_e32 v58, v44, v44
	v_add_f32_e32 v25, v25, v58
	v_add_f32_e32 v24, v24, v25
	v_mul_f32_e32 v25, v27, v27
	v_fmac_f32_e32 v25, v26, v26
	v_mfma_f32_16x16x4_f32 v[20:23], v59, v71, v[20:23]
	v_mfma_f32_16x16x4_f32 v[20:23], v60, v72, v[20:23]
	v_mfma_f32_16x16x4_f32 v[20:23], v61, v73, v[20:23]
	v_mfma_f32_16x16x4_f32 v[20:23], v42, v46, v[20:23]
	v_mul_f32_e32 v42, v29, v29
	v_fmac_f32_e32 v42, v28, v28
	v_add_f32_e32 v25, v25, v42
	v_add_f32_e32 v24, v24, v25
	v_mul_f32_e32 v25, v7, v7
	v_fmac_f32_e32 v25, v6, v6
	v_mfma_f32_16x16x4_f32 v[20:23], v43, v47, v[20:23]
	v_mfma_f32_16x16x4_f32 v[20:23], v44, v48, v[20:23]
	v_mfma_f32_16x16x4_f32 v[20:23], v45, v49, v[20:23]
	global_load_dwordx4 v[110:113], v[152:153], off offset:2560
	global_load_dwordx4 v[114:117], v[18:19], off
	global_load_dwordx4 v[94:97], v[152:153], off offset:2624
	global_load_dwordx4 v[98:101], v[18:19], off offset:1024
	global_load_dwordx4 v[78:81], v[152:153], off offset:2688
	global_load_dwordx4 v[82:85], v[18:19], off offset:2048
	global_load_dwordx4 v[58:61], v[152:153], off offset:2752
	global_load_dwordx4 v[70:73], v[18:19], off offset:3072
	global_load_dwordx4 v[42:45], v[152:153], off offset:2816
	s_waitcnt vmcnt(8)
	v_mul_f32_e32 v138, v113, v113
	v_mfma_f32_16x16x4_f32 v[20:23], v26, v30, v[20:23]
	v_mul_f32_e32 v26, v9, v9
	v_fmac_f32_e32 v26, v8, v8
	v_add_f32_e32 v25, v25, v26
	v_add_f32_e32 v132, v24, v25
	v_fmac_f32_e32 v138, v112, v112
	v_mfma_f32_16x16x4_f32 v[20:23], v27, v31, v[20:23]
	v_mfma_f32_16x16x4_f32 v[20:23], v28, v32, v[20:23]
	v_mfma_f32_16x16x4_f32 v[20:23], v29, v33, v[20:23]
	v_mfma_f32_16x16x4_f32 v[20:23], v6, v14, v[20:23]
	v_add_co_u32_e32 v14, vcc, s22, v154
	s_mov_b32 s22, 0xd000
	v_mfma_f32_16x16x4_f32 v[20:23], v7, v15, v[20:23]
	v_addc_co_u32_e32 v15, vcc, 0, v155, vcc
	v_add_co_u32_e32 v130, vcc, s84, v154
	s_nop 1
	v_addc_co_u32_e32 v131, vcc, 0, v155, vcc
	v_mfma_f32_16x16x4_f32 v[20:23], v8, v16, v[20:23]
	v_mfma_f32_16x16x4_f32 v[126:129], v9, v17, v[20:23]
	global_load_dwordx4 v[46:49], v[130:131], off offset:-4096
	global_load_dwordx4 v[26:29], v[152:153], off offset:2880
	global_load_dwordx4 v[30:33], v[14:15], off offset:1024
	s_nop 5
	global_load_dwordx4 v[18:21], v[152:153], off offset:2944
	global_load_dwordx4 v[22:25], v[14:15], off offset:2048
	global_load_dwordx4 v[6:9], v[152:153], off offset:3008
	s_nop 0
	global_load_dwordx4 v[14:17], v[14:15], off offset:3072
	v_mfma_f32_16x16x4_f32 v[126:129], v122, v134, v[126:129]
	v_mfma_f32_16x16x4_f32 v[126:129], v123, v135, v[126:129]
	v_mfma_f32_16x16x4_f32 v[126:129], v124, v136, v[126:129]
	v_mfma_f32_16x16x4_f32 v[122:125], v125, v137, v[126:129]
	s_nop 8
	v_mul_f32_e32 v127, v107, v107
	v_mul_f32_e32 v128, v109, v109
	v_fmac_f32_e32 v127, v106, v106
	v_fmac_f32_e32 v128, v108, v108
	v_add_f32_e32 v126, v132, v133
	v_mul_f32_e32 v137, v111, v111
	v_fmac_f32_e32 v137, v110, v110
	v_mfma_f32_16x16x4_f32 v[122:125], v106, v118, v[122:125]
	v_add_f32_e32 v127, v127, v128
	v_add_f32_e32 v118, v126, v127
	v_add_f32_e32 v137, v137, v138
	v_mfma_f32_16x16x4_f32 v[122:125], v107, v119, v[122:125]
	v_mul_f32_e32 v119, v91, v91
	v_fmac_f32_e32 v119, v90, v90
	v_mfma_f32_16x16x4_f32 v[122:125], v108, v120, v[122:125]
; __device__ __forceinline__ void norm2_block(float* xl, float* xc, const float* MOD, const float* gn, const float* WP, bf16_t* H, float* AFF, int L, int row0, int nrows, int lane) {
;     ...
;     for (int q = 0; q < 8; ++q) { xa[q] = *(const f32x4*)(xr + 16 * q); wb[q] = *(const f32x4*)(wp + 256 * q); }
; #pragma unroll
;     for (int g = 0; g < 8; ++g) {
;         f32x4 xn[8], wn[8];
;         if (g < 7) {
; #pragma unroll
;             for (int q = 0; q < 8; ++q) { xn[q] = *(const f32x4*)(xr + 16 * (8 * (g + 1) + q)); wn[q] = *(const f32x4*)(wp + 256 * (8 * (g + 1) + q)); } }
; #pragma unroll
;         for (int q = 0; q < 8; ++q) {
;             sq += (xa[q][0] * xa[q][0] + xa[q][1] * xa[q][1]) + (xa[q][2] * xa[q][2] + xa[q][3] * xa[q][3]);
; #pragma unroll
;             for (int i = 0; i < 4; ++i) acc = __builtin_amdgcn_mfma_f32_16x16x4f32(xa[q][i], wb[q][i], acc, 0, 0, 0); }
;         if (g < 7) {
; #pragma unroll
;             for (int q = 0; q < 8; ++q) { xa[q] = xn[q]; wb[q] = wn[q]; } }
;     }
	v_mul_f32_e32 v120, v93, v93
	v_fmac_f32_e32 v120, v92, v92
	v_add_f32_e32 v119, v119, v120
	v_mfma_f32_16x16x4_f32 v[106:109], v109, v121, v[122:125]
	v_mfma_f32_16x16x4_f32 v[106:109], v90, v102, v[106:109]
	v_add_f32_e32 v102, v118, v119
	v_mfma_f32_16x16x4_f32 v[106:109], v91, v103, v[106:109]
	v_mul_f32_e32 v103, v75, v75
	v_fmac_f32_e32 v103, v74, v74
	v_mfma_f32_16x16x4_f32 v[106:109], v92, v104, v[106:109]
	v_mul_f32_e32 v104, v77, v77
	v_fmac_f32_e32 v104, v76, v76
	v_add_f32_e32 v103, v103, v104
	v_mfma_f32_16x16x4_f32 v[90:93], v93, v105, v[106:109]
	v_mfma_f32_16x16x4_f32 v[90:93], v74, v86, v[90:93]
	v_add_f32_e32 v86, v102, v103
	v_mfma_f32_16x16x4_f32 v[90:93], v75, v87, v[90:93]
	v_mul_f32_e32 v87, v63, v63
	v_fmac_f32_e32 v87, v62, v62
	v_mfma_f32_16x16x4_f32 v[90:93], v76, v88, v[90:93]
	v_mul_f32_e32 v88, v65, v65
	v_fmac_f32_e32 v88, v64, v64
	v_add_f32_e32 v87, v87, v88
	v_mfma_f32_16x16x4_f32 v[74:77], v77, v89, v[90:93]
	v_mfma_f32_16x16x4_f32 v[74:77], v62, v66, v[74:77]
	v_add_f32_e32 v66, v86, v87
	v_mfma_f32_16x16x4_f32 v[74:77], v63, v67, v[74:77]
	v_mul_f32_e32 v67, v51, v51
	v_fmac_f32_e32 v67, v50, v50
	v_mfma_f32_16x16x4_f32 v[74:77], v64, v68, v[74:77]
	v_mul_f32_e32 v68, v53, v53
	v_fmac_f32_e32 v68, v52, v52
	v_add_f32_e32 v67, v67, v68
	v_mfma_f32_16x16x4_f32 v[62:65], v65, v69, v[74:77]
	v_mfma_f32_16x16x4_f32 v[62:65], v50, v54, v[62:65]
	v_add_f32_e32 v54, v66, v67
	v_mfma_f32_16x16x4_f32 v[62:65], v51, v55, v[62:65]
	v_mul_f32_e32 v55, v35, v35
	v_fmac_f32_e32 v55, v34, v34
	v_mfma_f32_16x16x4_f32 v[62:65], v52, v56, v[62:65]
	v_mul_f32_e32 v56, v37, v37
	v_fmac_f32_e32 v56, v36, v36
	v_add_f32_e32 v55, v55, v56
	v_mfma_f32_16x16x4_f32 v[50:53], v53, v57, v[62:65]
	global_load_dwordx4 v[122:125], v[152:153], off offset:3072
	global_load_dwordx4 v[126:129], v[130:131], off
	global_load_dwordx4 v[106:109], v[152:153], off offset:3136
	global_load_dwordx4 v[118:121], v[130:131], off offset:1024
	global_load_dwordx4 v[90:93], v[152:153], off offset:3200
	global_load_dwordx4 v[102:105], v[130:131], off offset:2048
	global_load_dwordx4 v[74:77], v[152:153], off offset:3264
	global_load_dwordx4 v[86:89], v[130:131], off offset:3072
	global_load_dwordx4 v[62:65], v[152:153], off offset:3328
	v_mfma_f32_16x16x4_f32 v[50:53], v34, v38, v[50:53]
	v_add_f32_e32 v38, v54, v55
	v_mfma_f32_16x16x4_f32 v[50:53], v35, v39, v[50:53]
	v_mul_f32_e32 v39, v3, v3
	v_fmac_f32_e32 v39, v2, v2
	v_mfma_f32_16x16x4_f32 v[50:53], v36, v40, v[50:53]
	v_mul_f32_e32 v40, v5, v5
	v_fmac_f32_e32 v40, v4, v4
	v_add_f32_e32 v39, v39, v40
	v_add_f32_e32 v136, v38, v39
	v_mfma_f32_16x16x4_f32 v[34:37], v37, v41, v[50:53]
	v_mfma_f32_16x16x4_f32 v[34:37], v2, v10, v[34:37]
	v_add_co_u32_e32 v10, vcc, s22, v154
	s_mov_b32 s22, 0xf000
	v_mfma_f32_16x16x4_f32 v[34:37], v3, v11, v[34:37]
	v_addc_co_u32_e32 v11, vcc, 0, v155, vcc
	v_add_co_u32_e32 v130, vcc, s86, v154
	s_nop 1
	v_addc_co_u32_e32 v131, vcc, 0, v155, vcc
	v_mfma_f32_16x16x4_f32 v[34:37], v4, v12, v[34:37]
	v_mfma_f32_16x16x4_f32 v[132:135], v5, v13, v[34:37]
	global_load_dwordx4 v[66:69], v[130:131], off offset:-4096
	global_load_dwordx4 v[50:53], v[152:153], off offset:3392
	global_load_dwordx4 v[54:57], v[10:11], off offset:1024
	s_nop 5
	global_load_dwordx4 v[34:37], v[152:153], off offset:3456
	global_load_dwordx4 v[38:41], v[10:11], off offset:2048
	global_load_dwordx4 v[2:5], v[152:153], off offset:3520
	s_nop 0
	global_load_dwordx4 v[10:13], v[10:11], off offset:3072
	s_waitcnt vmcnt(30)
	v_mfma_f32_16x16x4_f32 v[132:135], v110, v114, v[132:135]
	v_add_f32_e32 v114, v136, v137
	s_waitcnt vmcnt(15)
	v_mul_f32_e32 v136, v125, v125
	v_fmac_f32_e32 v136, v124, v124
	v_mfma_f32_16x16x4_f32 v[132:135], v111, v115, v[132:135]
	v_mul_f32_e32 v115, v95, v95
	v_fmac_f32_e32 v115, v94, v94
	v_mfma_f32_16x16x4_f32 v[132:135], v112, v116, v[132:135]
	v_mul_f32_e32 v116, v97, v97
	v_fmac_f32_e32 v116, v96, v96
	v_add_f32_e32 v115, v115, v116
	v_mfma_f32_16x16x4_f32 v[110:113], v113, v117, v[132:135]
	s_nop 5
	v_mul_f32_e32 v135, v123, v123
	v_fmac_f32_e32 v135, v122, v122
	v_add_f32_e32 v135, v135, v136
	v_mfma_f32_16x16x4_f32 v[110:113], v94, v98, v[110:113]
	v_add_f32_e32 v98, v114, v115
	v_mfma_f32_16x16x4_f32 v[110:113], v95, v99, v[110:113]
	v_mul_f32_e32 v99, v79, v79
	v_fmac_f32_e32 v99, v78, v78
	v_mfma_f32_16x16x4_f32 v[110:113], v96, v100, v[110:113]
	v_mul_f32_e32 v100, v81, v81
	v_fmac_f32_e32 v100, v80, v80
	v_add_f32_e32 v99, v99, v100
	v_mfma_f32_16x16x4_f32 v[94:97], v97, v101, v[110:113]
	v_mfma_f32_16x16x4_f32 v[94:97], v78, v82, v[94:97]
	v_add_f32_e32 v82, v98, v99
	v_mfma_f32_16x16x4_f32 v[94:97], v79, v83, v[94:97]
	v_mul_f32_e32 v83, v59, v59
	v_fmac_f32_e32 v83, v58, v58
	v_mfma_f32_16x16x4_f32 v[94:97], v80, v84, v[94:97]
	v_mul_f32_e32 v84, v61, v61
	v_fmac_f32_e32 v84, v60, v60
	v_add_f32_e32 v83, v83, v84
	v_mfma_f32_16x16x4_f32 v[78:81], v81, v85, v[94:97]
	v_mfma_f32_16x16x4_f32 v[78:81], v58, v70, v[78:81]
	v_add_f32_e32 v70, v82, v83
	v_mfma_f32_16x16x4_f32 v[78:81], v59, v71, v[78:81]
	v_mul_f32_e32 v71, v43, v43
	v_fmac_f32_e32 v71, v42, v42
	v_mfma_f32_16x16x4_f32 v[78:81], v60, v72, v[78:81]
	v_mul_f32_e32 v72, v45, v45
	v_fmac_f32_e32 v72, v44, v44
	v_add_f32_e32 v71, v71, v72
	v_mfma_f32_16x16x4_f32 v[58:61], v61, v73, v[78:81]
	v_mfma_f32_16x16x4_f32 v[58:61], v42, v46, v[58:61]
	v_add_f32_e32 v46, v70, v71
	v_mfma_f32_16x16x4_f32 v[58:61], v43, v47, v[58:61]
	v_mul_f32_e32 v47, v27, v27
	v_fmac_f32_e32 v47, v26, v26
	v_mfma_f32_16x16x4_f32 v[58:61], v44, v48, v[58:61]
	v_mul_f32_e32 v48, v29, v29
	v_fmac_f32_e32 v48, v28, v28
; __device__ __forceinline__ void norm2_block(float* xl, float* xc, const float* MOD, const float* gn, const float* WP, bf16_t* H, float* AFF, int L, int row0, int nrows, int lane) {
;     ...
; #pragma unroll
;     for (int g = 0; g < 8; ++g) {
;         f32x4 xn[8], wn[8];
;         if (g < 7) {
; #pragma unroll
;             for (int q = 0; q < 8; ++q) { xn[q] = *(const f32x4*)(xr + 16 * (8 * (g + 1) + q)); wn[q] = *(const f32x4*)(wp + 256 * (8 * (g + 1) + q)); } }
; #pragma unroll
;         for (int q = 0; q < 8; ++q) {
;             sq += (xa[q][0] * xa[q][0] + xa[q][1] * xa[q][1]) + (xa[q][2] * xa[q][2] + xa[q][3] * xa[q][3]);
; #pragma unroll
;             for (int i = 0; i < 4; ++i) acc = __builtin_amdgcn_mfma_f32_16x16x4f32(xa[q][i], wb[q][i], acc, 0, 0, 0); }
;         if (g < 7) {
; #pragma unroll
;             for (int q = 0; q < 8; ++q) { xa[q] = xn[q]; wb[q] = wn[q]; } }
;     }
	v_add_f32_e32 v47, v47, v48
	v_mfma_f32_16x16x4_f32 v[42:45], v45, v49, v[58:61]
	v_mfma_f32_16x16x4_f32 v[42:45], v26, v30, v[42:45]
	v_add_f32_e32 v30, v46, v47
	global_load_dwordx4 v[46:49], v[152:153], off offset:3584
	s_nop 2
	global_load_dwordx4 v[58:61], v[130:131], off
	global_load_dwordx4 v[70:73], v[152:153], off offset:3648
	global_load_dwordx4 v[78:81], v[130:131], off offset:1024
	global_load_dwordx4 v[82:85], v[152:153], off offset:3712
	global_load_dwordx4 v[94:97], v[130:131], off offset:2048
	global_load_dwordx4 v[98:101], v[152:153], off offset:3776
	global_load_dwordx4 v[110:113], v[130:131], off offset:3072
	global_load_dwordx4 v[114:117], v[152:153], off offset:3840
	v_mfma_f32_16x16x4_f32 v[42:45], v27, v31, v[42:45]
	v_mul_f32_e32 v31, v19, v19
	v_fmac_f32_e32 v31, v18, v18
	v_mfma_f32_16x16x4_f32 v[42:45], v28, v32, v[42:45]
	v_mul_f32_e32 v32, v21, v21
	v_fmac_f32_e32 v32, v20, v20
	v_add_f32_e32 v31, v31, v32
	v_mfma_f32_16x16x4_f32 v[26:29], v29, v33, v[42:45]
	v_mfma_f32_16x16x4_f32 v[26:29], v18, v22, v[26:29]
	v_add_f32_e32 v22, v30, v31
	v_mfma_f32_16x16x4_f32 v[26:29], v19, v23, v[26:29]
	v_mul_f32_e32 v23, v7, v7
	v_fmac_f32_e32 v23, v6, v6
	v_mfma_f32_16x16x4_f32 v[26:29], v20, v24, v[26:29]
	v_mul_f32_e32 v24, v9, v9
	v_fmac_f32_e32 v24, v8, v8
	v_add_f32_e32 v23, v23, v24
	v_add_f32_e32 v134, v22, v23
	v_mfma_f32_16x16x4_f32 v[18:21], v21, v25, v[26:29]
	v_mfma_f32_16x16x4_f32 v[18:21], v6, v14, v[18:21]
	v_add_co_u32_e32 v14, vcc, s22, v154
	v_mfma_f32_16x16x4_f32 v[18:21], v7, v15, v[18:21]
	s_nop 0
	v_addc_co_u32_e32 v15, vcc, 0, v155, vcc
	v_mfma_f32_16x16x4_f32 v[18:21], v8, v16, v[18:21]
	v_mfma_f32_16x16x4_f32 v[42:45], v9, v17, v[18:21]
	global_load_dwordx4 v[130:133], v[14:15], off
	global_load_dwordx4 v[26:29], v[152:153], off offset:3904
	global_load_dwordx4 v[30:33], v[14:15], off offset:1024
	s_nop 5
	global_load_dwordx4 v[18:21], v[152:153], off offset:3968
	global_load_dwordx4 v[22:25], v[14:15], off offset:2048
	global_load_dwordx4 v[6:9], v[152:153], off offset:4032
	s_nop 0
	global_load_dwordx4 v[14:17], v[14:15], off offset:3072
	s_waitcnt vmcnt(30)
	v_mfma_f32_16x16x4_f32 v[42:45], v122, v126, v[42:45]
	v_add_f32_e32 v122, v134, v135
	v_mfma_f32_16x16x4_f32 v[42:45], v123, v127, v[42:45]
	s_waitcnt vmcnt(29)
	v_mul_f32_e32 v123, v107, v107
	v_fmac_f32_e32 v123, v106, v106
	v_mfma_f32_16x16x4_f32 v[42:45], v124, v128, v[42:45]
	v_mul_f32_e32 v124, v109, v109
	v_fmac_f32_e32 v124, v108, v108
	v_add_f32_e32 v123, v123, v124
	v_mfma_f32_16x16x4_f32 v[42:45], v125, v129, v[42:45]
	s_waitcnt vmcnt(28)
	v_mfma_f32_16x16x4_f32 v[42:45], v106, v118, v[42:45]
	v_add_f32_e32 v106, v122, v123
	v_mfma_f32_16x16x4_f32 v[42:45], v107, v119, v[42:45]
	s_waitcnt vmcnt(27)
	v_mul_f32_e32 v107, v91, v91
	v_fmac_f32_e32 v107, v90, v90
	v_mfma_f32_16x16x4_f32 v[42:45], v108, v120, v[42:45]
	v_mul_f32_e32 v108, v93, v93
	v_fmac_f32_e32 v108, v92, v92
	v_add_f32_e32 v107, v107, v108
	v_mfma_f32_16x16x4_f32 v[42:45], v109, v121, v[42:45]
	s_waitcnt vmcnt(26)
	v_mfma_f32_16x16x4_f32 v[42:45], v90, v102, v[42:45]
	v_add_f32_e32 v90, v106, v107
	v_mfma_f32_16x16x4_f32 v[42:45], v91, v103, v[42:45]
	s_waitcnt vmcnt(25)
	v_mul_f32_e32 v91, v75, v75
	v_fmac_f32_e32 v91, v74, v74
	v_mfma_f32_16x16x4_f32 v[42:45], v92, v104, v[42:45]
	v_mul_f32_e32 v92, v77, v77
	v_fmac_f32_e32 v92, v76, v76
	v_add_f32_e32 v91, v91, v92
	v_mfma_f32_16x16x4_f32 v[42:45], v93, v105, v[42:45]
	s_waitcnt vmcnt(24)
	v_mfma_f32_16x16x4_f32 v[42:45], v74, v86, v[42:45]
	v_add_f32_e32 v74, v90, v91
	v_mfma_f32_16x16x4_f32 v[42:45], v75, v87, v[42:45]
	s_waitcnt vmcnt(23)
	v_mul_f32_e32 v75, v63, v63
	v_fmac_f32_e32 v75, v62, v62
	v_mfma_f32_16x16x4_f32 v[42:45], v76, v88, v[42:45]
	v_mul_f32_e32 v76, v65, v65
	v_fmac_f32_e32 v76, v64, v64
	v_add_f32_e32 v75, v75, v76
	v_mfma_f32_16x16x4_f32 v[42:45], v77, v89, v[42:45]
	s_waitcnt vmcnt(22)
	v_mfma_f32_16x16x4_f32 v[42:45], v62, v66, v[42:45]
	v_add_f32_e32 v62, v74, v75
	v_mfma_f32_16x16x4_f32 v[42:45], v63, v67, v[42:45]
	s_waitcnt vmcnt(21)
	v_mul_f32_e32 v63, v51, v51
	v_fmac_f32_e32 v63, v50, v50
	v_mfma_f32_16x16x4_f32 v[42:45], v64, v68, v[42:45]
	v_mul_f32_e32 v64, v53, v53
	v_fmac_f32_e32 v64, v52, v52
	v_add_f32_e32 v63, v63, v64
	v_mfma_f32_16x16x4_f32 v[42:45], v65, v69, v[42:45]
	s_waitcnt vmcnt(20)
	v_mfma_f32_16x16x4_f32 v[42:45], v50, v54, v[42:45]
	v_add_f32_e32 v50, v62, v63
	v_mfma_f32_16x16x4_f32 v[42:45], v51, v55, v[42:45]
	s_waitcnt vmcnt(19)
	v_mul_f32_e32 v51, v35, v35
	v_fmac_f32_e32 v51, v34, v34
	v_mfma_f32_16x16x4_f32 v[42:45], v52, v56, v[42:45]
	v_mul_f32_e32 v52, v37, v37
	v_fmac_f32_e32 v52, v36, v36
	v_add_f32_e32 v51, v51, v52
	v_mfma_f32_16x16x4_f32 v[42:45], v53, v57, v[42:45]
	s_waitcnt vmcnt(18)
	v_mfma_f32_16x16x4_f32 v[42:45], v34, v38, v[42:45]
	v_add_f32_e32 v38, v50, v51
	v_mfma_f32_16x16x4_f32 v[42:45], v35, v39, v[42:45]
	s_waitcnt vmcnt(17)
	v_mul_f32_e32 v39, v3, v3
	v_fmac_f32_e32 v39, v2, v2
	v_mfma_f32_16x16x4_f32 v[42:45], v36, v40, v[42:45]
	v_mul_f32_e32 v40, v5, v5
	v_fmac_f32_e32 v40, v4, v4
	v_add_f32_e32 v39, v39, v40
	v_mfma_f32_16x16x4_f32 v[34:37], v37, v41, v[42:45]
	s_waitcnt vmcnt(16)
	v_mfma_f32_16x16x4_f32 v[34:37], v2, v10, v[34:37]
	v_add_f32_e32 v10, v38, v39
	v_mfma_f32_16x16x4_f32 v[34:37], v3, v11, v[34:37]
	s_waitcnt vmcnt(15)
	v_mul_f32_e32 v11, v47, v47
	v_fmac_f32_e32 v11, v46, v46
	v_mfma_f32_16x16x4_f32 v[34:37], v4, v12, v[34:37]
	v_mul_f32_e32 v12, v49, v49
	v_fmac_f32_e32 v12, v48, v48
	v_add_f32_e32 v11, v11, v12
	v_add_f32_e32 v10, v10, v11
	s_waitcnt vmcnt(13)
; __device__ __forceinline__ void norm2_block(float* xl, float* xc, const float* MOD, const float* gn, const float* WP, bf16_t* H, float* AFF, int L, int row0, int nrows, int lane) {
;     ...
;             for (int i = 0; i < 4; ++i) acc = __builtin_amdgcn_mfma_f32_16x16x4f32(xa[q][i], wb[q][i], acc, 0, 0, 0); }
;         if (g < 7) {
; #pragma unroll
;             for (int q = 0; q < 8; ++q) { xa[q] = xn[q]; wb[q] = wn[q]; } }
;     }
;     sq = att::lanes4_sum(sq);
;     const float rstd = rsqrtf(sq * (1.f / DM) + EPS);
;     const float bias = WP[9 * 16384 + s_ * 16 + r16];
; #pragma unroll
;     for (int i = 0; i < 4; ++i) {
;         const float rs = __shfl(rstd, 4 * kq + i);
;         const float lg = acc[i] * rs + bias;
;         float mx = lg;
; #pragma unroll
;         for (int o = 1; o < 16; o <<= 1) mx = fmaxf(mx, __shfl_xor(mx, o));
;         const float mine = __expf(lg - mx); float den = mine;
; #pragma unroll
;         for (int o = 1; o < 16; o <<= 1) den += __shfl_xor(den, o);
;         if (4 * kq + i < nrows) AFF[(size_t)(row0 + 4 * kq + i) * 16 + r16] = mine / den;
;     }
	v_mul_f32_e32 v11, v71, v71
	v_mul_f32_e32 v12, v73, v73
	v_fmac_f32_e32 v11, v70, v70
	v_mfma_f32_16x16x4_f32 v[2:5], v5, v13, v[34:37]
	v_fmac_f32_e32 v12, v72, v72
	v_add_f32_e32 v11, v11, v12
	v_add_f32_e32 v10, v10, v11
	s_waitcnt vmcnt(11)
	v_mul_f32_e32 v11, v83, v83
	v_mul_f32_e32 v12, v85, v85
	v_fmac_f32_e32 v11, v82, v82
	v_fmac_f32_e32 v12, v84, v84
	v_mfma_f32_16x16x4_f32 v[2:5], v46, v58, v[2:5]
	v_add_f32_e32 v11, v11, v12
	v_add_f32_e32 v10, v10, v11
	s_waitcnt vmcnt(9)
	v_mul_f32_e32 v11, v99, v99
	v_mul_f32_e32 v12, v101, v101
	v_fmac_f32_e32 v11, v98, v98
	v_fmac_f32_e32 v12, v100, v100
	v_add_f32_e32 v11, v11, v12
	v_mfma_f32_16x16x4_f32 v[2:5], v47, v59, v[2:5]
	v_add_f32_e32 v10, v10, v11
	s_waitcnt vmcnt(7)
	v_mul_f32_e32 v11, v115, v115
	v_mul_f32_e32 v12, v117, v117
	v_fmac_f32_e32 v11, v114, v114
	v_fmac_f32_e32 v12, v116, v116
	v_add_f32_e32 v11, v11, v12
	v_add_f32_e32 v10, v10, v11
	v_mfma_f32_16x16x4_f32 v[2:5], v48, v60, v[2:5]
	s_waitcnt vmcnt(5)
	v_mul_f32_e32 v11, v27, v27
	v_mul_f32_e32 v12, v29, v29
	v_fmac_f32_e32 v11, v26, v26
	v_fmac_f32_e32 v12, v28, v28
	v_add_f32_e32 v11, v11, v12
	v_add_f32_e32 v10, v10, v11
	s_waitcnt vmcnt(3)
	v_mul_f32_e32 v11, v19, v19
	v_mfma_f32_16x16x4_f32 v[2:5], v49, v61, v[2:5]
	v_mul_f32_e32 v12, v21, v21
	v_fmac_f32_e32 v11, v18, v18
	v_fmac_f32_e32 v12, v20, v20
	v_add_f32_e32 v11, v11, v12
	v_add_f32_e32 v10, v10, v11
	s_waitcnt vmcnt(1)
	v_mul_f32_e32 v11, v7, v7
	v_mul_f32_e32 v12, v9, v9
	v_mfma_f32_16x16x4_f32 v[2:5], v70, v78, v[2:5]
	v_fmac_f32_e32 v11, v6, v6
	v_fmac_f32_e32 v12, v8, v8
	v_add_f32_e32 v11, v11, v12
	v_mfma_f32_16x16x4_f32 v[2:5], v71, v79, v[2:5]
	v_mfma_f32_16x16x4_f32 v[2:5], v72, v80, v[2:5]
	v_mfma_f32_16x16x4_f32 v[2:5], v73, v81, v[2:5]
	v_mfma_f32_16x16x4_f32 v[2:5], v82, v94, v[2:5]
	v_mfma_f32_16x16x4_f32 v[2:5], v83, v95, v[2:5]
	v_mfma_f32_16x16x4_f32 v[2:5], v84, v96, v[2:5]
	v_mfma_f32_16x16x4_f32 v[2:5], v85, v97, v[2:5]
	v_mfma_f32_16x16x4_f32 v[2:5], v98, v110, v[2:5]
	v_mfma_f32_16x16x4_f32 v[2:5], v99, v111, v[2:5]
	v_mfma_f32_16x16x4_f32 v[2:5], v100, v112, v[2:5]
	v_mfma_f32_16x16x4_f32 v[2:5], v101, v113, v[2:5]
	v_mfma_f32_16x16x4_f32 v[2:5], v114, v130, v[2:5]
	v_mfma_f32_16x16x4_f32 v[2:5], v115, v131, v[2:5]
	v_mfma_f32_16x16x4_f32 v[2:5], v116, v132, v[2:5]
	v_mfma_f32_16x16x4_f32 v[2:5], v117, v133, v[2:5]
	v_mfma_f32_16x16x4_f32 v[2:5], v26, v30, v[2:5]
	v_mfma_f32_16x16x4_f32 v[2:5], v27, v31, v[2:5]
	v_mfma_f32_16x16x4_f32 v[2:5], v28, v32, v[2:5]
	v_mfma_f32_16x16x4_f32 v[2:5], v29, v33, v[2:5]
	v_mfma_f32_16x16x4_f32 v[2:5], v18, v22, v[2:5]
	v_mfma_f32_16x16x4_f32 v[2:5], v19, v23, v[2:5]
	v_mfma_f32_16x16x4_f32 v[2:5], v20, v24, v[2:5]
	v_mfma_f32_16x16x4_f32 v[2:5], v21, v25, v[2:5]
	s_waitcnt vmcnt(0)
	v_mfma_f32_16x16x4_f32 v[2:5], v6, v14, v[2:5]
	v_add_f32_e32 v6, v10, v11
	v_mfma_f32_16x16x4_f32 v[2:5], v7, v15, v[2:5]
	v_mov_b32_e32 v7, v6
	s_nop 1
	v_permlane16_swap_b32_e32 v6, v7
	v_add_f32_e32 v6, v6, v7
	v_mov_b32_e32 v7, v6
	s_nop 1
	v_permlane32_swap_b32_e32 v6, v7
	v_add_f32_e32 v6, v6, v7
	v_fmamk_f32 v6, v6, 0x3a800000, v196
	v_cmp_gt_f32_e32 vcc, s95, v6
	v_mul_f32_e32 v7, 0x4b800000, v6
	v_mfma_f32_16x16x4_f32 v[2:5], v8, v16, v[2:5]
	v_cndmask_b32_e32 v6, v6, v7, vcc
	v_rsq_f32_e32 v6, v6
	v_or_b32_e32 v8, v226, v142
	v_lshlrev_b32_e32 v8, 2, v8
	v_mul_f32_e32 v7, 0x45800000, v6
	v_cndmask_b32_e32 v34, v6, v7, vcc
	v_lshl_add_u32 v6, s24, 4, v143
	v_ashrrev_i32_e32 v7, 31, v6
	v_lshl_add_u64 v[6:7], v[6:7], 2, s[12:13]
	global_load_dword v7, v[6:7], off
	v_mfma_f32_16x16x4_f32 v[2:5], v9, v17, v[2:5]
	ds_bpermute_b32 v8, v8, v34
	v_cmp_lt_i32_e32 vcc, v233, v227
	v_add_u32_e32 v6, s18, v142
	s_waitcnt vmcnt(0) lgkmcnt(0)
	s_nop 5
	v_fma_f32 v11, v2, v8, v7
	v_cndmask_b32_e32 v2, v225, v233, vcc
	v_lshlrev_b32_e32 v2, 2, v2
	ds_bpermute_b32 v8, v2, v11
	v_cmp_lt_i32_e32 vcc, v171, v227
	s_waitcnt lgkmcnt(0)
	v_max_f32_e32 v8, v8, v8
	v_max_f32_e32 v9, v11, v8
	v_cndmask_b32_e32 v8, v225, v171, vcc
	v_lshlrev_b32_e32 v8, 2, v8
	s_nop 1
	v_mov_b32_dpp v10, v9 quad_perm:[2,3,0,1] row_mask:0xf bank_mask:0xf
	v_cmp_lt_i32_e32 vcc, v172, v227
	s_waitcnt lgkmcnt(0)
	v_max_f32_e32 v10, v10, v10
	v_max_f32_e32 v10, v9, v10
	v_cndmask_b32_e32 v9, v225, v172, vcc
	v_lshlrev_b32_e32 v9, 2, v9
	s_nop 1
	v_mov_b32_dpp v12, v10 row_shl:4 row_mask:0xf bank_mask:0x5
	v_mov_b32_dpp v12, v10 row_shr:4 row_mask:0xf bank_mask:0xa
	v_cmp_lt_i32_e32 vcc, v173, v227
	s_waitcnt lgkmcnt(0)
	v_max_f32_e32 v12, v12, v12
	v_max_f32_e32 v12, v10, v12
	v_cndmask_b32_e32 v10, v225, v173, vcc
	v_lshlrev_b32_e32 v10, 2, v10
	s_nop 1
	v_mov_b32_dpp v13, v12 row_shl:8 row_mask:0xf bank_mask:0x3
	v_mov_b32_dpp v13, v12 row_shr:8 row_mask:0xf bank_mask:0xc
	s_waitcnt lgkmcnt(0)
	v_max_f32_e32 v13, v13, v13
	v_max_f32_e32 v12, v12, v13
	v_sub_f32_e32 v11, v11, v12
	v_mul_f32_e32 v11, 0x3fb8aa3b, v11
	v_exp_f32_e32 v11, v11
	ds_bpermute_b32 v12, v2, v11
	s_waitcnt lgkmcnt(0)
	v_add_f32_e32 v12, v11, v12
	s_nop 1
	v_mov_b32_dpp v13, v12 quad_perm:[2,3,0,1] row_mask:0xf bank_mask:0xf
	s_waitcnt lgkmcnt(0)
	v_add_f32_e32 v12, v12, v13
	s_nop 1
	v_mov_b32_dpp v13, v12 row_shl:4 row_mask:0xf bank_mask:0x5
	v_mov_b32_dpp v13, v12 row_shr:4 row_mask:0xf bank_mask:0xa
	s_waitcnt lgkmcnt(0)
	v_add_f32_e32 v12, v12, v13
	s_nop 1
	v_mov_b32_dpp v13, v12 row_shl:8 row_mask:0xf bank_mask:0x3
	v_mov_b32_dpp v13, v12 row_shr:8 row_mask:0xf bank_mask:0xc
	s_and_saveexec_b64 s[22:23], s[4:5]
	s_cbranch_execz .LBB0_1198
	s_waitcnt lgkmcnt(0)
	v_add_f32_e32 v13, v12, v13
	v_div_scale_f32 v14, s[26:27], v13, v13, v11
	v_rcp_f32_e32 v15, v14
	v_add_u32_e32 v12, -7, v6
	v_fma_f32 v16, -v14, v15, 1.0
	v_fmac_f32_e32 v15, v16, v15
	v_div_scale_f32 v16, vcc, v11, v13, v11
	v_mul_f32_e32 v17, v16, v15
	v_fma_f32 v18, -v14, v17, v16
	v_fmac_f32_e32 v17, v18, v15
	v_fma_f32 v14, -v14, v17, v16
	v_div_fmas_f32 v14, v14, v15, v17
	v_div_fixup_f32 v11, v14, v13, v11
	v_ashrrev_i32_e32 v13, 31, v12
	v_lshlrev_b64 v[12:13], 6, v[12:13]
	v_lshl_add_u64 v[12:13], v[146:147], 0, v[12:13]
	global_store_dword v[12:13], v11, off
; __device__ __forceinline__ void norm2_block(float* xl, float* xc, const float* MOD, const float* gn, const float* WP, bf16_t* H, float* AFF, int L, int row0, int nrows, int lane) {
;     ...
;     for (int i = 0; i < 4; ++i) {
;         const float rs = __shfl(rstd, 4 * kq + i);
;         const float lg = acc[i] * rs + bias;
;         float mx = lg;
; #pragma unroll
;         for (int o = 1; o < 16; o <<= 1) mx = fmaxf(mx, __shfl_xor(mx, o));
;         const float mine = __expf(lg - mx); float den = mine;
; #pragma unroll
;         for (int o = 1; o < 16; o <<= 1) den += __shfl_xor(den, o);
;         if (4 * kq + i < nrows) AFF[(size_t)(row0 + 4 * kq + i) * 16 + r16] = mine / den;
;     }
.LBB0_1198:
	s_or_b64 exec, exec, s[22:23]
	v_or_b32_e32 v11, v226, v160
	v_lshlrev_b32_e32 v11, 2, v11
	ds_bpermute_b32 v11, v11, v34
	s_waitcnt lgkmcnt(0)
	v_fma_f32 v3, v3, v11, v7
	ds_bpermute_b32 v11, v2, v3
	s_waitcnt lgkmcnt(0)
	v_max_f32_e32 v11, v11, v11
	v_max_f32_e32 v11, v3, v11
	s_nop 1
	v_mov_b32_dpp v12, v11 quad_perm:[2,3,0,1] row_mask:0xf bank_mask:0xf
	s_waitcnt lgkmcnt(0)
	v_max_f32_e32 v12, v12, v12
	v_max_f32_e32 v11, v11, v12
	s_nop 1
	v_mov_b32_dpp v12, v11 row_shl:4 row_mask:0xf bank_mask:0x5
	v_mov_b32_dpp v12, v11 row_shr:4 row_mask:0xf bank_mask:0xa
	s_waitcnt lgkmcnt(0)
	v_max_f32_e32 v12, v12, v12
	v_max_f32_e32 v11, v11, v12
	s_nop 1
	v_mov_b32_dpp v12, v11 row_shl:8 row_mask:0xf bank_mask:0x3
	v_mov_b32_dpp v12, v11 row_shr:8 row_mask:0xf bank_mask:0xc
	s_waitcnt lgkmcnt(0)
	v_max_f32_e32 v12, v12, v12
	v_max_f32_e32 v11, v11, v12
	v_sub_f32_e32 v3, v3, v11
	v_mul_f32_e32 v3, 0x3fb8aa3b, v3
	v_exp_f32_e32 v3, v3
	ds_bpermute_b32 v11, v2, v3
	s_waitcnt lgkmcnt(0)
	v_add_f32_e32 v11, v3, v11
	s_nop 1
	v_mov_b32_dpp v12, v11 quad_perm:[2,3,0,1] row_mask:0xf bank_mask:0xf
	s_waitcnt lgkmcnt(0)
	v_add_f32_e32 v11, v11, v12
	s_nop 1
	v_mov_b32_dpp v12, v11 row_shl:4 row_mask:0xf bank_mask:0x5
	v_mov_b32_dpp v12, v11 row_shr:4 row_mask:0xf bank_mask:0xa
	s_waitcnt lgkmcnt(0)
	v_add_f32_e32 v11, v11, v12
	s_nop 1
	v_mov_b32_dpp v12, v11 row_shl:8 row_mask:0xf bank_mask:0x3
	v_mov_b32_dpp v12, v11 row_shr:8 row_mask:0xf bank_mask:0xc
	s_and_saveexec_b64 s[22:23], s[4:5]
	s_cbranch_execz .LBB0_1200
	s_waitcnt lgkmcnt(0)
	v_add_f32_e32 v11, v11, v12
	v_div_scale_f32 v12, s[26:27], v11, v11, v3
	v_rcp_f32_e32 v13, v12
	v_div_scale_f32 v14, vcc, v3, v11, v3
	v_fma_f32 v15, -v12, v13, 1.0
	v_fmac_f32_e32 v13, v15, v13
	v_mul_f32_e32 v15, v14, v13
	v_fma_f32 v16, -v12, v15, v14
	v_fmac_f32_e32 v15, v16, v13
	v_fma_f32 v12, -v12, v15, v14
	v_div_fmas_f32 v12, v12, v13, v15
	v_div_fixup_f32 v3, v12, v11, v3
	v_add_u32_e32 v12, -6, v6
	v_ashrrev_i32_e32 v13, 31, v12
	v_lshlrev_b64 v[12:13], 6, v[12:13]
	v_lshl_add_u64 v[12:13], v[146:147], 0, v[12:13]
	global_store_dword v[12:13], v3, off
.LBB0_1200:
	s_or_b64 exec, exec, s[22:23]
	v_or_b32_e32 v3, v226, v161
	v_lshlrev_b32_e32 v3, 2, v3
	ds_bpermute_b32 v3, v3, v34
	s_waitcnt lgkmcnt(0)
	v_fma_f32 v3, v4, v3, v7
	ds_bpermute_b32 v4, v2, v3
	s_waitcnt lgkmcnt(0)
	v_max_f32_e32 v4, v4, v4
	v_max_f32_e32 v4, v3, v4
	s_nop 1
	v_mov_b32_dpp v11, v4 quad_perm:[2,3,0,1] row_mask:0xf bank_mask:0xf
	s_waitcnt lgkmcnt(0)
	v_max_f32_e32 v11, v11, v11
	v_max_f32_e32 v4, v4, v11
	s_nop 1
	v_mov_b32_dpp v11, v4 row_shl:4 row_mask:0xf bank_mask:0x5
	v_mov_b32_dpp v11, v4 row_shr:4 row_mask:0xf bank_mask:0xa
	s_waitcnt lgkmcnt(0)
	v_max_f32_e32 v11, v11, v11
	v_max_f32_e32 v4, v4, v11
	s_nop 1
	v_mov_b32_dpp v11, v4 row_shl:8 row_mask:0xf bank_mask:0x3
	v_mov_b32_dpp v11, v4 row_shr:8 row_mask:0xf bank_mask:0xc
	s_waitcnt lgkmcnt(0)
	v_max_f32_e32 v11, v11, v11
	v_max_f32_e32 v4, v4, v11
	v_sub_f32_e32 v3, v3, v4
	v_mul_f32_e32 v3, 0x3fb8aa3b, v3
	v_exp_f32_e32 v3, v3
	ds_bpermute_b32 v4, v2, v3
	s_waitcnt lgkmcnt(0)
	v_add_f32_e32 v4, v3, v4
	s_nop 1
	v_mov_b32_dpp v11, v4 quad_perm:[2,3,0,1] row_mask:0xf bank_mask:0xf
	s_waitcnt lgkmcnt(0)
	v_add_f32_e32 v4, v4, v11
	s_nop 1
	v_mov_b32_dpp v11, v4 row_shl:4 row_mask:0xf bank_mask:0x5
	v_mov_b32_dpp v11, v4 row_shr:4 row_mask:0xf bank_mask:0xa
	s_waitcnt lgkmcnt(0)
	v_add_f32_e32 v4, v4, v11
	s_nop 1
	v_mov_b32_dpp v11, v4 row_shl:8 row_mask:0xf bank_mask:0x3
	v_mov_b32_dpp v11, v4 row_shr:8 row_mask:0xf bank_mask:0xc
	s_and_saveexec_b64 s[22:23], s[4:5]
	s_cbranch_execz .LBB0_1202
	s_waitcnt lgkmcnt(0)
	v_add_f32_e32 v4, v4, v11
	v_div_scale_f32 v11, s[26:27], v4, v4, v3
	v_rcp_f32_e32 v12, v11
	v_div_scale_f32 v13, vcc, v3, v4, v3
	v_fma_f32 v14, -v11, v12, 1.0
	v_fmac_f32_e32 v12, v14, v12
	v_mul_f32_e32 v14, v13, v12
	v_fma_f32 v15, -v11, v14, v13
	v_fmac_f32_e32 v14, v15, v12
	v_fma_f32 v11, -v11, v14, v13
	v_div_fmas_f32 v11, v11, v12, v14
	v_add_u32_e32 v12, -5, v6
	v_ashrrev_i32_e32 v13, 31, v12
	v_lshlrev_b64 v[12:13], 6, v[12:13]
	v_div_fixup_f32 v3, v11, v4, v3
	v_lshl_add_u64 v[12:13], v[146:147], 0, v[12:13]
	global_store_dword v[12:13], v3, off
.LBB0_1202:
	s_or_b64 exec, exec, s[22:23]
	v_or_b32_e32 v3, v226, v162
	v_lshlrev_b32_e32 v3, 2, v3
	ds_bpermute_b32 v3, v3, v34
	s_waitcnt lgkmcnt(0)
	v_fmac_f32_e32 v7, v5, v3
	ds_bpermute_b32 v3, v2, v7
	s_waitcnt lgkmcnt(0)
	v_max_f32_e32 v3, v3, v3
	v_max_f32_e32 v3, v7, v3
	s_nop 1
	v_mov_b32_dpp v4, v3 quad_perm:[2,3,0,1] row_mask:0xf bank_mask:0xf
	s_waitcnt lgkmcnt(0)
	v_max_f32_e32 v4, v4, v4
	v_max_f32_e32 v3, v3, v4
	s_nop 1
	v_mov_b32_dpp v4, v3 row_shl:4 row_mask:0xf bank_mask:0x5
	v_mov_b32_dpp v4, v3 row_shr:4 row_mask:0xf bank_mask:0xa
	s_waitcnt lgkmcnt(0)
	v_max_f32_e32 v4, v4, v4
	v_max_f32_e32 v3, v3, v4
	s_nop 1
	v_mov_b32_dpp v4, v3 row_shl:8 row_mask:0xf bank_mask:0x3
	v_mov_b32_dpp v4, v3 row_shr:8 row_mask:0xf bank_mask:0xc
	s_waitcnt lgkmcnt(0)
	v_max_f32_e32 v4, v4, v4
	v_max_f32_e32 v3, v3, v4
	v_sub_f32_e32 v3, v7, v3
	v_mul_f32_e32 v3, 0x3fb8aa3b, v3
	v_exp_f32_e32 v3, v3
	ds_bpermute_b32 v2, v2, v3
	s_waitcnt lgkmcnt(0)
	v_add_f32_e32 v2, v3, v2
	s_nop 1
	v_mov_b32_dpp v4, v2 quad_perm:[2,3,0,1] row_mask:0xf bank_mask:0xf
	s_waitcnt lgkmcnt(0)
	v_add_f32_e32 v2, v2, v4
	s_nop 1
	v_mov_b32_dpp v4, v2 row_shl:4 row_mask:0xf bank_mask:0x5
	v_mov_b32_dpp v4, v2 row_shr:4 row_mask:0xf bank_mask:0xa
	s_waitcnt lgkmcnt(0)
	v_add_f32_e32 v2, v2, v4
	s_nop 1
	v_mov_b32_dpp v4, v2 row_shl:8 row_mask:0xf bank_mask:0x3
	v_mov_b32_dpp v4, v2 row_shr:8 row_mask:0xf bank_mask:0xc
	s_and_saveexec_b64 s[22:23], s[4:5]
	s_cbranch_execz .LBB0_1189
	s_waitcnt lgkmcnt(0)
	v_add_f32_e32 v2, v2, v4
	v_div_scale_f32 v4, s[26:27], v2, v2, v3
	v_rcp_f32_e32 v5, v4
	v_div_scale_f32 v7, vcc, v3, v2, v3
	v_fma_f32 v8, -v4, v5, 1.0
	v_fmac_f32_e32 v5, v8, v5
	v_mul_f32_e32 v8, v7, v5
	v_fma_f32 v9, -v4, v8, v7
	v_fmac_f32_e32 v8, v9, v5
	v_fma_f32 v4, -v4, v8, v7
	v_div_fmas_f32 v4, v4, v5, v8
	v_div_fixup_f32 v4, v4, v2, v3
	v_add_u32_e32 v2, -4, v6
	v_ashrrev_i32_e32 v3, 31, v2
	v_lshlrev_b64 v[2:3], 6, v[2:3]
	v_lshl_add_u64 v[2:3], v[146:147], 0, v[2:3]
	global_store_dword v[2:3], v4, off
	s_branch .LBB0_1189

; __device__ __forceinline__ float* xrow_ptr(float* xl, float* xc, int b, int t) { return (t < SEQ) ? xl + ((size_t)(b * SEQ + t)) * DM : xc + ((size_t)(b * CTXL + (t - SEQ))) * DM; }
; #define xl OUTP(launder(kargs))
; __device__ __forceinline__ void norm2_block(float* xl, float* xc, const float* MOD, const float* gn, const float* WP, bf16_t* H, float* AFF, int L, int row0, int nrows, int lane) {
;     ...
;     const int b = row0 / TPS, t0 = row0 - b * TPS; const int s_ = (t0 >= SEQ) ? 8 : b;
;     if (L == 3 && t0 >= SEQ) return;
;     const int rl = (r16 < nrows) ? r16 : r16 - nrows;
;     const float* xr = xrow_ptr(xl, xc, b, t0 + rl) + 4 * kq;
;     const float* wp = WP + s_ * 16384 + (kq * 16 + r16) * 4;
;     f32x4 acc = {0.f, 0.f, 0.f, 0.f}; float sq = 0.f;
;     f32x4 xa[8], wb[8];
; #pragma unroll
;     for (int q = 0; q < 8; ++q) { xa[q] = *(const f32x4*)(xr + 16 * q); wb[q] = *(const f32x4*)(wp + 256 * q); }
; #pragma unroll
;     for (int g = 0; g < 8; ++g) {
;         f32x4 xn[8], wn[8];
;         if (g < 7) {
; #pragma unroll
;             for (int q = 0; q < 8; ++q) { xn[q] = *(const f32x4*)(xr + 16 * (8 * (g + 1) + q)); wn[q] = *(const f32x4*)(wp + 256 * (8 * (g + 1) + q)); } }
; #pragma unroll
;         for (int q = 0; q < 8; ++q) {
;             sq += (xa[q][0] * xa[q][0] + xa[q][1] * xa[q][1]) + (xa[q][2] * xa[q][2] + xa[q][3] * xa[q][3]);
; #pragma unroll
;             for (int i = 0; i < 4; ++i) acc = __builtin_amdgcn_mfma_f32_16x16x4f32(xa[q][i], wb[q][i], acc, 0, 0, 0); }
.LBB0_1207:
	s_or_b64 exec, exec, s[14:15]
	v_ashrrev_i32_e32 v3, 31, v2
	s_and_b64 s[10:11], s[10:11], exec
	v_lshlrev_b64 v[2:3], 12, v[2:3]
	s_cselect_b32 s5, 8, s5
	v_lshl_add_u64 v[2:3], v[4:5], 0, v[2:3]
	v_lshlrev_b32_e32 v194, 2, v142
	v_lshl_add_u64 v[154:155], v[2:3], 0, v[194:195]
	s_lshl_b32 s38, s5, 14
	v_lshl_add_u64 v[156:157], s[38:39], 2, v[144:145]
	global_load_dwordx4 v[122:125], v[154:155], off
	global_load_dwordx4 v[128:131], v[156:157], off
	global_load_dwordx4 v[114:117], v[154:155], off offset:64
	global_load_dwordx4 v[118:121], v[156:157], off offset:1024
	global_load_dwordx4 v[102:105], v[154:155], off offset:128
	global_load_dwordx4 v[106:109], v[156:157], off offset:2048
	global_load_dwordx4 v[86:89], v[154:155], off offset:192
	global_load_dwordx4 v[90:93], v[156:157], off offset:3072
	global_load_dwordx4 v[66:69], v[154:155], off offset:256
	s_movk_i32 s10, 0x1000
	v_add_co_u32_e32 v2, vcc, s10, v156
	s_movk_i32 s10, 0x2000
	s_nop 0
	v_addc_co_u32_e32 v3, vcc, 0, v157, vcc
	v_add_co_u32_e32 v4, vcc, s10, v156
	s_movk_i32 s10, 0x3000
	s_nop 0
	v_addc_co_u32_e32 v5, vcc, 0, v157, vcc
	global_load_dwordx4 v[74:77], v[4:5], off offset:-4096
	global_load_dwordx4 v[50:53], v[154:155], off offset:320
	global_load_dwordx4 v[54:57], v[2:3], off offset:1024
	global_load_dwordx4 v[34:37], v[154:155], off offset:384
	global_load_dwordx4 v[38:41], v[2:3], off offset:2048
	global_load_dwordx4 v[18:21], v[154:155], off offset:448
	global_load_dwordx4 v[22:25], v[2:3], off offset:3072
	global_load_dwordx4 v[98:101], v[154:155], off offset:512
	global_load_dwordx4 v[110:113], v[4:5], off
	global_load_dwordx4 v[82:85], v[154:155], off offset:576
	global_load_dwordx4 v[94:97], v[4:5], off offset:1024
	global_load_dwordx4 v[70:73], v[154:155], off offset:640
	global_load_dwordx4 v[78:81], v[4:5], off offset:2048
	global_load_dwordx4 v[58:61], v[154:155], off offset:704
	global_load_dwordx4 v[62:65], v[4:5], off offset:3072
	global_load_dwordx4 v[42:45], v[154:155], off offset:768
	v_add_co_u32_e32 v6, vcc, s10, v156
	s_movk_i32 s10, 0x6000
	s_nop 0
	v_addc_co_u32_e32 v7, vcc, 0, v157, vcc
	v_add_co_u32_e32 v126, vcc, s80, v156
	v_mov_b32_e32 v153, v195
	s_nop 0
	v_addc_co_u32_e32 v127, vcc, 0, v157, vcc
	global_load_dwordx4 v[46:49], v[126:127], off offset:-4096
	global_load_dwordx4 v[26:29], v[154:155], off offset:832
	global_load_dwordx4 v[30:33], v[6:7], off offset:1024
	global_load_dwordx4 v[10:13], v[154:155], off offset:896
	global_load_dwordx4 v[14:17], v[6:7], off offset:2048
	global_load_dwordx4 v[2:5], v[154:155], off offset:960
	s_nop 0
	global_load_dwordx4 v[6:9], v[6:7], off offset:3072
	s_waitcnt vmcnt(31)
	v_mul_f32_e32 v132, v123, v123
	v_mul_f32_e32 v133, v125, v125
	v_fmac_f32_e32 v132, v122, v122
	v_fmac_f32_e32 v133, v124, v124
	v_add_f32_e32 v136, v132, v133
	s_waitcnt vmcnt(30)
	v_mfma_f32_16x16x4_f32 v[132:135], v122, v128, 0
	s_waitcnt vmcnt(29)
	v_mul_f32_e32 v128, v115, v115
	v_fmac_f32_e32 v128, v114, v114
	v_mfma_f32_16x16x4_f32 v[132:135], v123, v129, v[132:135]
	v_mul_f32_e32 v129, v117, v117
	v_fmac_f32_e32 v129, v116, v116
	v_add_f32_e32 v128, v128, v129
	v_mfma_f32_16x16x4_f32 v[132:135], v124, v130, v[132:135]
	v_mfma_f32_16x16x4_f32 v[122:125], v125, v131, v[132:135]
	s_waitcnt vmcnt(28)
	v_mfma_f32_16x16x4_f32 v[122:125], v114, v118, v[122:125]
	v_add_f32_e32 v118, v136, v128
	v_mfma_f32_16x16x4_f32 v[122:125], v115, v119, v[122:125]
	s_waitcnt vmcnt(27)
	v_mul_f32_e32 v119, v103, v103
	v_fmac_f32_e32 v119, v102, v102
	v_mfma_f32_16x16x4_f32 v[122:125], v116, v120, v[122:125]
	v_mul_f32_e32 v120, v105, v105
	v_fmac_f32_e32 v120, v104, v104
	v_add_f32_e32 v119, v119, v120
	v_mfma_f32_16x16x4_f32 v[114:117], v117, v121, v[122:125]
	s_waitcnt vmcnt(26)
	v_mfma_f32_16x16x4_f32 v[114:117], v102, v106, v[114:117]
	v_add_f32_e32 v106, v118, v119
	v_mfma_f32_16x16x4_f32 v[114:117], v103, v107, v[114:117]
	s_waitcnt vmcnt(25)
	v_mul_f32_e32 v107, v87, v87
	v_fmac_f32_e32 v107, v86, v86
	v_mfma_f32_16x16x4_f32 v[114:117], v104, v108, v[114:117]
	v_mul_f32_e32 v108, v89, v89
	v_fmac_f32_e32 v108, v88, v88
	v_add_f32_e32 v107, v107, v108
	v_mfma_f32_16x16x4_f32 v[102:105], v105, v109, v[114:117]
	s_waitcnt vmcnt(24)
	v_mfma_f32_16x16x4_f32 v[102:105], v86, v90, v[102:105]
	v_add_f32_e32 v90, v106, v107
	v_mfma_f32_16x16x4_f32 v[102:105], v87, v91, v[102:105]
	s_waitcnt vmcnt(23)
	v_mul_f32_e32 v91, v67, v67
	v_fmac_f32_e32 v91, v66, v66
	v_mfma_f32_16x16x4_f32 v[102:105], v88, v92, v[102:105]
	v_mul_f32_e32 v92, v69, v69
	v_fmac_f32_e32 v92, v68, v68
	v_add_f32_e32 v91, v91, v92
	v_mfma_f32_16x16x4_f32 v[86:89], v89, v93, v[102:105]
	s_waitcnt vmcnt(22)
	v_mfma_f32_16x16x4_f32 v[86:89], v66, v74, v[86:89]
	v_add_f32_e32 v74, v90, v91
	v_mfma_f32_16x16x4_f32 v[86:89], v67, v75, v[86:89]
	s_waitcnt vmcnt(21)
	v_mul_f32_e32 v75, v51, v51
	v_fmac_f32_e32 v75, v50, v50
	v_mfma_f32_16x16x4_f32 v[86:89], v68, v76, v[86:89]
	v_mul_f32_e32 v76, v53, v53
	v_fmac_f32_e32 v76, v52, v52
	v_add_f32_e32 v75, v75, v76
	v_mfma_f32_16x16x4_f32 v[66:69], v69, v77, v[86:89]
	s_waitcnt vmcnt(20)
	v_mfma_f32_16x16x4_f32 v[66:69], v50, v54, v[66:69]
	v_add_f32_e32 v54, v74, v75
	v_mfma_f32_16x16x4_f32 v[66:69], v51, v55, v[66:69]
	s_waitcnt vmcnt(19)
; __device__ __forceinline__ void norm2_block(float* xl, float* xc, const float* MOD, const float* gn, const float* WP, bf16_t* H, float* AFF, int L, int row0, int nrows, int lane) {
;     ...
;     for (int q = 0; q < 8; ++q) { xa[q] = *(const f32x4*)(xr + 16 * q); wb[q] = *(const f32x4*)(wp + 256 * q); }
; #pragma unroll
;     for (int g = 0; g < 8; ++g) {
;         f32x4 xn[8], wn[8];
;         if (g < 7) {
; #pragma unroll
;             for (int q = 0; q < 8; ++q) { xn[q] = *(const f32x4*)(xr + 16 * (8 * (g + 1) + q)); wn[q] = *(const f32x4*)(wp + 256 * (8 * (g + 1) + q)); } }
; #pragma unroll
;         for (int q = 0; q < 8; ++q) {
;             sq += (xa[q][0] * xa[q][0] + xa[q][1] * xa[q][1]) + (xa[q][2] * xa[q][2] + xa[q][3] * xa[q][3]);
; #pragma unroll
;             for (int i = 0; i < 4; ++i) acc = __builtin_amdgcn_mfma_f32_16x16x4f32(xa[q][i], wb[q][i], acc, 0, 0, 0); }
;         if (g < 7) {
; #pragma unroll
;             for (int q = 0; q < 8; ++q) { xa[q] = xn[q]; wb[q] = wn[q]; } }
;     }
	v_mul_f32_e32 v55, v35, v35
	v_fmac_f32_e32 v55, v34, v34
	v_mfma_f32_16x16x4_f32 v[66:69], v52, v56, v[66:69]
	v_mul_f32_e32 v56, v37, v37
	v_fmac_f32_e32 v56, v36, v36
	v_add_f32_e32 v55, v55, v56
	v_mfma_f32_16x16x4_f32 v[50:53], v53, v57, v[66:69]
	global_load_dwordx4 v[134:137], v[154:155], off offset:1024
	global_load_dwordx4 v[138:141], v[126:127], off
	global_load_dwordx4 v[118:121], v[154:155], off offset:1088
	global_load_dwordx4 v[122:125], v[126:127], off offset:1024
	global_load_dwordx4 v[102:105], v[154:155], off offset:1152
	global_load_dwordx4 v[106:109], v[126:127], off offset:2048
	global_load_dwordx4 v[86:89], v[154:155], off offset:1216
	global_load_dwordx4 v[90:93], v[126:127], off offset:3072
	global_load_dwordx4 v[66:69], v[154:155], off offset:1280
	s_waitcnt vmcnt(24)
	v_mul_f32_e32 v126, v99, v99
	v_mul_f32_e32 v127, v101, v101
	v_fmac_f32_e32 v126, v98, v98
	v_fmac_f32_e32 v127, v100, v100
	v_add_f32_e32 v126, v126, v127
	v_mfma_f32_16x16x4_f32 v[50:53], v34, v38, v[50:53]
	v_add_f32_e32 v38, v54, v55
	v_mfma_f32_16x16x4_f32 v[50:53], v35, v39, v[50:53]
	v_mul_f32_e32 v39, v19, v19
	v_fmac_f32_e32 v39, v18, v18
	v_mfma_f32_16x16x4_f32 v[50:53], v36, v40, v[50:53]
	v_mul_f32_e32 v40, v21, v21
	v_fmac_f32_e32 v40, v20, v20
	v_add_f32_e32 v39, v39, v40
	v_add_f32_e32 v128, v38, v39
	v_mfma_f32_16x16x4_f32 v[34:37], v37, v41, v[50:53]
	v_mfma_f32_16x16x4_f32 v[34:37], v18, v22, v[34:37]
	v_add_co_u32_e32 v22, vcc, s77, v156
	v_mfma_f32_16x16x4_f32 v[34:37], v19, v23, v[34:37]
	s_nop 0
	v_addc_co_u32_e32 v23, vcc, 0, v157, vcc
	v_add_co_u32_e32 v158, vcc, s10, v156
	s_movk_i32 s10, 0x7000
	s_nop 0
	v_addc_co_u32_e32 v159, vcc, 0, v157, vcc
	v_mfma_f32_16x16x4_f32 v[34:37], v20, v24, v[34:37]
	v_mfma_f32_16x16x4_f32 v[114:117], v21, v25, v[34:37]
	global_load_dwordx4 v[74:77], v[158:159], off offset:-4096
	global_load_dwordx4 v[50:53], v[154:155], off offset:1344
	global_load_dwordx4 v[54:57], v[22:23], off offset:1024
	s_nop 5
	global_load_dwordx4 v[34:37], v[154:155], off offset:1408
	global_load_dwordx4 v[38:41], v[22:23], off offset:2048
	global_load_dwordx4 v[18:21], v[154:155], off offset:1472
	s_nop 0
	global_load_dwordx4 v[22:25], v[22:23], off offset:3072
	s_waitcnt vmcnt(30)
	v_mfma_f32_16x16x4_f32 v[114:117], v98, v110, v[114:117]
	v_add_f32_e32 v110, v128, v126
	v_mfma_f32_16x16x4_f32 v[114:117], v99, v111, v[114:117]
	s_waitcnt vmcnt(29)
	v_mul_f32_e32 v111, v83, v83
	v_fmac_f32_e32 v111, v82, v82
	v_mfma_f32_16x16x4_f32 v[114:117], v100, v112, v[114:117]
	v_mul_f32_e32 v112, v85, v85
	v_fmac_f32_e32 v112, v84, v84
	v_add_f32_e32 v111, v111, v112
	v_mfma_f32_16x16x4_f32 v[98:101], v101, v113, v[114:117]
	s_waitcnt vmcnt(28)
	v_mfma_f32_16x16x4_f32 v[98:101], v82, v94, v[98:101]
	v_add_f32_e32 v94, v110, v111
	v_mfma_f32_16x16x4_f32 v[98:101], v83, v95, v[98:101]
	s_waitcnt vmcnt(27)
	v_mul_f32_e32 v95, v71, v71
	v_fmac_f32_e32 v95, v70, v70
	v_mfma_f32_16x16x4_f32 v[98:101], v84, v96, v[98:101]
	v_mul_f32_e32 v96, v73, v73
	v_fmac_f32_e32 v96, v72, v72
	v_add_f32_e32 v95, v95, v96
	v_mfma_f32_16x16x4_f32 v[82:85], v85, v97, v[98:101]
	s_waitcnt vmcnt(26)
	v_mfma_f32_16x16x4_f32 v[82:85], v70, v78, v[82:85]
	v_add_f32_e32 v78, v94, v95
	v_mfma_f32_16x16x4_f32 v[82:85], v71, v79, v[82:85]
	s_waitcnt vmcnt(25)
	v_mul_f32_e32 v79, v59, v59
	v_fmac_f32_e32 v79, v58, v58
	v_mfma_f32_16x16x4_f32 v[82:85], v72, v80, v[82:85]
	v_mul_f32_e32 v80, v61, v61
	v_fmac_f32_e32 v80, v60, v60
	v_add_f32_e32 v79, v79, v80
	v_mfma_f32_16x16x4_f32 v[70:73], v73, v81, v[82:85]
	s_waitcnt vmcnt(24)
	v_mfma_f32_16x16x4_f32 v[70:73], v58, v62, v[70:73]
	v_add_f32_e32 v62, v78, v79
	v_mfma_f32_16x16x4_f32 v[70:73], v59, v63, v[70:73]
	s_waitcnt vmcnt(23)
	v_mul_f32_e32 v63, v43, v43
	v_fmac_f32_e32 v63, v42, v42
	v_mfma_f32_16x16x4_f32 v[70:73], v60, v64, v[70:73]
	v_mul_f32_e32 v64, v45, v45
	v_fmac_f32_e32 v64, v44, v44
	v_add_f32_e32 v63, v63, v64
	v_mfma_f32_16x16x4_f32 v[58:61], v61, v65, v[70:73]
	s_waitcnt vmcnt(22)
	v_mfma_f32_16x16x4_f32 v[58:61], v42, v46, v[58:61]
	v_add_f32_e32 v46, v62, v63
	v_mfma_f32_16x16x4_f32 v[58:61], v43, v47, v[58:61]
	s_waitcnt vmcnt(21)
	v_mul_f32_e32 v47, v27, v27
	v_fmac_f32_e32 v47, v26, v26
	v_mfma_f32_16x16x4_f32 v[58:61], v44, v48, v[58:61]
	v_mul_f32_e32 v48, v29, v29
	v_fmac_f32_e32 v48, v28, v28
	v_add_f32_e32 v47, v47, v48
	v_mfma_f32_16x16x4_f32 v[42:45], v45, v49, v[58:61]
	global_load_dwordx4 v[126:129], v[154:155], off offset:1536
	global_load_dwordx4 v[130:133], v[158:159], off
	global_load_dwordx4 v[110:113], v[154:155], off offset:1600
	global_load_dwordx4 v[114:117], v[158:159], off offset:1024
	global_load_dwordx4 v[94:97], v[154:155], off offset:1664
	global_load_dwordx4 v[98:101], v[158:159], off offset:2048
	global_load_dwordx4 v[78:81], v[154:155], off offset:1728
	global_load_dwordx4 v[82:85], v[158:159], off offset:3072
	global_load_dwordx4 v[58:61], v[154:155], off offset:1792
	s_waitcnt vmcnt(29)
	v_mfma_f32_16x16x4_f32 v[42:45], v26, v30, v[42:45]
	v_add_f32_e32 v30, v46, v47
	v_mfma_f32_16x16x4_f32 v[42:45], v27, v31, v[42:45]
	s_waitcnt vmcnt(28)
	v_mul_f32_e32 v31, v11, v11
	v_fmac_f32_e32 v31, v10, v10
	v_mfma_f32_16x16x4_f32 v[42:45], v28, v32, v[42:45]
	v_mul_f32_e32 v32, v13, v13
	v_fmac_f32_e32 v32, v12, v12
	v_add_f32_e32 v31, v31, v32
	v_mfma_f32_16x16x4_f32 v[26:29], v29, v33, v[42:45]
	s_waitcnt vmcnt(27)
	v_mfma_f32_16x16x4_f32 v[26:29], v10, v14, v[26:29]
	v_add_f32_e32 v14, v30, v31
	v_mfma_f32_16x16x4_f32 v[26:29], v11, v15, v[26:29]
	s_waitcnt vmcnt(26)
; __device__ __forceinline__ void norm2_block(float* xl, float* xc, const float* MOD, const float* gn, const float* WP, bf16_t* H, float* AFF, int L, int row0, int nrows, int lane) {
;     ...
;     for (int q = 0; q < 8; ++q) { xa[q] = *(const f32x4*)(xr + 16 * q); wb[q] = *(const f32x4*)(wp + 256 * q); }
; #pragma unroll
;     for (int g = 0; g < 8; ++g) {
;         f32x4 xn[8], wn[8];
;         if (g < 7) {
; #pragma unroll
;             for (int q = 0; q < 8; ++q) { xn[q] = *(const f32x4*)(xr + 16 * (8 * (g + 1) + q)); wn[q] = *(const f32x4*)(wp + 256 * (8 * (g + 1) + q)); } }
; #pragma unroll
;         for (int q = 0; q < 8; ++q) {
;             sq += (xa[q][0] * xa[q][0] + xa[q][1] * xa[q][1]) + (xa[q][2] * xa[q][2] + xa[q][3] * xa[q][3]);
; #pragma unroll
;             for (int i = 0; i < 4; ++i) acc = __builtin_amdgcn_mfma_f32_16x16x4f32(xa[q][i], wb[q][i], acc, 0, 0, 0); }
;         if (g < 7) {
; #pragma unroll
;             for (int q = 0; q < 8; ++q) { xa[q] = xn[q]; wb[q] = wn[q]; } }
;     }
	v_mul_f32_e32 v15, v3, v3
	v_fmac_f32_e32 v15, v2, v2
	v_mfma_f32_16x16x4_f32 v[26:29], v12, v16, v[26:29]
	v_mul_f32_e32 v16, v5, v5
	v_fmac_f32_e32 v16, v4, v4
	v_add_f32_e32 v15, v15, v16
	v_add_f32_e32 v62, v14, v15
	v_mfma_f32_16x16x4_f32 v[10:13], v13, v17, v[26:29]
	s_waitcnt vmcnt(25)
	v_mfma_f32_16x16x4_f32 v[10:13], v2, v6, v[10:13]
	v_mfma_f32_16x16x4_f32 v[10:13], v3, v7, v[10:13]
	v_mfma_f32_16x16x4_f32 v[10:13], v4, v8, v[10:13]
	v_add_co_u32_e32 v4, vcc, s10, v156
	s_mov_b32 s10, 0xb000
	v_mfma_f32_16x16x4_f32 v[10:13], v5, v9, v[10:13]
	v_addc_co_u32_e32 v5, vcc, 0, v157, vcc
	v_add_co_u32_e32 v2, vcc, s81, v156
	s_nop 1
	v_addc_co_u32_e32 v3, vcc, 0, v157, vcc
	s_waitcnt vmcnt(23)
	v_mfma_f32_16x16x4_f32 v[10:13], v134, v138, v[10:13]
	global_load_dwordx4 v[70:73], v[2:3], off offset:-4096
	global_load_dwordx4 v[42:45], v[154:155], off offset:1856
	global_load_dwordx4 v[46:49], v[4:5], off offset:1024
	global_load_dwordx4 v[26:29], v[154:155], off offset:1920
	global_load_dwordx4 v[30:33], v[4:5], off offset:2048
	global_load_dwordx4 v[6:9], v[154:155], off offset:1984
	global_load_dwordx4 v[14:17], v[4:5], off offset:3072
	v_mul_f32_e32 v4, v135, v135
	v_mul_f32_e32 v5, v137, v137
	v_fmac_f32_e32 v4, v134, v134
	v_fmac_f32_e32 v5, v136, v136
	v_add_f32_e32 v4, v4, v5
	v_add_f32_e32 v4, v62, v4
	v_mfma_f32_16x16x4_f32 v[10:13], v135, v139, v[10:13]
	s_waitcnt vmcnt(29)
	v_mul_f32_e32 v5, v119, v119
	v_mul_f32_e32 v62, v121, v121
	v_fmac_f32_e32 v5, v118, v118
	v_fmac_f32_e32 v62, v120, v120
	v_add_f32_e32 v5, v5, v62
	v_add_f32_e32 v4, v4, v5
	s_waitcnt vmcnt(27)
	v_mul_f32_e32 v5, v103, v103
	v_mfma_f32_16x16x4_f32 v[10:13], v136, v140, v[10:13]
	v_mul_f32_e32 v62, v105, v105
	v_fmac_f32_e32 v5, v102, v102
	v_fmac_f32_e32 v62, v104, v104
	v_add_f32_e32 v5, v5, v62
	v_add_f32_e32 v4, v4, v5
	s_waitcnt vmcnt(25)
	v_mul_f32_e32 v5, v87, v87
	v_mul_f32_e32 v62, v89, v89
	v_mfma_f32_16x16x4_f32 v[10:13], v137, v141, v[10:13]
	v_fmac_f32_e32 v5, v86, v86
	v_fmac_f32_e32 v62, v88, v88
	v_add_f32_e32 v5, v5, v62
	v_add_f32_e32 v4, v4, v5
	s_waitcnt vmcnt(23)
	v_mul_f32_e32 v5, v67, v67
	v_mul_f32_e32 v62, v69, v69
	v_fmac_f32_e32 v5, v66, v66
	v_mfma_f32_16x16x4_f32 v[10:13], v118, v122, v[10:13]
	v_fmac_f32_e32 v62, v68, v68
	v_add_f32_e32 v5, v5, v62
	v_add_f32_e32 v4, v4, v5
	s_waitcnt vmcnt(21)
	v_mul_f32_e32 v5, v51, v51
	v_mul_f32_e32 v62, v53, v53
	v_fmac_f32_e32 v5, v50, v50
	v_fmac_f32_e32 v62, v52, v52
	v_mfma_f32_16x16x4_f32 v[10:13], v119, v123, v[10:13]
	v_add_f32_e32 v5, v5, v62
	v_add_f32_e32 v4, v4, v5
	s_waitcnt vmcnt(19)
	v_mul_f32_e32 v5, v35, v35
	v_fmac_f32_e32 v5, v34, v34
	s_waitcnt vmcnt(15)
	v_mul_f32_e32 v138, v129, v129
	v_fmac_f32_e32 v138, v128, v128
	v_mfma_f32_16x16x4_f32 v[10:13], v120, v124, v[10:13]
	v_mfma_f32_16x16x4_f32 v[10:13], v121, v125, v[10:13]
	v_mfma_f32_16x16x4_f32 v[10:13], v102, v106, v[10:13]
	v_mfma_f32_16x16x4_f32 v[10:13], v103, v107, v[10:13]
	v_mfma_f32_16x16x4_f32 v[10:13], v104, v108, v[10:13]
	v_mfma_f32_16x16x4_f32 v[10:13], v105, v109, v[10:13]
	v_mfma_f32_16x16x4_f32 v[10:13], v86, v90, v[10:13]
	v_mfma_f32_16x16x4_f32 v[10:13], v87, v91, v[10:13]
	v_mfma_f32_16x16x4_f32 v[10:13], v88, v92, v[10:13]
	v_mfma_f32_16x16x4_f32 v[10:13], v89, v93, v[10:13]
	v_mfma_f32_16x16x4_f32 v[10:13], v66, v74, v[10:13]
	v_mfma_f32_16x16x4_f32 v[10:13], v67, v75, v[10:13]
	v_mfma_f32_16x16x4_f32 v[10:13], v68, v76, v[10:13]
	v_mfma_f32_16x16x4_f32 v[10:13], v69, v77, v[10:13]
	global_load_dwordx4 v[122:125], v[154:155], off offset:2048
	global_load_dwordx4 v[134:137], v[2:3], off
	global_load_dwordx4 v[106:109], v[154:155], off offset:2112
	global_load_dwordx4 v[118:121], v[2:3], off offset:1024
	global_load_dwordx4 v[90:93], v[154:155], off offset:2176
	global_load_dwordx4 v[102:105], v[2:3], off offset:2048
	global_load_dwordx4 v[74:77], v[154:155], off offset:2240
	global_load_dwordx4 v[86:89], v[2:3], off offset:3072
	global_load_dwordx4 v[62:65], v[154:155], off offset:2304
	v_mfma_f32_16x16x4_f32 v[10:13], v50, v54, v[10:13]
	v_mul_f32_e32 v50, v37, v37
	v_fmac_f32_e32 v50, v36, v36
	v_add_f32_e32 v5, v5, v50
	v_add_f32_e32 v4, v4, v5
	v_mul_f32_e32 v5, v19, v19
	v_fmac_f32_e32 v5, v18, v18
	v_mfma_f32_16x16x4_f32 v[10:13], v51, v55, v[10:13]
	v_mfma_f32_16x16x4_f32 v[10:13], v52, v56, v[10:13]
	v_mfma_f32_16x16x4_f32 v[10:13], v53, v57, v[10:13]
	v_mfma_f32_16x16x4_f32 v[10:13], v34, v38, v[10:13]
	v_mul_f32_e32 v34, v21, v21
	v_fmac_f32_e32 v34, v20, v20
	v_add_f32_e32 v5, v5, v34
	v_mfma_f32_16x16x4_f32 v[10:13], v35, v39, v[10:13]
	v_mfma_f32_16x16x4_f32 v[10:13], v36, v40, v[10:13]
	v_mfma_f32_16x16x4_f32 v[10:13], v37, v41, v[10:13]
	v_mfma_f32_16x16x4_f32 v[10:13], v18, v22, v[10:13]
	v_mfma_f32_16x16x4_f32 v[10:13], v19, v23, v[10:13]
	v_mfma_f32_16x16x4_f32 v[10:13], v20, v24, v[10:13]
	v_add_f32_e32 v24, v4, v5
	v_mfma_f32_16x16x4_f32 v[20:23], v21, v25, v[10:13]
	v_mul_f32_e32 v25, v127, v127
	v_fmac_f32_e32 v25, v126, v126
	v_add_f32_e32 v25, v25, v138
	v_add_f32_e32 v24, v24, v25
	s_waitcnt vmcnt(22)
	v_mul_f32_e32 v25, v111, v111
	v_fmac_f32_e32 v25, v110, v110
	s_waitcnt vmcnt(8)
; __device__ __forceinline__ void norm2_block(float* xl, float* xc, const float* MOD, const float* gn, const float* WP, bf16_t* H, float* AFF, int L, int row0, int nrows, int lane) {
;     ...
;     for (int q = 0; q < 8; ++q) { xa[q] = *(const f32x4*)(xr + 16 * q); wb[q] = *(const f32x4*)(wp + 256 * q); }
; #pragma unroll
;     for (int g = 0; g < 8; ++g) {
;         f32x4 xn[8], wn[8];
;         if (g < 7) {
; #pragma unroll
;             for (int q = 0; q < 8; ++q) { xn[q] = *(const f32x4*)(xr + 16 * (8 * (g + 1) + q)); wn[q] = *(const f32x4*)(wp + 256 * (8 * (g + 1) + q)); } }
; #pragma unroll
;         for (int q = 0; q < 8; ++q) {
;             sq += (xa[q][0] * xa[q][0] + xa[q][1] * xa[q][1]) + (xa[q][2] * xa[q][2] + xa[q][3] * xa[q][3]);
; #pragma unroll
;             for (int i = 0; i < 4; ++i) acc = __builtin_amdgcn_mfma_f32_16x16x4f32(xa[q][i], wb[q][i], acc, 0, 0, 0); }
;         if (g < 7) {
; #pragma unroll
;             for (int q = 0; q < 8; ++q) { xa[q] = xn[q]; wb[q] = wn[q]; } }
;     }
	v_mul_f32_e32 v138, v125, v125
	v_mfma_f32_16x16x4_f32 v[20:23], v126, v130, v[20:23]
	v_mul_f32_e32 v126, v113, v113
	v_fmac_f32_e32 v126, v112, v112
	v_add_f32_e32 v25, v25, v126
	v_fmac_f32_e32 v138, v124, v124
	v_add_co_u32_e32 v10, vcc, s93, v156
	v_add_f32_e32 v24, v24, v25
	v_mfma_f32_16x16x4_f32 v[20:23], v127, v131, v[20:23]
	v_addc_co_u32_e32 v11, vcc, 0, v157, vcc
	v_add_co_u32_e32 v18, vcc, s85, v156
	v_mul_f32_e32 v25, v95, v95
	s_nop 0
	v_addc_co_u32_e32 v19, vcc, 0, v157, vcc
	v_mfma_f32_16x16x4_f32 v[20:23], v128, v132, v[20:23]
	global_load_dwordx4 v[66:69], v[18:19], off offset:-4096
	global_load_dwordx4 v[50:53], v[154:155], off offset:2368
	global_load_dwordx4 v[54:57], v[10:11], off offset:1024
	global_load_dwordx4 v[34:37], v[154:155], off offset:2432
	global_load_dwordx4 v[38:41], v[10:11], off offset:2048
	global_load_dwordx4 v[2:5], v[154:155], off offset:2496
	s_nop 0
	global_load_dwordx4 v[10:13], v[10:11], off offset:3072
	v_fmac_f32_e32 v25, v94, v94
	v_mfma_f32_16x16x4_f32 v[20:23], v129, v133, v[20:23]
	v_mul_f32_e32 v133, v123, v123
	v_fmac_f32_e32 v133, v122, v122
	v_add_f32_e32 v133, v133, v138
	v_mfma_f32_16x16x4_f32 v[20:23], v110, v114, v[20:23]
	v_mul_f32_e32 v110, v97, v97
	v_fmac_f32_e32 v110, v96, v96
	v_add_f32_e32 v25, v25, v110
	v_add_f32_e32 v24, v24, v25
	v_mul_f32_e32 v25, v79, v79
	v_fmac_f32_e32 v25, v78, v78
	v_mfma_f32_16x16x4_f32 v[20:23], v111, v115, v[20:23]
	v_mfma_f32_16x16x4_f32 v[20:23], v112, v116, v[20:23]
	v_mfma_f32_16x16x4_f32 v[20:23], v113, v117, v[20:23]
	v_mfma_f32_16x16x4_f32 v[20:23], v94, v98, v[20:23]
	v_mul_f32_e32 v94, v81, v81
	v_fmac_f32_e32 v94, v80, v80
	v_add_f32_e32 v25, v25, v94
	v_add_f32_e32 v24, v24, v25
	v_mul_f32_e32 v25, v59, v59
	v_fmac_f32_e32 v25, v58, v58
	v_mfma_f32_16x16x4_f32 v[20:23], v95, v99, v[20:23]
	v_mfma_f32_16x16x4_f32 v[20:23], v96, v100, v[20:23]
	v_mfma_f32_16x16x4_f32 v[20:23], v97, v101, v[20:23]
	v_mfma_f32_16x16x4_f32 v[20:23], v78, v82, v[20:23]
	v_mul_f32_e32 v78, v61, v61
	v_fmac_f32_e32 v78, v60, v60
	v_add_f32_e32 v25, v25, v78
	v_add_f32_e32 v24, v24, v25
	v_mul_f32_e32 v25, v43, v43
	v_fmac_f32_e32 v25, v42, v42
	v_mfma_f32_16x16x4_f32 v[20:23], v79, v83, v[20:23]
	v_mfma_f32_16x16x4_f32 v[20:23], v80, v84, v[20:23]
	v_mfma_f32_16x16x4_f32 v[20:23], v81, v85, v[20:23]
	v_mfma_f32_16x16x4_f32 v[20:23], v58, v70, v[20:23]
	v_mul_f32_e32 v58, v45, v45
	v_fmac_f32_e32 v58, v44, v44
	v_add_f32_e32 v25, v25, v58
	v_add_f32_e32 v24, v24, v25
	v_mul_f32_e32 v25, v27, v27
	v_fmac_f32_e32 v25, v26, v26
	v_mfma_f32_16x16x4_f32 v[20:23], v59, v71, v[20:23]
	v_mfma_f32_16x16x4_f32 v[20:23], v60, v72, v[20:23]
	v_mfma_f32_16x16x4_f32 v[20:23], v61, v73, v[20:23]
	v_mfma_f32_16x16x4_f32 v[20:23], v42, v46, v[20:23]
	v_mul_f32_e32 v42, v29, v29
	v_fmac_f32_e32 v42, v28, v28
	v_add_f32_e32 v25, v25, v42
	v_add_f32_e32 v24, v24, v25
	v_mul_f32_e32 v25, v7, v7
	v_fmac_f32_e32 v25, v6, v6
	v_mfma_f32_16x16x4_f32 v[20:23], v43, v47, v[20:23]
	v_mfma_f32_16x16x4_f32 v[20:23], v44, v48, v[20:23]
	v_mfma_f32_16x16x4_f32 v[20:23], v45, v49, v[20:23]
	global_load_dwordx4 v[110:113], v[154:155], off offset:2560
	global_load_dwordx4 v[114:117], v[18:19], off
	global_load_dwordx4 v[94:97], v[154:155], off offset:2624
	global_load_dwordx4 v[98:101], v[18:19], off offset:1024
	global_load_dwordx4 v[78:81], v[154:155], off offset:2688
	global_load_dwordx4 v[82:85], v[18:19], off offset:2048
	global_load_dwordx4 v[58:61], v[154:155], off offset:2752
	global_load_dwordx4 v[70:73], v[18:19], off offset:3072
	global_load_dwordx4 v[42:45], v[154:155], off offset:2816
	s_waitcnt vmcnt(8)
	v_mul_f32_e32 v138, v113, v113
	v_mfma_f32_16x16x4_f32 v[20:23], v26, v30, v[20:23]
	v_mul_f32_e32 v26, v9, v9
	v_fmac_f32_e32 v26, v8, v8
	v_add_f32_e32 v25, v25, v26
	v_add_f32_e32 v132, v24, v25
	v_fmac_f32_e32 v138, v112, v112
	v_mfma_f32_16x16x4_f32 v[20:23], v27, v31, v[20:23]
	v_mfma_f32_16x16x4_f32 v[20:23], v28, v32, v[20:23]
	v_mfma_f32_16x16x4_f32 v[20:23], v29, v33, v[20:23]
	v_mfma_f32_16x16x4_f32 v[20:23], v6, v14, v[20:23]
	v_add_co_u32_e32 v14, vcc, s10, v156
	s_mov_b32 s10, 0xd000
	v_mfma_f32_16x16x4_f32 v[20:23], v7, v15, v[20:23]
	v_addc_co_u32_e32 v15, vcc, 0, v157, vcc
	v_add_co_u32_e32 v130, vcc, s84, v156
	s_nop 1
	v_addc_co_u32_e32 v131, vcc, 0, v157, vcc
	v_mfma_f32_16x16x4_f32 v[20:23], v8, v16, v[20:23]
	v_mfma_f32_16x16x4_f32 v[126:129], v9, v17, v[20:23]
	global_load_dwordx4 v[46:49], v[130:131], off offset:-4096
	global_load_dwordx4 v[26:29], v[154:155], off offset:2880
	global_load_dwordx4 v[30:33], v[14:15], off offset:1024
	s_nop 5
	global_load_dwordx4 v[18:21], v[154:155], off offset:2944
	global_load_dwordx4 v[22:25], v[14:15], off offset:2048
	global_load_dwordx4 v[6:9], v[154:155], off offset:3008
	s_nop 0
	global_load_dwordx4 v[14:17], v[14:15], off offset:3072
	v_mfma_f32_16x16x4_f32 v[126:129], v122, v134, v[126:129]
	v_mfma_f32_16x16x4_f32 v[126:129], v123, v135, v[126:129]
	v_mfma_f32_16x16x4_f32 v[126:129], v124, v136, v[126:129]
	v_mfma_f32_16x16x4_f32 v[122:125], v125, v137, v[126:129]
	s_nop 8
	v_mul_f32_e32 v127, v107, v107
	v_mul_f32_e32 v128, v109, v109
	v_fmac_f32_e32 v127, v106, v106
	v_fmac_f32_e32 v128, v108, v108
	v_add_f32_e32 v126, v132, v133
	v_mul_f32_e32 v137, v111, v111
	v_fmac_f32_e32 v137, v110, v110
	v_mfma_f32_16x16x4_f32 v[122:125], v106, v118, v[122:125]
	v_add_f32_e32 v127, v127, v128
	v_add_f32_e32 v118, v126, v127
	v_add_f32_e32 v137, v137, v138
	v_mfma_f32_16x16x4_f32 v[122:125], v107, v119, v[122:125]
	v_mul_f32_e32 v119, v91, v91
	v_fmac_f32_e32 v119, v90, v90
	v_mfma_f32_16x16x4_f32 v[122:125], v108, v120, v[122:125]
; __device__ __forceinline__ void norm2_block(float* xl, float* xc, const float* MOD, const float* gn, const float* WP, bf16_t* H, float* AFF, int L, int row0, int nrows, int lane) {
;     ...
;     for (int q = 0; q < 8; ++q) { xa[q] = *(const f32x4*)(xr + 16 * q); wb[q] = *(const f32x4*)(wp + 256 * q); }
; #pragma unroll
;     for (int g = 0; g < 8; ++g) {
;         f32x4 xn[8], wn[8];
;         if (g < 7) {
; #pragma unroll
;             for (int q = 0; q < 8; ++q) { xn[q] = *(const f32x4*)(xr + 16 * (8 * (g + 1) + q)); wn[q] = *(const f32x4*)(wp + 256 * (8 * (g + 1) + q)); } }
; #pragma unroll
;         for (int q = 0; q < 8; ++q) {
;             sq += (xa[q][0] * xa[q][0] + xa[q][1] * xa[q][1]) + (xa[q][2] * xa[q][2] + xa[q][3] * xa[q][3]);
; #pragma unroll
;             for (int i = 0; i < 4; ++i) acc = __builtin_amdgcn_mfma_f32_16x16x4f32(xa[q][i], wb[q][i], acc, 0, 0, 0); }
;         if (g < 7) {
; #pragma unroll
;             for (int q = 0; q < 8; ++q) { xa[q] = xn[q]; wb[q] = wn[q]; } }
;     }
	v_mul_f32_e32 v120, v93, v93
	v_fmac_f32_e32 v120, v92, v92
	v_add_f32_e32 v119, v119, v120
	v_mfma_f32_16x16x4_f32 v[106:109], v109, v121, v[122:125]
	v_mfma_f32_16x16x4_f32 v[106:109], v90, v102, v[106:109]
	v_add_f32_e32 v102, v118, v119
	v_mfma_f32_16x16x4_f32 v[106:109], v91, v103, v[106:109]
	v_mul_f32_e32 v103, v75, v75
	v_fmac_f32_e32 v103, v74, v74
	v_mfma_f32_16x16x4_f32 v[106:109], v92, v104, v[106:109]
	v_mul_f32_e32 v104, v77, v77
	v_fmac_f32_e32 v104, v76, v76
	v_add_f32_e32 v103, v103, v104
	v_mfma_f32_16x16x4_f32 v[90:93], v93, v105, v[106:109]
	v_mfma_f32_16x16x4_f32 v[90:93], v74, v86, v[90:93]
	v_add_f32_e32 v86, v102, v103
	v_mfma_f32_16x16x4_f32 v[90:93], v75, v87, v[90:93]
	v_mul_f32_e32 v87, v63, v63
	v_fmac_f32_e32 v87, v62, v62
	v_mfma_f32_16x16x4_f32 v[90:93], v76, v88, v[90:93]
	v_mul_f32_e32 v88, v65, v65
	v_fmac_f32_e32 v88, v64, v64
	v_add_f32_e32 v87, v87, v88
	v_mfma_f32_16x16x4_f32 v[74:77], v77, v89, v[90:93]
	v_mfma_f32_16x16x4_f32 v[74:77], v62, v66, v[74:77]
	v_add_f32_e32 v66, v86, v87
	v_mfma_f32_16x16x4_f32 v[74:77], v63, v67, v[74:77]
	v_mul_f32_e32 v67, v51, v51
	v_fmac_f32_e32 v67, v50, v50
	v_mfma_f32_16x16x4_f32 v[74:77], v64, v68, v[74:77]
	v_mul_f32_e32 v68, v53, v53
	v_fmac_f32_e32 v68, v52, v52
	v_add_f32_e32 v67, v67, v68
	v_mfma_f32_16x16x4_f32 v[62:65], v65, v69, v[74:77]
	v_mfma_f32_16x16x4_f32 v[62:65], v50, v54, v[62:65]
	v_add_f32_e32 v54, v66, v67
	v_mfma_f32_16x16x4_f32 v[62:65], v51, v55, v[62:65]
	v_mul_f32_e32 v55, v35, v35
	v_fmac_f32_e32 v55, v34, v34
	v_mfma_f32_16x16x4_f32 v[62:65], v52, v56, v[62:65]
	v_mul_f32_e32 v56, v37, v37
	v_fmac_f32_e32 v56, v36, v36
	v_add_f32_e32 v55, v55, v56
	v_mfma_f32_16x16x4_f32 v[50:53], v53, v57, v[62:65]
	global_load_dwordx4 v[122:125], v[154:155], off offset:3072
	global_load_dwordx4 v[126:129], v[130:131], off
	global_load_dwordx4 v[106:109], v[154:155], off offset:3136
	global_load_dwordx4 v[118:121], v[130:131], off offset:1024
	global_load_dwordx4 v[90:93], v[154:155], off offset:3200
	global_load_dwordx4 v[102:105], v[130:131], off offset:2048
	global_load_dwordx4 v[74:77], v[154:155], off offset:3264
	global_load_dwordx4 v[86:89], v[130:131], off offset:3072
	global_load_dwordx4 v[62:65], v[154:155], off offset:3328
	v_mfma_f32_16x16x4_f32 v[50:53], v34, v38, v[50:53]
	v_add_f32_e32 v38, v54, v55
	v_mfma_f32_16x16x4_f32 v[50:53], v35, v39, v[50:53]
	v_mul_f32_e32 v39, v3, v3
	v_fmac_f32_e32 v39, v2, v2
	v_mfma_f32_16x16x4_f32 v[50:53], v36, v40, v[50:53]
	v_mul_f32_e32 v40, v5, v5
	v_fmac_f32_e32 v40, v4, v4
	v_add_f32_e32 v39, v39, v40
	v_add_f32_e32 v136, v38, v39
	v_mfma_f32_16x16x4_f32 v[34:37], v37, v41, v[50:53]
	v_mfma_f32_16x16x4_f32 v[34:37], v2, v10, v[34:37]
	v_add_co_u32_e32 v10, vcc, s10, v156
	s_mov_b32 s10, 0xf000
	v_mfma_f32_16x16x4_f32 v[34:37], v3, v11, v[34:37]
	v_addc_co_u32_e32 v11, vcc, 0, v157, vcc
	v_add_co_u32_e32 v130, vcc, s86, v156
	s_nop 1
	v_addc_co_u32_e32 v131, vcc, 0, v157, vcc
	v_mfma_f32_16x16x4_f32 v[34:37], v4, v12, v[34:37]
	v_mfma_f32_16x16x4_f32 v[132:135], v5, v13, v[34:37]
	global_load_dwordx4 v[66:69], v[130:131], off offset:-4096
	global_load_dwordx4 v[50:53], v[154:155], off offset:3392
	global_load_dwordx4 v[54:57], v[10:11], off offset:1024
	s_nop 5
	global_load_dwordx4 v[34:37], v[154:155], off offset:3456
	global_load_dwordx4 v[38:41], v[10:11], off offset:2048
	global_load_dwordx4 v[2:5], v[154:155], off offset:3520
	s_nop 0
	global_load_dwordx4 v[10:13], v[10:11], off offset:3072
	s_waitcnt vmcnt(30)
	v_mfma_f32_16x16x4_f32 v[132:135], v110, v114, v[132:135]
	v_add_f32_e32 v114, v136, v137
	s_waitcnt vmcnt(15)
	v_mul_f32_e32 v136, v125, v125
	v_fmac_f32_e32 v136, v124, v124
	v_mfma_f32_16x16x4_f32 v[132:135], v111, v115, v[132:135]
	v_mul_f32_e32 v115, v95, v95
	v_fmac_f32_e32 v115, v94, v94
	v_mfma_f32_16x16x4_f32 v[132:135], v112, v116, v[132:135]
	v_mul_f32_e32 v116, v97, v97
	v_fmac_f32_e32 v116, v96, v96
	v_add_f32_e32 v115, v115, v116
	v_mfma_f32_16x16x4_f32 v[110:113], v113, v117, v[132:135]
	s_nop 5
	v_mul_f32_e32 v135, v123, v123
	v_fmac_f32_e32 v135, v122, v122
	v_add_f32_e32 v135, v135, v136
	v_mfma_f32_16x16x4_f32 v[110:113], v94, v98, v[110:113]
	v_add_f32_e32 v98, v114, v115
	v_mfma_f32_16x16x4_f32 v[110:113], v95, v99, v[110:113]
	v_mul_f32_e32 v99, v79, v79
	v_fmac_f32_e32 v99, v78, v78
	v_mfma_f32_16x16x4_f32 v[110:113], v96, v100, v[110:113]
	v_mul_f32_e32 v100, v81, v81
	v_fmac_f32_e32 v100, v80, v80
	v_add_f32_e32 v99, v99, v100
	v_mfma_f32_16x16x4_f32 v[94:97], v97, v101, v[110:113]
	v_mfma_f32_16x16x4_f32 v[94:97], v78, v82, v[94:97]
	v_add_f32_e32 v82, v98, v99
	v_mfma_f32_16x16x4_f32 v[94:97], v79, v83, v[94:97]
	v_mul_f32_e32 v83, v59, v59
	v_fmac_f32_e32 v83, v58, v58
	v_mfma_f32_16x16x4_f32 v[94:97], v80, v84, v[94:97]
	v_mul_f32_e32 v84, v61, v61
	v_fmac_f32_e32 v84, v60, v60
	v_add_f32_e32 v83, v83, v84
	v_mfma_f32_16x16x4_f32 v[78:81], v81, v85, v[94:97]
	v_mfma_f32_16x16x4_f32 v[78:81], v58, v70, v[78:81]
	v_add_f32_e32 v70, v82, v83
	v_mfma_f32_16x16x4_f32 v[78:81], v59, v71, v[78:81]
	v_mul_f32_e32 v71, v43, v43
	v_fmac_f32_e32 v71, v42, v42
	v_mfma_f32_16x16x4_f32 v[78:81], v60, v72, v[78:81]
	v_mul_f32_e32 v72, v45, v45
	v_fmac_f32_e32 v72, v44, v44
	v_add_f32_e32 v71, v71, v72
	v_mfma_f32_16x16x4_f32 v[58:61], v61, v73, v[78:81]
	v_mfma_f32_16x16x4_f32 v[58:61], v42, v46, v[58:61]
	v_add_f32_e32 v46, v70, v71
	v_mfma_f32_16x16x4_f32 v[58:61], v43, v47, v[58:61]
	v_mul_f32_e32 v47, v27, v27
	v_fmac_f32_e32 v47, v26, v26
	v_mfma_f32_16x16x4_f32 v[58:61], v44, v48, v[58:61]
	v_mul_f32_e32 v48, v29, v29
	v_fmac_f32_e32 v48, v28, v28
; __device__ __forceinline__ void norm2_block(float* xl, float* xc, const float* MOD, const float* gn, const float* WP, bf16_t* H, float* AFF, int L, int row0, int nrows, int lane) {
;     ...
;     for (int q = 0; q < 8; ++q) { xa[q] = *(const f32x4*)(xr + 16 * q); wb[q] = *(const f32x4*)(wp + 256 * q); }
; #pragma unroll
;     for (int g = 0; g < 8; ++g) {
;         f32x4 xn[8], wn[8];
;         if (g < 7) {
; #pragma unroll
;             for (int q = 0; q < 8; ++q) { xn[q] = *(const f32x4*)(xr + 16 * (8 * (g + 1) + q)); wn[q] = *(const f32x4*)(wp + 256 * (8 * (g + 1) + q)); } }
; #pragma unroll
;         for (int q = 0; q < 8; ++q) {
;             sq += (xa[q][0] * xa[q][0] + xa[q][1] * xa[q][1]) + (xa[q][2] * xa[q][2] + xa[q][3] * xa[q][3]);
; #pragma unroll
;             for (int i = 0; i < 4; ++i) acc = __builtin_amdgcn_mfma_f32_16x16x4f32(xa[q][i], wb[q][i], acc, 0, 0, 0); }
;         if (g < 7) {
; #pragma unroll
;             for (int q = 0; q < 8; ++q) { xa[q] = xn[q]; wb[q] = wn[q]; } }
;     }
	v_add_f32_e32 v47, v47, v48
	v_mfma_f32_16x16x4_f32 v[42:45], v45, v49, v[58:61]
	v_mfma_f32_16x16x4_f32 v[42:45], v26, v30, v[42:45]
	v_add_f32_e32 v30, v46, v47
	v_mfma_f32_16x16x4_f32 v[42:45], v27, v31, v[42:45]
	v_mul_f32_e32 v31, v19, v19
	v_fmac_f32_e32 v31, v18, v18
	v_mfma_f32_16x16x4_f32 v[42:45], v28, v32, v[42:45]
	v_mul_f32_e32 v32, v21, v21
	v_fmac_f32_e32 v32, v20, v20
	v_add_f32_e32 v31, v31, v32
	v_mfma_f32_16x16x4_f32 v[26:29], v29, v33, v[42:45]
	v_mfma_f32_16x16x4_f32 v[26:29], v18, v22, v[26:29]
	v_add_f32_e32 v22, v30, v31
	v_mfma_f32_16x16x4_f32 v[26:29], v19, v23, v[26:29]
	v_mul_f32_e32 v23, v7, v7
	v_fmac_f32_e32 v23, v6, v6
	v_mfma_f32_16x16x4_f32 v[26:29], v20, v24, v[26:29]
	v_mul_f32_e32 v24, v9, v9
	v_fmac_f32_e32 v24, v8, v8
	v_add_f32_e32 v23, v23, v24
	v_add_f32_e32 v134, v22, v23
	v_mfma_f32_16x16x4_f32 v[18:21], v21, v25, v[26:29]
	v_mfma_f32_16x16x4_f32 v[18:21], v6, v14, v[18:21]
	v_mfma_f32_16x16x4_f32 v[18:21], v7, v15, v[18:21]
	v_mfma_f32_16x16x4_f32 v[18:21], v8, v16, v[18:21]
	v_mfma_f32_16x16x4_f32 v[6:9], v9, v17, v[18:21]
	global_load_dwordx4 v[14:17], v[154:155], off offset:3584
	s_nop 7
	global_load_dwordx4 v[18:21], v[130:131], off
	global_load_dwordx4 v[22:25], v[154:155], off offset:3648
	global_load_dwordx4 v[26:29], v[130:131], off offset:1024
	global_load_dwordx4 v[30:33], v[154:155], off offset:3712
	global_load_dwordx4 v[42:45], v[130:131], off offset:2048
	global_load_dwordx4 v[46:49], v[154:155], off offset:3776
	global_load_dwordx4 v[58:61], v[130:131], off offset:3072
	global_load_dwordx4 v[70:73], v[154:155], off offset:3840
	v_add_co_u32_e32 v130, vcc, s10, v156
	s_lshl_b32 s10, s5, 4
	s_nop 0
	v_addc_co_u32_e32 v131, vcc, 0, v157, vcc
	global_load_dwordx4 v[78:81], v[130:131], off
	global_load_dwordx4 v[82:85], v[154:155], off offset:3904
	global_load_dwordx4 v[94:97], v[130:131], off offset:1024
	global_load_dwordx4 v[98:101], v[154:155], off offset:3968
	global_load_dwordx4 v[110:113], v[130:131], off offset:2048
	global_load_dwordx4 v[114:117], v[154:155], off offset:4032
	s_nop 0
	global_load_dwordx4 v[130:133], v[130:131], off offset:3072
	s_waitcnt vmcnt(30)
	v_mfma_f32_16x16x4_f32 v[6:9], v122, v126, v[6:9]
	v_add_f32_e32 v122, v134, v135
	s_add_i32 s5, s5, s70
	v_mfma_f32_16x16x4_f32 v[6:9], v123, v127, v[6:9]
	s_waitcnt vmcnt(29)
	v_mul_f32_e32 v123, v107, v107
	v_fmac_f32_e32 v123, v106, v106
	v_mfma_f32_16x16x4_f32 v[6:9], v124, v128, v[6:9]
	v_mul_f32_e32 v124, v109, v109
	v_fmac_f32_e32 v124, v108, v108
	v_add_f32_e32 v123, v123, v124
	v_mfma_f32_16x16x4_f32 v[6:9], v125, v129, v[6:9]
	s_waitcnt vmcnt(28)
	v_mfma_f32_16x16x4_f32 v[6:9], v106, v118, v[6:9]
	v_add_f32_e32 v106, v122, v123
	v_mfma_f32_16x16x4_f32 v[6:9], v107, v119, v[6:9]
	s_waitcnt vmcnt(27)
	v_mul_f32_e32 v107, v91, v91
	v_fmac_f32_e32 v107, v90, v90
	v_mfma_f32_16x16x4_f32 v[6:9], v108, v120, v[6:9]
	v_mul_f32_e32 v108, v93, v93
	v_fmac_f32_e32 v108, v92, v92
	v_add_f32_e32 v107, v107, v108
	v_mfma_f32_16x16x4_f32 v[6:9], v109, v121, v[6:9]
	s_waitcnt vmcnt(26)
	v_mfma_f32_16x16x4_f32 v[6:9], v90, v102, v[6:9]
	v_add_f32_e32 v90, v106, v107
	v_mfma_f32_16x16x4_f32 v[6:9], v91, v103, v[6:9]
	s_waitcnt vmcnt(25)
	v_mul_f32_e32 v91, v75, v75
	v_fmac_f32_e32 v91, v74, v74
	v_mfma_f32_16x16x4_f32 v[6:9], v92, v104, v[6:9]
	v_mul_f32_e32 v92, v77, v77
	v_fmac_f32_e32 v92, v76, v76
	v_add_f32_e32 v91, v91, v92
	v_mfma_f32_16x16x4_f32 v[6:9], v93, v105, v[6:9]
	s_waitcnt vmcnt(24)
	v_mfma_f32_16x16x4_f32 v[6:9], v74, v86, v[6:9]
	v_add_f32_e32 v74, v90, v91
	v_mfma_f32_16x16x4_f32 v[6:9], v75, v87, v[6:9]
	s_waitcnt vmcnt(23)
	v_mul_f32_e32 v75, v63, v63
	v_fmac_f32_e32 v75, v62, v62
	v_mfma_f32_16x16x4_f32 v[6:9], v76, v88, v[6:9]
	v_mul_f32_e32 v76, v65, v65
	v_fmac_f32_e32 v76, v64, v64
	v_add_f32_e32 v75, v75, v76
	v_mfma_f32_16x16x4_f32 v[6:9], v77, v89, v[6:9]
	s_waitcnt vmcnt(22)
	v_mfma_f32_16x16x4_f32 v[6:9], v62, v66, v[6:9]
	v_add_f32_e32 v62, v74, v75
	v_mfma_f32_16x16x4_f32 v[6:9], v63, v67, v[6:9]
	s_waitcnt vmcnt(21)
	v_mul_f32_e32 v63, v51, v51
	v_fmac_f32_e32 v63, v50, v50
	v_mfma_f32_16x16x4_f32 v[6:9], v64, v68, v[6:9]
	v_mul_f32_e32 v64, v53, v53
	v_fmac_f32_e32 v64, v52, v52
	v_add_f32_e32 v63, v63, v64
	v_mfma_f32_16x16x4_f32 v[6:9], v65, v69, v[6:9]
	s_waitcnt vmcnt(20)
	v_mfma_f32_16x16x4_f32 v[6:9], v50, v54, v[6:9]
	v_add_f32_e32 v50, v62, v63
	v_mfma_f32_16x16x4_f32 v[6:9], v51, v55, v[6:9]
	s_waitcnt vmcnt(19)
	v_mul_f32_e32 v51, v35, v35
	v_fmac_f32_e32 v51, v34, v34
	v_mfma_f32_16x16x4_f32 v[6:9], v52, v56, v[6:9]
	v_mul_f32_e32 v52, v37, v37
	v_fmac_f32_e32 v52, v36, v36
	v_add_f32_e32 v51, v51, v52
	v_mfma_f32_16x16x4_f32 v[6:9], v53, v57, v[6:9]
	s_waitcnt vmcnt(18)
	v_mfma_f32_16x16x4_f32 v[6:9], v34, v38, v[6:9]
	v_add_f32_e32 v34, v50, v51
	v_mfma_f32_16x16x4_f32 v[6:9], v35, v39, v[6:9]
	s_waitcnt vmcnt(17)
	v_mul_f32_e32 v35, v3, v3
	v_fmac_f32_e32 v35, v2, v2
	v_mfma_f32_16x16x4_f32 v[6:9], v36, v40, v[6:9]
	v_mul_f32_e32 v36, v5, v5
	v_fmac_f32_e32 v36, v4, v4
	v_add_f32_e32 v35, v35, v36
	v_mfma_f32_16x16x4_f32 v[6:9], v37, v41, v[6:9]
	s_waitcnt vmcnt(16)
	v_mfma_f32_16x16x4_f32 v[6:9], v2, v10, v[6:9]
	v_mfma_f32_16x16x4_f32 v[6:9], v3, v11, v[6:9]
	v_mfma_f32_16x16x4_f32 v[6:9], v4, v12, v[6:9]
	v_mfma_f32_16x16x4_f32 v[2:5], v5, v13, v[6:9]
	s_waitcnt vmcnt(15)
	s_nop 7
	v_mul_f32_e32 v7, v15, v15
	v_mul_f32_e32 v8, v17, v17
	v_fmac_f32_e32 v7, v14, v14
	v_fmac_f32_e32 v8, v16, v16
	v_add_f32_e32 v6, v34, v35
	v_add_f32_e32 v7, v7, v8
	v_add_f32_e32 v6, v6, v7
	s_waitcnt vmcnt(14)
	v_mfma_f32_16x16x4_f32 v[2:5], v14, v18, v[2:5]
	s_waitcnt vmcnt(13)
; __device__ __forceinline__ void norm2_block(float* xl, float* xc, const float* MOD, const float* gn, const float* WP, bf16_t* H, float* AFF, int L, int row0, int nrows, int lane) {
;     ...
;     sq = att::lanes4_sum(sq);
;     const float rstd = rsqrtf(sq * (1.f / DM) + EPS);
;     const float bias = WP[9 * 16384 + s_ * 16 + r16];
; #pragma unroll
;     for (int i = 0; i < 4; ++i) {
;         const float rs = __shfl(rstd, 4 * kq + i);
;         const float lg = acc[i] * rs + bias;
;         float mx = lg;
; #pragma unroll
;         for (int o = 1; o < 16; o <<= 1) mx = fmaxf(mx, __shfl_xor(mx, o));
;         const float mine = __expf(lg - mx); float den = mine;
; #pragma unroll
;         for (int o = 1; o < 16; o <<= 1) den += __shfl_xor(den, o);
;         if (4 * kq + i < nrows) AFF[(size_t)(row0 + 4 * kq + i) * 16 + r16] = mine / den;
;     }
	v_mul_f32_e32 v7, v23, v23
	v_mul_f32_e32 v8, v25, v25
	v_fmac_f32_e32 v7, v22, v22
	v_fmac_f32_e32 v8, v24, v24
	v_add_f32_e32 v7, v7, v8
	v_add_f32_e32 v6, v6, v7
	s_waitcnt vmcnt(11)
	v_mul_f32_e32 v7, v31, v31
	v_mfma_f32_16x16x4_f32 v[2:5], v15, v19, v[2:5]
	v_mul_f32_e32 v8, v33, v33
	v_fmac_f32_e32 v7, v30, v30
	v_fmac_f32_e32 v8, v32, v32
	v_add_f32_e32 v7, v7, v8
	v_add_f32_e32 v6, v6, v7
	s_waitcnt vmcnt(9)
	v_mul_f32_e32 v7, v47, v47
	v_mul_f32_e32 v8, v49, v49
	v_mfma_f32_16x16x4_f32 v[2:5], v16, v20, v[2:5]
	v_fmac_f32_e32 v7, v46, v46
	v_fmac_f32_e32 v8, v48, v48
	v_add_f32_e32 v7, v7, v8
	v_add_f32_e32 v6, v6, v7
	s_waitcnt vmcnt(7)
	v_mul_f32_e32 v7, v71, v71
	v_mul_f32_e32 v8, v73, v73
	v_fmac_f32_e32 v7, v70, v70
	v_mfma_f32_16x16x4_f32 v[2:5], v17, v21, v[2:5]
	v_fmac_f32_e32 v8, v72, v72
	v_add_f32_e32 v7, v7, v8
	v_add_f32_e32 v6, v6, v7
	s_waitcnt vmcnt(5)
	v_mul_f32_e32 v7, v83, v83
	v_mul_f32_e32 v8, v85, v85
	v_fmac_f32_e32 v7, v82, v82
	v_fmac_f32_e32 v8, v84, v84
	v_mfma_f32_16x16x4_f32 v[2:5], v22, v26, v[2:5]
	v_add_f32_e32 v7, v7, v8
	v_add_f32_e32 v6, v6, v7
	s_waitcnt vmcnt(3)
	v_mul_f32_e32 v7, v99, v99
	v_mul_f32_e32 v8, v101, v101
	v_fmac_f32_e32 v7, v98, v98
	v_fmac_f32_e32 v8, v100, v100
	v_add_f32_e32 v7, v7, v8
	v_mfma_f32_16x16x4_f32 v[2:5], v23, v27, v[2:5]
	v_add_f32_e32 v6, v6, v7
	s_waitcnt vmcnt(1)
	v_mul_f32_e32 v7, v115, v115
	v_mul_f32_e32 v8, v117, v117
	v_fmac_f32_e32 v7, v114, v114
	v_fmac_f32_e32 v8, v116, v116
	v_add_f32_e32 v7, v7, v8
	v_add_f32_e32 v6, v6, v7
	v_mfma_f32_16x16x4_f32 v[2:5], v24, v28, v[2:5]
	v_mov_b32_e32 v7, v6
	s_nop 1
	v_permlane16_swap_b32_e32 v6, v7
	v_add_f32_e32 v6, v6, v7
	v_mov_b32_e32 v7, v6
	s_nop 1
	v_permlane32_swap_b32_e32 v6, v7
	v_mfma_f32_16x16x4_f32 v[2:5], v25, v29, v[2:5]
	v_add_f32_e32 v6, v6, v7
	v_fmamk_f32 v6, v6, 0x3a800000, v196
	v_cmp_gt_f32_e32 vcc, s95, v6
	v_mul_f32_e32 v7, 0x4b800000, v6
	v_or_b32_e32 v8, v226, v142
	v_cndmask_b32_e32 v6, v6, v7, vcc
	v_rsq_f32_e32 v6, v6
	v_mfma_f32_16x16x4_f32 v[2:5], v30, v42, v[2:5]
	v_lshlrev_b32_e32 v8, 2, v8
	v_mul_f32_e32 v7, 0x45800000, v6
	v_mfma_f32_16x16x4_f32 v[2:5], v31, v43, v[2:5]
	v_mfma_f32_16x16x4_f32 v[2:5], v32, v44, v[2:5]
	v_mfma_f32_16x16x4_f32 v[2:5], v33, v45, v[2:5]
	v_mfma_f32_16x16x4_f32 v[2:5], v46, v58, v[2:5]
	v_mfma_f32_16x16x4_f32 v[2:5], v47, v59, v[2:5]
	v_mfma_f32_16x16x4_f32 v[2:5], v48, v60, v[2:5]
	v_mfma_f32_16x16x4_f32 v[2:5], v49, v61, v[2:5]
	v_mfma_f32_16x16x4_f32 v[2:5], v70, v78, v[2:5]
	v_mfma_f32_16x16x4_f32 v[2:5], v71, v79, v[2:5]
	v_mfma_f32_16x16x4_f32 v[2:5], v72, v80, v[2:5]
	v_mfma_f32_16x16x4_f32 v[2:5], v73, v81, v[2:5]
	v_mfma_f32_16x16x4_f32 v[2:5], v82, v94, v[2:5]
	v_mfma_f32_16x16x4_f32 v[2:5], v83, v95, v[2:5]
	v_mfma_f32_16x16x4_f32 v[2:5], v84, v96, v[2:5]
	v_mfma_f32_16x16x4_f32 v[2:5], v85, v97, v[2:5]
	v_mfma_f32_16x16x4_f32 v[2:5], v98, v110, v[2:5]
	v_cndmask_b32_e32 v98, v6, v7, vcc
	v_add_lshl_u32 v6, s10, v160, 2
	global_load_dword v6, v6, s[12:13]
	ds_bpermute_b32 v8, v8, v98
	v_cmp_lt_i32_e32 vcc, v233, v227
	v_add_u32_e32 v7, s16, v142
	v_add_u32_e32 v194, 0x107f0, v7
	v_mfma_f32_16x16x4_f32 v[2:5], v99, v111, v[2:5]
	v_mfma_f32_16x16x4_f32 v[2:5], v100, v112, v[2:5]
	v_mfma_f32_16x16x4_f32 v[2:5], v101, v113, v[2:5]
	s_waitcnt vmcnt(1)
	v_mfma_f32_16x16x4_f32 v[2:5], v114, v130, v[2:5]
	v_mfma_f32_16x16x4_f32 v[2:5], v115, v131, v[2:5]
	v_mfma_f32_16x16x4_f32 v[2:5], v116, v132, v[2:5]
	v_mfma_f32_16x16x4_f32 v[2:5], v117, v133, v[2:5]
	s_waitcnt vmcnt(0) lgkmcnt(0)
	s_nop 8
	v_fma_f32 v11, v2, v8, v6
	v_cndmask_b32_e32 v2, v225, v233, vcc
	v_lshlrev_b32_e32 v2, 2, v2
	ds_bpermute_b32 v8, v2, v11
	v_cmp_lt_i32_e32 vcc, v171, v227
	s_waitcnt lgkmcnt(0)
	v_max_f32_e32 v8, v8, v8
	v_max_f32_e32 v9, v11, v8
	v_cndmask_b32_e32 v8, v225, v171, vcc
	v_lshlrev_b32_e32 v8, 2, v8
	s_nop 1
	v_mov_b32_dpp v10, v9 quad_perm:[2,3,0,1] row_mask:0xf bank_mask:0xf
	v_cmp_lt_i32_e32 vcc, v172, v227
	s_waitcnt lgkmcnt(0)
	v_max_f32_e32 v10, v10, v10
	v_max_f32_e32 v10, v9, v10
	v_cndmask_b32_e32 v9, v225, v172, vcc
	v_lshlrev_b32_e32 v9, 2, v9
	s_nop 1
	v_mov_b32_dpp v12, v10 row_shl:4 row_mask:0xf bank_mask:0x5
	v_mov_b32_dpp v12, v10 row_shr:4 row_mask:0xf bank_mask:0xa
	v_cmp_lt_i32_e32 vcc, v173, v227
	s_waitcnt lgkmcnt(0)
	v_max_f32_e32 v12, v12, v12
	v_max_f32_e32 v12, v10, v12
	v_cndmask_b32_e32 v10, v225, v173, vcc
	v_lshlrev_b32_e32 v10, 2, v10
	s_nop 1
	v_mov_b32_dpp v13, v12 row_shl:8 row_mask:0xf bank_mask:0x3
	v_mov_b32_dpp v13, v12 row_shr:8 row_mask:0xf bank_mask:0xc
	s_waitcnt lgkmcnt(0)
	v_max_f32_e32 v13, v13, v13
	v_max_f32_e32 v12, v12, v13
	v_sub_f32_e32 v11, v11, v12
	v_mul_f32_e32 v11, 0x3fb8aa3b, v11
	v_exp_f32_e32 v11, v11
	ds_bpermute_b32 v12, v2, v11
	s_waitcnt lgkmcnt(0)
	v_add_f32_e32 v12, v11, v12
	s_nop 1
	v_mov_b32_dpp v13, v12 quad_perm:[2,3,0,1] row_mask:0xf bank_mask:0xf
	s_waitcnt lgkmcnt(0)
	v_add_f32_e32 v12, v12, v13
	s_nop 1
	v_mov_b32_dpp v13, v12 row_shl:4 row_mask:0xf bank_mask:0x5
	v_mov_b32_dpp v13, v12 row_shr:4 row_mask:0xf bank_mask:0xa
	s_waitcnt lgkmcnt(0)
	v_add_f32_e32 v12, v12, v13
	s_nop 1
	v_mov_b32_dpp v13, v12 row_shl:8 row_mask:0xf bank_mask:0x3
	v_mov_b32_dpp v13, v12 row_shr:8 row_mask:0xf bank_mask:0xc
	s_waitcnt lgkmcnt(0)
	v_add_f32_e32 v12, v12, v13
	v_div_scale_f32 v13, s[10:11], v12, v12, v11
	v_rcp_f32_e32 v14, v13
	s_nop 0
	v_fma_f32 v15, -v13, v14, 1.0
	v_fmac_f32_e32 v14, v15, v14
	v_div_scale_f32 v15, vcc, v11, v12, v11
	v_mul_f32_e32 v16, v15, v14
	v_fma_f32 v17, -v13, v16, v15
	v_fmac_f32_e32 v16, v17, v14
	v_fma_f32 v13, -v13, v16, v15
	v_div_fmas_f32 v13, v13, v14, v16
	v_div_fixup_f32 v11, v13, v12, v11
	v_lshlrev_b64 v[12:13], 6, v[194:195]
	v_lshl_add_u64 v[12:13], v[146:147], 0, v[12:13]
	global_store_dword v[12:13], v11, off
	v_or_b32_e32 v11, v226, v161
	v_lshlrev_b32_e32 v11, 2, v11
	ds_bpermute_b32 v11, v11, v98
	v_add_u32_e32 v194, 0x107f1, v7
	s_waitcnt lgkmcnt(0)
; __device__ __forceinline__ void norm2_block(float* xl, float* xc, const float* MOD, const float* gn, const float* WP, bf16_t* H, float* AFF, int L, int row0, int nrows, int lane) {
;     ...
;     for (int i = 0; i < 4; ++i) {
;         const float rs = __shfl(rstd, 4 * kq + i);
;         const float lg = acc[i] * rs + bias;
;         float mx = lg;
; #pragma unroll
;         for (int o = 1; o < 16; o <<= 1) mx = fmaxf(mx, __shfl_xor(mx, o));
;         const float mine = __expf(lg - mx); float den = mine;
; #pragma unroll
;         for (int o = 1; o < 16; o <<= 1) den += __shfl_xor(den, o);
;         if (4 * kq + i < nrows) AFF[(size_t)(row0 + 4 * kq + i) * 16 + r16] = mine / den;
;     }
	v_fma_f32 v3, v3, v11, v6
	ds_bpermute_b32 v11, v2, v3
	s_waitcnt lgkmcnt(0)
	v_max_f32_e32 v11, v11, v11
	v_max_f32_e32 v11, v3, v11
	s_nop 1
	v_mov_b32_dpp v12, v11 quad_perm:[2,3,0,1] row_mask:0xf bank_mask:0xf
	s_waitcnt lgkmcnt(0)
	v_max_f32_e32 v12, v12, v12
	v_max_f32_e32 v11, v11, v12
	s_nop 1
	v_mov_b32_dpp v12, v11 row_shl:4 row_mask:0xf bank_mask:0x5
	v_mov_b32_dpp v12, v11 row_shr:4 row_mask:0xf bank_mask:0xa
	s_waitcnt lgkmcnt(0)
	v_max_f32_e32 v12, v12, v12
	v_max_f32_e32 v11, v11, v12
	s_nop 1
	v_mov_b32_dpp v12, v11 row_shl:8 row_mask:0xf bank_mask:0x3
	v_mov_b32_dpp v12, v11 row_shr:8 row_mask:0xf bank_mask:0xc
	s_waitcnt lgkmcnt(0)
	v_max_f32_e32 v12, v12, v12
	v_max_f32_e32 v11, v11, v12
	v_sub_f32_e32 v3, v3, v11
	v_mul_f32_e32 v3, 0x3fb8aa3b, v3
	v_exp_f32_e32 v3, v3
	ds_bpermute_b32 v11, v2, v3
	s_waitcnt lgkmcnt(0)
	v_add_f32_e32 v11, v3, v11
	s_nop 1
	v_mov_b32_dpp v12, v11 quad_perm:[2,3,0,1] row_mask:0xf bank_mask:0xf
	s_waitcnt lgkmcnt(0)
	v_add_f32_e32 v11, v11, v12
	s_nop 1
	v_mov_b32_dpp v12, v11 row_shl:4 row_mask:0xf bank_mask:0x5
	v_mov_b32_dpp v12, v11 row_shr:4 row_mask:0xf bank_mask:0xa
	s_waitcnt lgkmcnt(0)
	v_add_f32_e32 v11, v11, v12
	s_nop 1
	v_mov_b32_dpp v12, v11 row_shl:8 row_mask:0xf bank_mask:0x3
	v_mov_b32_dpp v12, v11 row_shr:8 row_mask:0xf bank_mask:0xc
	s_waitcnt lgkmcnt(0)
	v_add_f32_e32 v11, v11, v12
	v_div_scale_f32 v12, s[10:11], v11, v11, v3
	v_rcp_f32_e32 v13, v12
	s_nop 0
	v_fma_f32 v14, -v12, v13, 1.0
	v_fmac_f32_e32 v13, v14, v13
	v_div_scale_f32 v14, vcc, v3, v11, v3
	v_mul_f32_e32 v15, v14, v13
	v_fma_f32 v16, -v12, v15, v14
	v_fmac_f32_e32 v15, v16, v13
	v_fma_f32 v12, -v12, v15, v14
	v_div_fmas_f32 v12, v12, v13, v15
	v_div_fixup_f32 v3, v12, v11, v3
	v_lshlrev_b64 v[12:13], 6, v[194:195]
	v_lshl_add_u64 v[12:13], v[146:147], 0, v[12:13]
	global_store_dword v[12:13], v3, off
	v_or_b32_e32 v3, v226, v162
	v_lshlrev_b32_e32 v3, 2, v3
	ds_bpermute_b32 v3, v3, v98
	v_add_u32_e32 v194, 0x107f2, v7
	s_waitcnt lgkmcnt(0)
	v_fma_f32 v3, v4, v3, v6
	ds_bpermute_b32 v4, v2, v3
	s_waitcnt lgkmcnt(0)
	v_max_f32_e32 v4, v4, v4
	v_max_f32_e32 v4, v3, v4
	s_nop 1
	v_mov_b32_dpp v11, v4 quad_perm:[2,3,0,1] row_mask:0xf bank_mask:0xf
	s_waitcnt lgkmcnt(0)
	v_max_f32_e32 v11, v11, v11
	v_max_f32_e32 v4, v4, v11
	s_nop 1
	v_mov_b32_dpp v11, v4 row_shl:4 row_mask:0xf bank_mask:0x5
	v_mov_b32_dpp v11, v4 row_shr:4 row_mask:0xf bank_mask:0xa
	s_waitcnt lgkmcnt(0)
	v_max_f32_e32 v11, v11, v11
	v_max_f32_e32 v4, v4, v11
	s_nop 1
	v_mov_b32_dpp v11, v4 row_shl:8 row_mask:0xf bank_mask:0x3
	v_mov_b32_dpp v11, v4 row_shr:8 row_mask:0xf bank_mask:0xc
	s_waitcnt lgkmcnt(0)
	v_max_f32_e32 v11, v11, v11
	v_max_f32_e32 v4, v4, v11
	v_sub_f32_e32 v3, v3, v4
	v_mul_f32_e32 v3, 0x3fb8aa3b, v3
	v_exp_f32_e32 v3, v3
	ds_bpermute_b32 v4, v2, v3
	s_waitcnt lgkmcnt(0)
	v_add_f32_e32 v4, v3, v4
	s_nop 1
	v_mov_b32_dpp v11, v4 quad_perm:[2,3,0,1] row_mask:0xf bank_mask:0xf
	s_waitcnt lgkmcnt(0)
	v_add_f32_e32 v4, v4, v11
	s_nop 1
	v_mov_b32_dpp v11, v4 row_shl:4 row_mask:0xf bank_mask:0x5
	v_mov_b32_dpp v11, v4 row_shr:4 row_mask:0xf bank_mask:0xa
	s_waitcnt lgkmcnt(0)
	v_add_f32_e32 v4, v4, v11
	s_nop 1
	v_mov_b32_dpp v11, v4 row_shl:8 row_mask:0xf bank_mask:0x3
	v_mov_b32_dpp v11, v4 row_shr:8 row_mask:0xf bank_mask:0xc
	s_waitcnt lgkmcnt(0)
	v_add_f32_e32 v4, v4, v11
	v_div_scale_f32 v11, s[10:11], v4, v4, v3
	v_rcp_f32_e32 v12, v11
	s_nop 0
	v_fma_f32 v13, -v11, v12, 1.0
	v_fmac_f32_e32 v12, v13, v12
	v_div_scale_f32 v13, vcc, v3, v4, v3
	v_mul_f32_e32 v14, v13, v12
	v_fma_f32 v15, -v11, v14, v13
	v_fmac_f32_e32 v14, v15, v12
	v_fma_f32 v11, -v11, v14, v13
	v_div_fmas_f32 v11, v11, v12, v14
	v_lshlrev_b64 v[12:13], 6, v[194:195]
	v_div_fixup_f32 v3, v11, v4, v3
	v_lshl_add_u64 v[12:13], v[146:147], 0, v[12:13]
	global_store_dword v[12:13], v3, off
	v_or_b32_e32 v3, v226, v163
	v_lshlrev_b32_e32 v3, 2, v3
	ds_bpermute_b32 v3, v3, v98
	v_add_u32_e32 v194, 0x107f3, v7
	s_waitcnt lgkmcnt(0)
	v_fmac_f32_e32 v6, v5, v3
	ds_bpermute_b32 v3, v2, v6
	s_waitcnt lgkmcnt(0)
	v_max_f32_e32 v3, v3, v3
	v_max_f32_e32 v3, v6, v3
	s_nop 1
	v_mov_b32_dpp v4, v3 quad_perm:[2,3,0,1] row_mask:0xf bank_mask:0xf
	s_waitcnt lgkmcnt(0)
	v_max_f32_e32 v4, v4, v4
	v_max_f32_e32 v3, v3, v4
	s_nop 1
	v_mov_b32_dpp v4, v3 row_shl:4 row_mask:0xf bank_mask:0x5
	v_mov_b32_dpp v4, v3 row_shr:4 row_mask:0xf bank_mask:0xa
	s_waitcnt lgkmcnt(0)
	v_max_f32_e32 v4, v4, v4
	v_max_f32_e32 v3, v3, v4
	s_nop 1
	v_mov_b32_dpp v4, v3 row_shl:8 row_mask:0xf bank_mask:0x3
	v_mov_b32_dpp v4, v3 row_shr:8 row_mask:0xf bank_mask:0xc
	s_waitcnt lgkmcnt(0)
	v_max_f32_e32 v4, v4, v4
	v_max_f32_e32 v3, v3, v4
	v_sub_f32_e32 v3, v6, v3
	v_mul_f32_e32 v3, 0x3fb8aa3b, v3
	v_exp_f32_e32 v3, v3
	ds_bpermute_b32 v2, v2, v3
	s_waitcnt lgkmcnt(0)
	v_add_f32_e32 v2, v3, v2
	s_nop 1
	v_mov_b32_dpp v4, v2 quad_perm:[2,3,0,1] row_mask:0xf bank_mask:0xf
	s_waitcnt lgkmcnt(0)
	v_add_f32_e32 v2, v2, v4
	s_nop 1
	v_mov_b32_dpp v4, v2 row_shl:4 row_mask:0xf bank_mask:0x5
	v_mov_b32_dpp v4, v2 row_shr:4 row_mask:0xf bank_mask:0xa
	s_waitcnt lgkmcnt(0)
	v_add_f32_e32 v2, v2, v4
	s_nop 1
	v_mov_b32_dpp v4, v2 row_shl:8 row_mask:0xf bank_mask:0x3
	v_mov_b32_dpp v4, v2 row_shr:8 row_mask:0xf bank_mask:0xc
	s_waitcnt lgkmcnt(0)
; __device__ __forceinline__ unsigned cvtpk(float lo, float hi) { f32x2 v = {lo, hi}; bf16x2_t b = __builtin_convertvector(v, bf16x2_t); return __builtin_bit_cast(unsigned, b); }
; __device__ __forceinline__ float* xrow_ptr(float* xl, float* xc, int b, int t) { return (t < SEQ) ? xl + ((size_t)(b * SEQ + t)) * DM : xc + ((size_t)(b * CTXL + (t - SEQ))) * DM; }
; #define xl OUTP(launder(kargs))
; __device__ __forceinline__ void norm2_block(float* xl, float* xc, const float* MOD, const float* gn, const float* WP, bf16_t* H, float* AFF, int L, int row0, int nrows, int lane) {
;     ...
;         if (4 * kq + i < nrows) AFF[(size_t)(row0 + 4 * kq + i) * 16 + r16] = mine / den;
;     }
;     const float* sh = MOD + ((size_t)(L * 9 + s_) * 6 + 3) * 1024; const float* scl = sh + 1024;
;     f32x4 mg[4], sf[4];
; #pragma unroll
;     for (int j = 0; j < 4; ++j) { const int c = 256 * j + 4 * lane; mg[j] = *(const f32x4*)(gn + c) * (*(const f32x4*)(scl + c) + 1.f); sf[j] = *(const f32x4*)(sh + c); }
; #pragma unroll
;     for (int r4 = 0; r4 < 4; ++r4) {
;         if (r4 * 4 < nrows) {
;             f32x4 v[4][4];
; #pragma unroll
;             for (int k = 0; k < 4; ++k) { const float* xq = xrow_ptr(xl, xc, b, t0 + r4 * 4 + k);
; #pragma unroll
;                 for (int j = 0; j < 4; ++j) v[k][j] = *(const f32x4*)(xq + 256 * j + 4 * lane); }
; #pragma unroll
;             for (int k = 0; k < 4; ++k) { const float rs = __builtin_bit_cast(float, __builtin_amdgcn_readlane(__builtin_bit_cast(int, rstd), r4 * 4 + k));
;                 bf16_t* hr = H + (size_t)(row0 + r4 * 4 + k) * DM;
; #pragma unroll
;                 for (int j = 0; j < 4; ++j) { const f32x4 h = (v[k][j] * rs) * mg[j] + sf[j]; u32x2 w; w.x = cvtpk(h[0], h[1]); w.y = cvtpk(h[2], h[3]); *(u32x2*)(hr + 256 * j + 4 * lane) = w; } }
	v_add_f32_e32 v2, v2, v4
	v_div_scale_f32 v4, s[10:11], v2, v2, v3
	v_rcp_f32_e32 v5, v4
	s_mul_hi_u32 s10, s5, 0x6000
	s_mulk_i32 s5, 0x6000
	s_add_u32 s5, s30, s5
	v_fma_f32 v6, -v4, v5, 1.0
	v_fmac_f32_e32 v5, v6, v5
	v_div_scale_f32 v6, vcc, v3, v2, v3
	v_mul_f32_e32 v8, v6, v5
	v_fma_f32 v9, -v4, v8, v6
	v_fmac_f32_e32 v8, v9, v5
	v_fma_f32 v4, -v4, v8, v6
	s_addc_u32 s15, s31, s10
	v_div_fmas_f32 v4, v4, v5, v8
	s_add_u32 s10, s5, 0x3000
	v_div_fixup_f32 v4, v4, v2, v3
	v_lshlrev_b64 v[2:3], 6, v[194:195]
	s_addc_u32 s11, s15, 0
	v_lshl_add_u64 v[2:3], v[146:147], 0, v[2:3]
	s_add_u32 s14, s5, 0x4000
	global_store_dword v[2:3], v4, off
	s_addc_u32 s15, s15, 0
	global_load_dwordx4 v[6:9], v152, s[14:15]
	global_load_dwordx4 v[2:5], v[148:149], off
	s_cmpk_lt_i32 s21, 0x2000
	s_cselect_b64 vcc, -1, 0
	s_mov_b32 s5, s39
	s_waitcnt vmcnt(1)
	v_pk_add_f32 v[8:9], v[8:9], 1.0 op_sel_hi:[1,0]
	v_pk_add_f32 v[6:7], v[6:7], 1.0 op_sel_hi:[1,0]
	s_waitcnt vmcnt(0)
	v_pk_mul_f32 v[94:95], v[4:5], v[8:9]
	v_pk_mul_f32 v[96:97], v[2:3], v[6:7]
	global_load_dwordx4 v[14:17], v152, s[10:11]
	global_load_dwordx4 v[2:5], v[148:149], off offset:1024
	global_load_dwordx4 v[6:9], v166, s[14:15]
	s_waitcnt vmcnt(0)
	v_pk_add_f32 v[8:9], v[8:9], 1.0 op_sel_hi:[1,0]
	v_pk_add_f32 v[6:7], v[6:7], 1.0 op_sel_hi:[1,0]
	v_pk_mul_f32 v[90:91], v[4:5], v[8:9]
	v_pk_mul_f32 v[92:93], v[2:3], v[6:7]
	global_load_dwordx4 v[10:13], v166, s[10:11]
	global_load_dwordx4 v[2:5], v[148:149], off offset:2048
	global_load_dwordx4 v[6:9], v167, s[14:15]
	s_waitcnt vmcnt(0)
	v_pk_add_f32 v[8:9], v[8:9], 1.0 op_sel_hi:[1,0]
	v_pk_add_f32 v[6:7], v[6:7], 1.0 op_sel_hi:[1,0]
	v_pk_mul_f32 v[86:87], v[4:5], v[8:9]
	v_pk_mul_f32 v[88:89], v[2:3], v[6:7]
	global_load_dwordx4 v[6:9], v167, s[10:11]
	global_load_dwordx4 v[2:5], v[148:149], off offset:3072
	global_load_dwordx4 v[18:21], v168, s[14:15]
	s_waitcnt vmcnt(0)
	v_pk_add_f32 v[18:19], v[18:19], 1.0 op_sel_hi:[1,0]
	s_nop 0
	v_pk_mul_f32 v[84:85], v[2:3], v[18:19]
	v_cndmask_b32_e32 v18, v170, v169, vcc
	v_add_u32_e32 v18, s20, v18
	v_pk_add_f32 v[20:21], v[20:21], 1.0 op_sel_hi:[1,0]
	v_add_u32_e32 v18, 0x107f0, v18
	v_pk_mul_f32 v[82:83], v[4:5], v[20:21]
	global_load_dwordx4 v[2:5], v168, s[10:11]
	s_and_b64 s[10:11], vcc, exec
	v_ashrrev_i32_e32 v19, 31, v18
	s_cselect_b32 s11, s9, s7
	s_cselect_b32 s10, s8, s6
	v_lshlrev_b64 v[18:19], 12, v[18:19]
	v_lshl_add_u64 v[18:19], s[10:11], 0, v[18:19]
	s_cmpk_lt_i32 s21, 0x1fff
	v_lshl_add_u64 v[18:19], v[18:19], 0, v[152:153]
	s_cselect_b64 vcc, -1, 0
	global_load_dwordx4 v[78:81], v[18:19], off
	global_load_dwordx4 v[74:77], v[18:19], off offset:1024
	global_load_dwordx4 v[70:73], v[18:19], off offset:2048
	global_load_dwordx4 v[66:69], v[18:19], off offset:3072
	v_cndmask_b32_e32 v18, v170, v169, vcc
	v_add_u32_e32 v18, s20, v18
	v_add_u32_e32 v18, 0x107f1, v18
	s_and_b64 s[10:11], vcc, exec
	v_ashrrev_i32_e32 v19, 31, v18
	s_cselect_b32 s11, s9, s7
	s_cselect_b32 s10, s8, s6
	v_lshlrev_b64 v[18:19], 12, v[18:19]
	v_lshl_add_u64 v[18:19], s[10:11], 0, v[18:19]
	s_cmpk_lt_i32 s21, 0x1ffe
	v_lshl_add_u64 v[18:19], v[18:19], 0, v[152:153]
	s_cselect_b64 vcc, -1, 0
	global_load_dwordx4 v[62:65], v[18:19], off
	global_load_dwordx4 v[58:61], v[18:19], off offset:1024
	global_load_dwordx4 v[54:57], v[18:19], off offset:2048
	global_load_dwordx4 v[50:53], v[18:19], off offset:3072
	v_cndmask_b32_e32 v18, v170, v169, vcc
	v_add_u32_e32 v18, s20, v18
	v_add_u32_e32 v18, 0x107f2, v18
	s_and_b64 s[10:11], vcc, exec
	v_ashrrev_i32_e32 v19, 31, v18
	s_cselect_b32 s11, s9, s7
	s_cselect_b32 s10, s8, s6
	v_lshlrev_b64 v[18:19], 12, v[18:19]
	v_lshl_add_u64 v[18:19], s[10:11], 0, v[18:19]
	s_cmpk_lt_i32 s21, 0x1ffd
	v_lshl_add_u64 v[18:19], v[18:19], 0, v[152:153]
	s_cselect_b64 vcc, -1, 0
	global_load_dwordx4 v[46:49], v[18:19], off
	global_load_dwordx4 v[42:45], v[18:19], off offset:1024
	global_load_dwordx4 v[38:41], v[18:19], off offset:2048
	global_load_dwordx4 v[34:37], v[18:19], off offset:3072
	v_cndmask_b32_e32 v18, v170, v169, vcc
	v_add_u32_e32 v18, s20, v18
	v_add_u32_e32 v18, 0x107f3, v18
	s_and_b64 s[10:11], vcc, exec
	v_ashrrev_i32_e32 v19, 31, v18
	s_cselect_b32 s11, s9, s7
	s_cselect_b32 s10, s8, s6
	v_lshlrev_b64 v[18:19], 12, v[18:19]
	v_lshl_add_u64 v[18:19], s[10:11], 0, v[18:19]
	v_lshl_add_u64 v[18:19], v[18:19], 0, v[152:153]
	global_load_dwordx4 v[30:33], v[18:19], off
	global_load_dwordx4 v[26:29], v[18:19], off offset:1024
	global_load_dwordx4 v[22:25], v[18:19], off offset:2048
	s_nop 0
	global_load_dwordx4 v[18:21], v[18:19], off offset:3072
	v_readlane_b32 s10, v98, 0
	s_lshl_b64 s[4:5], s[4:5], 11
	v_lshl_add_u64 v[100:101], v[150:151], 0, s[4:5]
	v_readlane_b32 s4, v98, 1
	s_add_i32 s38, s16, 0x107f1
	s_waitcnt vmcnt(15)
	v_pk_mul_f32 v[78:79], v[78:79], s[10:11] op_sel_hi:[1,0]
	v_pk_mul_f32 v[80:81], v[80:81], s[10:11] op_sel_hi:[1,0]
	s_waitcnt vmcnt(14)
	v_pk_mul_f32 v[74:75], v[74:75], s[10:11] op_sel_hi:[1,0]
	s_waitcnt vmcnt(12)
	v_pk_mul_f32 v[66:67], v[66:67], s[10:11] op_sel_hi:[1,0]
	v_pk_mul_f32 v[68:69], v[68:69], s[10:11] op_sel_hi:[1,0]
	v_pk_fma_f32 v[66:67], v[84:85], v[66:67], v[2:3]
	v_pk_fma_f32 v[68:69], v[82:83], v[68:69], v[4:5]
	v_pk_mul_f32 v[76:77], v[76:77], s[10:11] op_sel_hi:[1,0]
	v_pk_mul_f32 v[70:71], v[70:71], s[10:11] op_sel_hi:[1,0]
	v_pk_mul_f32 v[72:73], v[72:73], s[10:11] op_sel_hi:[1,0]
	v_cvt_pk_bf16_f32 v66, v66, v67
	v_cvt_pk_bf16_f32 v67, v68, v69
	s_lshl_b64 s[10:11], s[38:39], 11
	s_waitcnt vmcnt(11)
	v_pk_mul_f32 v[62:63], v[62:63], s[4:5] op_sel_hi:[1,0]
	v_pk_mul_f32 v[64:65], v[64:65], s[4:5] op_sel_hi:[1,0]
	s_waitcnt vmcnt(10)
; __device__ __forceinline__ unsigned cvtpk(float lo, float hi) { f32x2 v = {lo, hi}; bf16x2_t b = __builtin_convertvector(v, bf16x2_t); return __builtin_bit_cast(unsigned, b); }
; __device__ __forceinline__ float* xrow_ptr(float* xl, float* xc, int b, int t) { return (t < SEQ) ? xl + ((size_t)(b * SEQ + t)) * DM : xc + ((size_t)(b * CTXL + (t - SEQ))) * DM; }
; #define xl OUTP(launder(kargs))
; __device__ __forceinline__ void norm2_block(float* xl, float* xc, const float* MOD, const float* gn, const float* WP, bf16_t* H, float* AFF, int L, int row0, int nrows, int lane) {
;     ...
;     for (int r4 = 0; r4 < 4; ++r4) {
;         if (r4 * 4 < nrows) {
;             f32x4 v[4][4];
; #pragma unroll
;             for (int k = 0; k < 4; ++k) { const float* xq = xrow_ptr(xl, xc, b, t0 + r4 * 4 + k);
; #pragma unroll
;                 for (int j = 0; j < 4; ++j) v[k][j] = *(const f32x4*)(xq + 256 * j + 4 * lane); }
; #pragma unroll
;             for (int k = 0; k < 4; ++k) { const float rs = __builtin_bit_cast(float, __builtin_amdgcn_readlane(__builtin_bit_cast(int, rstd), r4 * 4 + k));
;                 bf16_t* hr = H + (size_t)(row0 + r4 * 4 + k) * DM;
; #pragma unroll
;                 for (int j = 0; j < 4; ++j) { const f32x4 h = (v[k][j] * rs) * mg[j] + sf[j]; u32x2 w; w.x = cvtpk(h[0], h[1]); w.y = cvtpk(h[2], h[3]); *(u32x2*)(hr + 256 * j + 4 * lane) = w; } }
;             asm volatile("" ::: "memory");
	v_pk_mul_f32 v[58:59], v[58:59], s[4:5] op_sel_hi:[1,0]
	s_waitcnt vmcnt(8)
	v_pk_mul_f32 v[50:51], v[50:51], s[4:5] op_sel_hi:[1,0]
	v_pk_mul_f32 v[52:53], v[52:53], s[4:5] op_sel_hi:[1,0]
	v_pk_mul_f32 v[60:61], v[60:61], s[4:5] op_sel_hi:[1,0]
	v_pk_mul_f32 v[54:55], v[54:55], s[4:5] op_sel_hi:[1,0]
	v_pk_mul_f32 v[56:57], v[56:57], s[4:5] op_sel_hi:[1,0]
	v_pk_fma_f32 v[52:53], v[82:83], v[52:53], v[4:5]
	v_pk_fma_f32 v[50:51], v[84:85], v[50:51], v[2:3]
	v_readlane_b32 s4, v98, 2
	s_add_i32 s38, s16, 0x107f2
	global_store_dwordx2 v[100:101], v[66:67], off offset:1536
	v_lshl_add_u64 v[66:67], v[150:151], 0, s[10:11]
	v_cvt_pk_bf16_f32 v50, v50, v51
	v_cvt_pk_bf16_f32 v51, v52, v53
	s_lshl_b64 s[10:11], s[38:39], 11
	s_waitcnt vmcnt(8)
	v_pk_mul_f32 v[46:47], v[46:47], s[4:5] op_sel_hi:[1,0]
	v_pk_mul_f32 v[48:49], v[48:49], s[4:5] op_sel_hi:[1,0]
	s_waitcnt vmcnt(7)
	v_pk_mul_f32 v[42:43], v[42:43], s[4:5] op_sel_hi:[1,0]
	v_pk_mul_f32 v[44:45], v[44:45], s[4:5] op_sel_hi:[1,0]
	s_waitcnt vmcnt(6)
	v_pk_mul_f32 v[38:39], v[38:39], s[4:5] op_sel_hi:[1,0]
	v_pk_mul_f32 v[40:41], v[40:41], s[4:5] op_sel_hi:[1,0]
	s_waitcnt vmcnt(5)
	v_pk_mul_f32 v[34:35], v[34:35], s[4:5] op_sel_hi:[1,0]
	v_pk_mul_f32 v[36:37], v[36:37], s[4:5] op_sel_hi:[1,0]
	v_readlane_b32 s4, v98, 3
	s_add_i32 s38, s16, 0x107f3
	global_store_dwordx2 v[66:67], v[50:51], off offset:1536
	v_lshl_add_u64 v[50:51], v[150:151], 0, s[10:11]
	v_pk_fma_f32 v[36:37], v[82:83], v[36:37], v[4:5]
	v_pk_fma_f32 v[34:35], v[84:85], v[34:35], v[2:3]
	s_lshl_b64 s[10:11], s[38:39], 11
	s_waitcnt vmcnt(2)
	v_pk_mul_f32 v[18:19], v[18:19], s[4:5] op_sel_hi:[1,0]
	v_pk_mul_f32 v[20:21], v[20:21], s[4:5] op_sel_hi:[1,0]
	v_cvt_pk_bf16_f32 v34, v34, v35
	v_cvt_pk_bf16_f32 v35, v36, v37
	v_pk_fma_f32 v[20:21], v[82:83], v[20:21], v[4:5]
	v_pk_fma_f32 v[18:19], v[84:85], v[18:19], v[2:3]
	s_cmpk_lt_i32 s21, 0x1ffc
	global_store_dwordx2 v[50:51], v[34:35], off offset:1536
	v_lshl_add_u64 v[34:35], v[150:151], 0, s[10:11]
	v_cvt_pk_bf16_f32 v18, v18, v19
	v_cvt_pk_bf16_f32 v19, v20, v21
	s_cselect_b64 vcc, -1, 0
	global_store_dwordx2 v[34:35], v[18:19], off offset:1536
	v_cndmask_b32_e32 v18, v170, v169, vcc
	v_add_u32_e32 v18, s20, v18
	v_pk_mul_f32 v[30:31], v[30:31], s[4:5] op_sel_hi:[1,0]
	v_pk_mul_f32 v[32:33], v[32:33], s[4:5] op_sel_hi:[1,0]
	v_pk_mul_f32 v[26:27], v[26:27], s[4:5] op_sel_hi:[1,0]
	v_pk_mul_f32 v[28:29], v[28:29], s[4:5] op_sel_hi:[1,0]
	v_pk_mul_f32 v[22:23], v[22:23], s[4:5] op_sel_hi:[1,0]
	v_pk_mul_f32 v[24:25], v[24:25], s[4:5] op_sel_hi:[1,0]
	v_add_u32_e32 v18, 0x107f4, v18
	v_pk_fma_f32 v[80:81], v[94:95], v[80:81], v[16:17]
	v_pk_fma_f32 v[78:79], v[96:97], v[78:79], v[14:15]
	v_pk_fma_f32 v[76:77], v[90:91], v[76:77], v[12:13]
	v_pk_fma_f32 v[74:75], v[92:93], v[74:75], v[10:11]
	v_pk_fma_f32 v[72:73], v[86:87], v[72:73], v[8:9]
	v_pk_fma_f32 v[70:71], v[88:89], v[70:71], v[6:7]
	v_pk_fma_f32 v[64:65], v[94:95], v[64:65], v[16:17]
	v_pk_fma_f32 v[62:63], v[96:97], v[62:63], v[14:15]
	v_pk_fma_f32 v[60:61], v[90:91], v[60:61], v[12:13]
	v_pk_fma_f32 v[58:59], v[92:93], v[58:59], v[10:11]
	v_pk_fma_f32 v[56:57], v[86:87], v[56:57], v[8:9]
	v_pk_fma_f32 v[54:55], v[88:89], v[54:55], v[6:7]
	v_pk_fma_f32 v[48:49], v[94:95], v[48:49], v[16:17]
	v_pk_fma_f32 v[46:47], v[96:97], v[46:47], v[14:15]
	v_pk_fma_f32 v[44:45], v[90:91], v[44:45], v[12:13]
	v_pk_fma_f32 v[42:43], v[92:93], v[42:43], v[10:11]
	v_pk_fma_f32 v[40:41], v[86:87], v[40:41], v[8:9]
	v_pk_fma_f32 v[38:39], v[88:89], v[38:39], v[6:7]
	v_pk_fma_f32 v[32:33], v[94:95], v[32:33], v[16:17]
	v_pk_fma_f32 v[30:31], v[96:97], v[30:31], v[14:15]
	v_pk_fma_f32 v[28:29], v[90:91], v[28:29], v[12:13]
	v_pk_fma_f32 v[26:27], v[92:93], v[26:27], v[10:11]
	v_pk_fma_f32 v[24:25], v[86:87], v[24:25], v[8:9]
	v_pk_fma_f32 v[22:23], v[88:89], v[22:23], v[6:7]
	s_and_b64 s[4:5], vcc, exec
	v_ashrrev_i32_e32 v19, 31, v18
	v_cvt_pk_bf16_f32 v78, v78, v79
	v_cvt_pk_bf16_f32 v79, v80, v81
	v_cvt_pk_bf16_f32 v74, v74, v75
	v_cvt_pk_bf16_f32 v75, v76, v77
	v_cvt_pk_bf16_f32 v70, v70, v71
	v_cvt_pk_bf16_f32 v71, v72, v73
	v_cvt_pk_bf16_f32 v62, v62, v63
	v_cvt_pk_bf16_f32 v63, v64, v65
	v_cvt_pk_bf16_f32 v58, v58, v59
	v_cvt_pk_bf16_f32 v59, v60, v61
	v_cvt_pk_bf16_f32 v54, v54, v55
	v_cvt_pk_bf16_f32 v55, v56, v57
	v_cvt_pk_bf16_f32 v46, v46, v47
	v_cvt_pk_bf16_f32 v47, v48, v49
	v_cvt_pk_bf16_f32 v42, v42, v43
	v_cvt_pk_bf16_f32 v43, v44, v45
	v_cvt_pk_bf16_f32 v38, v38, v39
	v_cvt_pk_bf16_f32 v39, v40, v41
	v_cvt_pk_bf16_f32 v30, v30, v31
	v_cvt_pk_bf16_f32 v31, v32, v33
	v_cvt_pk_bf16_f32 v26, v26, v27
	v_cvt_pk_bf16_f32 v27, v28, v29
	v_cvt_pk_bf16_f32 v22, v22, v23
	v_cvt_pk_bf16_f32 v23, v24, v25
	s_cselect_b32 s5, s9, s7
	s_cselect_b32 s4, s8, s6
	v_lshlrev_b64 v[18:19], 12, v[18:19]
	global_store_dwordx2 v[100:101], v[78:79], off
	global_store_dwordx2 v[100:101], v[74:75], off offset:512
	global_store_dwordx2 v[100:101], v[70:71], off offset:1024
	global_store_dwordx2 v[66:67], v[62:63], off
	global_store_dwordx2 v[66:67], v[58:59], off offset:512
	global_store_dwordx2 v[66:67], v[54:55], off offset:1024
	global_store_dwordx2 v[50:51], v[46:47], off
	global_store_dwordx2 v[50:51], v[42:43], off offset:512
	global_store_dwordx2 v[50:51], v[38:39], off offset:1024
	global_store_dwordx2 v[34:35], v[30:31], off
	global_store_dwordx2 v[34:35], v[26:27], off offset:512
	global_store_dwordx2 v[34:35], v[22:23], off offset:1024
	v_lshl_add_u64 v[18:19], s[4:5], 0, v[18:19]
	s_cmpk_lt_i32 s21, 0x1ffb
	v_lshl_add_u64 v[18:19], v[18:19], 0, v[152:153]
	s_cselect_b64 vcc, -1, 0
	global_load_dwordx4 v[62:65], v[18:19], off
; __device__ __forceinline__ unsigned cvtpk(float lo, float hi) { f32x2 v = {lo, hi}; bf16x2_t b = __builtin_convertvector(v, bf16x2_t); return __builtin_bit_cast(unsigned, b); }
; __device__ __forceinline__ float* xrow_ptr(float* xl, float* xc, int b, int t) { return (t < SEQ) ? xl + ((size_t)(b * SEQ + t)) * DM : xc + ((size_t)(b * CTXL + (t - SEQ))) * DM; }
; #define xl OUTP(launder(kargs))
; __device__ __forceinline__ void norm2_block(float* xl, float* xc, const float* MOD, const float* gn, const float* WP, bf16_t* H, float* AFF, int L, int row0, int nrows, int lane) {
;     ...
;     for (int r4 = 0; r4 < 4; ++r4) {
;         if (r4 * 4 < nrows) {
;             f32x4 v[4][4];
; #pragma unroll
;             for (int k = 0; k < 4; ++k) { const float* xq = xrow_ptr(xl, xc, b, t0 + r4 * 4 + k);
; #pragma unroll
;                 for (int j = 0; j < 4; ++j) v[k][j] = *(const f32x4*)(xq + 256 * j + 4 * lane); }
; #pragma unroll
;             for (int k = 0; k < 4; ++k) { const float rs = __builtin_bit_cast(float, __builtin_amdgcn_readlane(__builtin_bit_cast(int, rstd), r4 * 4 + k));
;                 bf16_t* hr = H + (size_t)(row0 + r4 * 4 + k) * DM;
; #pragma unroll
;                 for (int j = 0; j < 4; ++j) { const f32x4 h = (v[k][j] * rs) * mg[j] + sf[j]; u32x2 w; w.x = cvtpk(h[0], h[1]); w.y = cvtpk(h[2], h[3]); *(u32x2*)(hr + 256 * j + 4 * lane) = w; } }
;             asm volatile("" ::: "memory");
	global_load_dwordx4 v[58:61], v[18:19], off offset:1024
	global_load_dwordx4 v[54:57], v[18:19], off offset:2048
	global_load_dwordx4 v[50:53], v[18:19], off offset:3072
	v_cndmask_b32_e32 v18, v170, v169, vcc
	v_add_u32_e32 v18, s20, v18
	v_add_u32_e32 v18, 0x107f5, v18
	s_and_b64 s[4:5], vcc, exec
	v_ashrrev_i32_e32 v19, 31, v18
	s_cselect_b32 s5, s9, s7
	s_cselect_b32 s4, s8, s6
	v_lshlrev_b64 v[18:19], 12, v[18:19]
	v_lshl_add_u64 v[18:19], s[4:5], 0, v[18:19]
	s_cmpk_lt_i32 s21, 0x1ffa
	v_lshl_add_u64 v[18:19], v[18:19], 0, v[152:153]
	s_cselect_b64 vcc, -1, 0
	global_load_dwordx4 v[46:49], v[18:19], off
	global_load_dwordx4 v[42:45], v[18:19], off offset:1024
	global_load_dwordx4 v[38:41], v[18:19], off offset:2048
	global_load_dwordx4 v[34:37], v[18:19], off offset:3072
	v_cndmask_b32_e32 v18, v170, v169, vcc
	v_add_u32_e32 v18, s20, v18
	v_add_u32_e32 v18, 0x107f6, v18
	s_and_b64 s[4:5], vcc, exec
	s_cselect_b32 s5, s9, s7
	s_cselect_b32 s4, s8, s6
	v_ashrrev_i32_e32 v19, 31, v18
	s_cmpk_lt_i32 s21, 0x1ff9
	v_lshlrev_b64 v[18:19], 12, v[18:19]
	s_cselect_b64 vcc, -1, 0
	v_lshl_add_u64 v[18:19], s[4:5], 0, v[18:19]
	v_cndmask_b32_e32 v66, v170, v169, vcc
	v_lshl_add_u64 v[18:19], v[18:19], 0, v[152:153]
	v_add_u32_e32 v66, s20, v66
	global_load_dwordx4 v[30:33], v[18:19], off
	global_load_dwordx4 v[26:29], v[18:19], off offset:1024
	global_load_dwordx4 v[22:25], v[18:19], off offset:2048
	s_nop 0
	global_load_dwordx4 v[18:21], v[18:19], off offset:3072
	v_add_u32_e32 v66, 0x107f7, v66
	s_and_b64 s[4:5], vcc, exec
	v_ashrrev_i32_e32 v67, 31, v66
	s_cselect_b32 s5, s9, s7
	s_cselect_b32 s4, s8, s6
	v_lshlrev_b64 v[66:67], 12, v[66:67]
	v_lshl_add_u64 v[66:67], s[4:5], 0, v[66:67]
	v_lshl_add_u64 v[66:67], v[66:67], 0, v[152:153]
	global_load_dwordx4 v[78:81], v[66:67], off
	global_load_dwordx4 v[74:77], v[66:67], off offset:1024
	global_load_dwordx4 v[70:73], v[66:67], off offset:2048
	s_nop 0
	global_load_dwordx4 v[66:69], v[66:67], off offset:3072
	v_readlane_b32 s4, v98, 4
	s_add_i32 s38, s16, 0x107f4
	s_lshl_b64 s[10:11], s[38:39], 11
	s_add_i32 s38, s16, 0x107f5
	v_lshl_add_u64 v[100:101], v[150:151], 0, s[10:11]
	s_lshl_b64 s[10:11], s[38:39], 11
	s_add_i32 s38, s16, 0x107f6
	s_waitcnt vmcnt(15)
	v_pk_mul_f32 v[62:63], v[62:63], s[4:5] op_sel_hi:[1,0]
	v_pk_mul_f32 v[64:65], v[64:65], s[4:5] op_sel_hi:[1,0]
	s_waitcnt vmcnt(14)
	v_pk_mul_f32 v[58:59], v[58:59], s[4:5] op_sel_hi:[1,0]
	v_pk_mul_f32 v[60:61], v[60:61], s[4:5] op_sel_hi:[1,0]
	s_waitcnt vmcnt(13)
	v_pk_mul_f32 v[54:55], v[54:55], s[4:5] op_sel_hi:[1,0]
	v_pk_mul_f32 v[56:57], v[56:57], s[4:5] op_sel_hi:[1,0]
	s_waitcnt vmcnt(12)
	v_pk_mul_f32 v[50:51], v[50:51], s[4:5] op_sel_hi:[1,0]
	v_pk_mul_f32 v[52:53], v[52:53], s[4:5] op_sel_hi:[1,0]
	v_readlane_b32 s4, v98, 5
	v_pk_fma_f32 v[52:53], v[82:83], v[52:53], v[4:5]
	v_pk_fma_f32 v[50:51], v[84:85], v[50:51], v[2:3]
	v_pk_fma_f32 v[64:65], v[94:95], v[64:65], v[16:17]
	v_cvt_pk_bf16_f32 v50, v50, v51
	s_waitcnt vmcnt(11)
	v_pk_mul_f32 v[46:47], v[46:47], s[4:5] op_sel_hi:[1,0]
	v_pk_mul_f32 v[48:49], v[48:49], s[4:5] op_sel_hi:[1,0]
	s_waitcnt vmcnt(10)
	v_pk_mul_f32 v[42:43], v[42:43], s[4:5] op_sel_hi:[1,0]
	v_pk_mul_f32 v[44:45], v[44:45], s[4:5] op_sel_hi:[1,0]
	s_waitcnt vmcnt(9)
	v_pk_mul_f32 v[38:39], v[38:39], s[4:5] op_sel_hi:[1,0]
	v_pk_mul_f32 v[40:41], v[40:41], s[4:5] op_sel_hi:[1,0]
	s_waitcnt vmcnt(8)
	v_pk_mul_f32 v[34:35], v[34:35], s[4:5] op_sel_hi:[1,0]
	v_pk_mul_f32 v[36:37], v[36:37], s[4:5] op_sel_hi:[1,0]
	v_readlane_b32 s4, v98, 6
	v_cvt_pk_bf16_f32 v51, v52, v53
	v_pk_fma_f32 v[36:37], v[82:83], v[36:37], v[4:5]
	v_pk_fma_f32 v[34:35], v[84:85], v[34:35], v[2:3]
	global_store_dwordx2 v[100:101], v[50:51], off offset:1536
	v_lshl_add_u64 v[50:51], v[150:151], 0, s[10:11]
	v_cvt_pk_bf16_f32 v34, v34, v35
	v_cvt_pk_bf16_f32 v35, v36, v37
	s_lshl_b64 s[10:11], s[38:39], 11
	s_waitcnt vmcnt(6)
	v_pk_mul_f32 v[22:23], v[22:23], s[4:5] op_sel_hi:[1,0]
	v_pk_mul_f32 v[24:25], v[24:25], s[4:5] op_sel_hi:[1,0]
	v_pk_fma_f32 v[22:23], v[88:89], v[22:23], v[6:7]
	v_pk_fma_f32 v[24:25], v[86:87], v[24:25], v[8:9]
	s_waitcnt vmcnt(5)
	v_pk_mul_f32 v[18:19], v[18:19], s[4:5] op_sel_hi:[1,0]
	v_pk_mul_f32 v[20:21], v[20:21], s[4:5] op_sel_hi:[1,0]
	global_store_dwordx2 v[50:51], v[34:35], off offset:1536
	v_lshl_add_u64 v[34:35], v[150:151], 0, s[10:11]
	v_pk_mul_f32 v[30:31], v[30:31], s[4:5] op_sel_hi:[1,0]
	v_pk_mul_f32 v[32:33], v[32:33], s[4:5] op_sel_hi:[1,0]
	v_pk_mul_f32 v[26:27], v[26:27], s[4:5] op_sel_hi:[1,0]
	v_pk_mul_f32 v[28:29], v[28:29], s[4:5] op_sel_hi:[1,0]
	v_cvt_pk_bf16_f32 v22, v22, v23
	v_cvt_pk_bf16_f32 v23, v24, v25
	v_pk_fma_f32 v[20:21], v[82:83], v[20:21], v[4:5]
	v_pk_fma_f32 v[18:19], v[84:85], v[18:19], v[2:3]
	v_readlane_b32 s4, v98, 7
	global_store_dwordx2 v[34:35], v[22:23], off offset:1024
	v_cvt_pk_bf16_f32 v18, v18, v19
	v_cvt_pk_bf16_f32 v19, v20, v21
	s_add_i32 s38, s16, 0x107f7
	s_waitcnt vmcnt(6)
	v_pk_mul_f32 v[20:21], v[78:79], s[4:5] op_sel_hi:[1,0]
	v_pk_mul_f32 v[22:23], v[80:81], s[4:5] op_sel_hi:[1,0]
	s_lshl_b64 s[10:11], s[38:39], 11
	v_pk_fma_f32 v[22:23], v[94:95], v[22:23], v[16:17]
	v_pk_fma_f32 v[20:21], v[96:97], v[20:21], v[14:15]
	global_store_dwordx2 v[34:35], v[18:19], off offset:1536
	v_lshl_add_u64 v[18:19], v[150:151], 0, s[10:11]
	v_cvt_pk_bf16_f32 v20, v20, v21
	v_cvt_pk_bf16_f32 v21, v22, v23
	global_store_dwordx2 v[18:19], v[20:21], off
	s_waitcnt vmcnt(7)
; __device__ __forceinline__ unsigned cvtpk(float lo, float hi) { f32x2 v = {lo, hi}; bf16x2_t b = __builtin_convertvector(v, bf16x2_t); return __builtin_bit_cast(unsigned, b); }
; __device__ __forceinline__ float* xrow_ptr(float* xl, float* xc, int b, int t) { return (t < SEQ) ? xl + ((size_t)(b * SEQ + t)) * DM : xc + ((size_t)(b * CTXL + (t - SEQ))) * DM; }
; #define xl OUTP(launder(kargs))
; __device__ __forceinline__ void norm2_block(float* xl, float* xc, const float* MOD, const float* gn, const float* WP, bf16_t* H, float* AFF, int L, int row0, int nrows, int lane) {
;     ...
;     for (int r4 = 0; r4 < 4; ++r4) {
;         if (r4 * 4 < nrows) {
;             f32x4 v[4][4];
; #pragma unroll
;             for (int k = 0; k < 4; ++k) { const float* xq = xrow_ptr(xl, xc, b, t0 + r4 * 4 + k);
; #pragma unroll
;                 for (int j = 0; j < 4; ++j) v[k][j] = *(const f32x4*)(xq + 256 * j + 4 * lane); }
; #pragma unroll
;             for (int k = 0; k < 4; ++k) { const float rs = __builtin_bit_cast(float, __builtin_amdgcn_readlane(__builtin_bit_cast(int, rstd), r4 * 4 + k));
;                 bf16_t* hr = H + (size_t)(row0 + r4 * 4 + k) * DM;
; #pragma unroll
;                 for (int j = 0; j < 4; ++j) { const f32x4 h = (v[k][j] * rs) * mg[j] + sf[j]; u32x2 w; w.x = cvtpk(h[0], h[1]); w.y = cvtpk(h[2], h[3]); *(u32x2*)(hr + 256 * j + 4 * lane) = w; } }
;             asm volatile("" ::: "memory");
	v_pk_mul_f32 v[20:21], v[74:75], s[4:5] op_sel_hi:[1,0]
	v_pk_mul_f32 v[22:23], v[76:77], s[4:5] op_sel_hi:[1,0]
	v_pk_fma_f32 v[20:21], v[92:93], v[20:21], v[10:11]
	v_pk_fma_f32 v[22:23], v[90:91], v[22:23], v[12:13]
	v_cvt_pk_bf16_f32 v20, v20, v21
	v_cvt_pk_bf16_f32 v21, v22, v23
	global_store_dwordx2 v[18:19], v[20:21], off offset:512
	s_waitcnt vmcnt(7)
	v_pk_mul_f32 v[20:21], v[70:71], s[4:5] op_sel_hi:[1,0]
	v_pk_mul_f32 v[22:23], v[72:73], s[4:5] op_sel_hi:[1,0]
	v_pk_fma_f32 v[20:21], v[88:89], v[20:21], v[6:7]
	v_pk_fma_f32 v[22:23], v[86:87], v[22:23], v[8:9]
	v_cvt_pk_bf16_f32 v20, v20, v21
	v_cvt_pk_bf16_f32 v21, v22, v23
	global_store_dwordx2 v[18:19], v[20:21], off offset:1024
	s_waitcnt vmcnt(7)
	v_pk_mul_f32 v[20:21], v[66:67], s[4:5] op_sel_hi:[1,0]
	v_pk_mul_f32 v[22:23], v[68:69], s[4:5] op_sel_hi:[1,0]
	v_pk_fma_f32 v[20:21], v[84:85], v[20:21], v[2:3]
	v_pk_fma_f32 v[22:23], v[82:83], v[22:23], v[4:5]
	s_cmpk_lt_i32 s21, 0x1ff8
	v_cvt_pk_bf16_f32 v20, v20, v21
	v_cvt_pk_bf16_f32 v21, v22, v23
	s_cselect_b64 vcc, -1, 0
	global_store_dwordx2 v[18:19], v[20:21], off offset:1536
	v_cndmask_b32_e32 v18, v170, v169, vcc
	v_add_u32_e32 v18, s20, v18
	v_add_u32_e32 v18, 0x107f8, v18
	v_pk_fma_f32 v[62:63], v[96:97], v[62:63], v[14:15]
	v_pk_fma_f32 v[60:61], v[90:91], v[60:61], v[12:13]
	v_pk_fma_f32 v[58:59], v[92:93], v[58:59], v[10:11]
	v_pk_fma_f32 v[56:57], v[86:87], v[56:57], v[8:9]
	v_pk_fma_f32 v[54:55], v[88:89], v[54:55], v[6:7]
	v_pk_fma_f32 v[48:49], v[94:95], v[48:49], v[16:17]
	v_pk_fma_f32 v[46:47], v[96:97], v[46:47], v[14:15]
	v_pk_fma_f32 v[44:45], v[90:91], v[44:45], v[12:13]
	v_pk_fma_f32 v[42:43], v[92:93], v[42:43], v[10:11]
	v_pk_fma_f32 v[40:41], v[86:87], v[40:41], v[8:9]
	v_pk_fma_f32 v[38:39], v[88:89], v[38:39], v[6:7]
	v_pk_fma_f32 v[32:33], v[94:95], v[32:33], v[16:17]
	v_pk_fma_f32 v[30:31], v[96:97], v[30:31], v[14:15]
	v_pk_fma_f32 v[28:29], v[90:91], v[28:29], v[12:13]
	v_pk_fma_f32 v[26:27], v[92:93], v[26:27], v[10:11]
	s_and_b64 s[4:5], vcc, exec
	v_ashrrev_i32_e32 v19, 31, v18
	v_cvt_pk_bf16_f32 v62, v62, v63
	v_cvt_pk_bf16_f32 v63, v64, v65
	v_cvt_pk_bf16_f32 v58, v58, v59
	v_cvt_pk_bf16_f32 v59, v60, v61
	v_cvt_pk_bf16_f32 v54, v54, v55
	v_cvt_pk_bf16_f32 v55, v56, v57
	v_cvt_pk_bf16_f32 v46, v46, v47
	v_cvt_pk_bf16_f32 v47, v48, v49
	v_cvt_pk_bf16_f32 v42, v42, v43
	v_cvt_pk_bf16_f32 v43, v44, v45
	v_cvt_pk_bf16_f32 v38, v38, v39
	v_cvt_pk_bf16_f32 v39, v40, v41
	v_cvt_pk_bf16_f32 v30, v30, v31
	v_cvt_pk_bf16_f32 v31, v32, v33
	v_cvt_pk_bf16_f32 v26, v26, v27
	v_cvt_pk_bf16_f32 v27, v28, v29
	s_cselect_b32 s5, s9, s7
	s_cselect_b32 s4, s8, s6
	v_lshlrev_b64 v[18:19], 12, v[18:19]
	global_store_dwordx2 v[100:101], v[62:63], off
	global_store_dwordx2 v[100:101], v[58:59], off offset:512
	global_store_dwordx2 v[100:101], v[54:55], off offset:1024
	global_store_dwordx2 v[50:51], v[46:47], off
	global_store_dwordx2 v[50:51], v[42:43], off offset:512
	global_store_dwordx2 v[50:51], v[38:39], off offset:1024
	global_store_dwordx2 v[34:35], v[30:31], off
	global_store_dwordx2 v[34:35], v[26:27], off offset:512
	v_lshl_add_u64 v[18:19], s[4:5], 0, v[18:19]
	s_cmpk_lt_i32 s21, 0x1ff7
	v_lshl_add_u64 v[18:19], v[18:19], 0, v[152:153]
	s_cselect_b64 vcc, -1, 0
	global_load_dwordx4 v[62:65], v[18:19], off
	global_load_dwordx4 v[58:61], v[18:19], off offset:1024
	global_load_dwordx4 v[54:57], v[18:19], off offset:2048
	global_load_dwordx4 v[50:53], v[18:19], off offset:3072
	v_cndmask_b32_e32 v18, v170, v169, vcc
	v_add_u32_e32 v18, s20, v18
	v_add_u32_e32 v18, 0x107f9, v18
	s_and_b64 s[4:5], vcc, exec
	v_ashrrev_i32_e32 v19, 31, v18
	s_cselect_b32 s5, s9, s7
	s_cselect_b32 s4, s8, s6
	v_lshlrev_b64 v[18:19], 12, v[18:19]
	v_lshl_add_u64 v[18:19], s[4:5], 0, v[18:19]
	s_cmpk_lt_i32 s21, 0x1ff6
	v_lshl_add_u64 v[18:19], v[18:19], 0, v[152:153]
	s_cselect_b64 vcc, -1, 0
	global_load_dwordx4 v[46:49], v[18:19], off
	global_load_dwordx4 v[42:45], v[18:19], off offset:1024
	global_load_dwordx4 v[38:41], v[18:19], off offset:2048
	global_load_dwordx4 v[34:37], v[18:19], off offset:3072
	v_cndmask_b32_e32 v18, v170, v169, vcc
	v_add_u32_e32 v18, s20, v18
	v_add_u32_e32 v18, 0x107fa, v18
	s_and_b64 s[4:5], vcc, exec
	s_cselect_b32 s5, s9, s7
	s_cselect_b32 s4, s8, s6
	v_ashrrev_i32_e32 v19, 31, v18
	s_cmpk_lt_i32 s21, 0x1ff5
	v_lshlrev_b64 v[18:19], 12, v[18:19]
	s_cselect_b64 vcc, -1, 0
	v_lshl_add_u64 v[18:19], s[4:5], 0, v[18:19]
	v_cndmask_b32_e32 v66, v170, v169, vcc
	v_lshl_add_u64 v[18:19], v[18:19], 0, v[152:153]
	v_add_u32_e32 v66, s20, v66
	global_load_dwordx4 v[30:33], v[18:19], off
	global_load_dwordx4 v[26:29], v[18:19], off offset:1024
	global_load_dwordx4 v[22:25], v[18:19], off offset:2048
	s_nop 0
	global_load_dwordx4 v[18:21], v[18:19], off offset:3072
	v_add_u32_e32 v66, 0x107fb, v66
	s_and_b64 s[4:5], vcc, exec
	v_ashrrev_i32_e32 v67, 31, v66
	s_cselect_b32 s5, s9, s7
	s_cselect_b32 s4, s8, s6
	v_lshlrev_b64 v[66:67], 12, v[66:67]
	v_lshl_add_u64 v[66:67], s[4:5], 0, v[66:67]
	v_lshl_add_u64 v[66:67], v[66:67], 0, v[152:153]
	global_load_dwordx4 v[78:81], v[66:67], off
	global_load_dwordx4 v[74:77], v[66:67], off offset:1024
	global_load_dwordx4 v[70:73], v[66:67], off offset:2048
	s_nop 0
	global_load_dwordx4 v[66:69], v[66:67], off offset:3072
	v_readlane_b32 s4, v98, 8
	s_add_i32 s38, s16, 0x107f8
	s_lshl_b64 s[10:11], s[38:39], 11
	s_add_i32 s38, s16, 0x107f9
	v_lshl_add_u64 v[100:101], v[150:151], 0, s[10:11]
	s_lshl_b64 s[10:11], s[38:39], 11
	s_add_i32 s38, s16, 0x107fa
	s_waitcnt vmcnt(15)
	v_pk_mul_f32 v[62:63], v[62:63], s[4:5] op_sel_hi:[1,0]
	v_pk_mul_f32 v[64:65], v[64:65], s[4:5] op_sel_hi:[1,0]
	s_waitcnt vmcnt(14)
; __device__ __forceinline__ unsigned cvtpk(float lo, float hi) { f32x2 v = {lo, hi}; bf16x2_t b = __builtin_convertvector(v, bf16x2_t); return __builtin_bit_cast(unsigned, b); }
; __device__ __forceinline__ float* xrow_ptr(float* xl, float* xc, int b, int t) { return (t < SEQ) ? xl + ((size_t)(b * SEQ + t)) * DM : xc + ((size_t)(b * CTXL + (t - SEQ))) * DM; }
; #define xl OUTP(launder(kargs))
; __device__ __forceinline__ void norm2_block(float* xl, float* xc, const float* MOD, const float* gn, const float* WP, bf16_t* H, float* AFF, int L, int row0, int nrows, int lane) {
;     ...
;     for (int r4 = 0; r4 < 4; ++r4) {
;         if (r4 * 4 < nrows) {
;             f32x4 v[4][4];
; #pragma unroll
;             for (int k = 0; k < 4; ++k) { const float* xq = xrow_ptr(xl, xc, b, t0 + r4 * 4 + k);
; #pragma unroll
;                 for (int j = 0; j < 4; ++j) v[k][j] = *(const f32x4*)(xq + 256 * j + 4 * lane); }
; #pragma unroll
;             for (int k = 0; k < 4; ++k) { const float rs = __builtin_bit_cast(float, __builtin_amdgcn_readlane(__builtin_bit_cast(int, rstd), r4 * 4 + k));
;                 bf16_t* hr = H + (size_t)(row0 + r4 * 4 + k) * DM;
; #pragma unroll
;                 for (int j = 0; j < 4; ++j) { const f32x4 h = (v[k][j] * rs) * mg[j] + sf[j]; u32x2 w; w.x = cvtpk(h[0], h[1]); w.y = cvtpk(h[2], h[3]); *(u32x2*)(hr + 256 * j + 4 * lane) = w; } }
;             asm volatile("" ::: "memory");
	v_pk_mul_f32 v[58:59], v[58:59], s[4:5] op_sel_hi:[1,0]
	v_pk_mul_f32 v[60:61], v[60:61], s[4:5] op_sel_hi:[1,0]
	s_waitcnt vmcnt(13)
	v_pk_mul_f32 v[54:55], v[54:55], s[4:5] op_sel_hi:[1,0]
	v_pk_mul_f32 v[56:57], v[56:57], s[4:5] op_sel_hi:[1,0]
	s_waitcnt vmcnt(12)
	v_pk_mul_f32 v[50:51], v[50:51], s[4:5] op_sel_hi:[1,0]
	v_pk_mul_f32 v[52:53], v[52:53], s[4:5] op_sel_hi:[1,0]
	v_readlane_b32 s4, v98, 9
	v_pk_fma_f32 v[52:53], v[82:83], v[52:53], v[4:5]
	v_pk_fma_f32 v[50:51], v[84:85], v[50:51], v[2:3]
	v_pk_fma_f32 v[64:65], v[94:95], v[64:65], v[16:17]
	v_cvt_pk_bf16_f32 v50, v50, v51
	s_waitcnt vmcnt(11)
	v_pk_mul_f32 v[46:47], v[46:47], s[4:5] op_sel_hi:[1,0]
	v_pk_mul_f32 v[48:49], v[48:49], s[4:5] op_sel_hi:[1,0]
	s_waitcnt vmcnt(10)
	v_pk_mul_f32 v[42:43], v[42:43], s[4:5] op_sel_hi:[1,0]
	v_pk_mul_f32 v[44:45], v[44:45], s[4:5] op_sel_hi:[1,0]
	s_waitcnt vmcnt(9)
	v_pk_mul_f32 v[38:39], v[38:39], s[4:5] op_sel_hi:[1,0]
	v_pk_mul_f32 v[40:41], v[40:41], s[4:5] op_sel_hi:[1,0]
	s_waitcnt vmcnt(8)
	v_pk_mul_f32 v[34:35], v[34:35], s[4:5] op_sel_hi:[1,0]
	v_pk_mul_f32 v[36:37], v[36:37], s[4:5] op_sel_hi:[1,0]
	v_readlane_b32 s4, v98, 10
	v_cvt_pk_bf16_f32 v51, v52, v53
	v_pk_fma_f32 v[36:37], v[82:83], v[36:37], v[4:5]
	v_pk_fma_f32 v[34:35], v[84:85], v[34:35], v[2:3]
	global_store_dwordx2 v[100:101], v[50:51], off offset:1536
	v_lshl_add_u64 v[50:51], v[150:151], 0, s[10:11]
	v_cvt_pk_bf16_f32 v34, v34, v35
	v_cvt_pk_bf16_f32 v35, v36, v37
	s_lshl_b64 s[10:11], s[38:39], 11
	s_waitcnt vmcnt(6)
	v_pk_mul_f32 v[22:23], v[22:23], s[4:5] op_sel_hi:[1,0]
	v_pk_mul_f32 v[24:25], v[24:25], s[4:5] op_sel_hi:[1,0]
	v_pk_fma_f32 v[22:23], v[88:89], v[22:23], v[6:7]
	v_pk_fma_f32 v[24:25], v[86:87], v[24:25], v[8:9]
	s_waitcnt vmcnt(5)
	v_pk_mul_f32 v[18:19], v[18:19], s[4:5] op_sel_hi:[1,0]
	v_pk_mul_f32 v[20:21], v[20:21], s[4:5] op_sel_hi:[1,0]
	global_store_dwordx2 v[50:51], v[34:35], off offset:1536
	v_lshl_add_u64 v[34:35], v[150:151], 0, s[10:11]
	v_pk_mul_f32 v[30:31], v[30:31], s[4:5] op_sel_hi:[1,0]
	v_pk_mul_f32 v[32:33], v[32:33], s[4:5] op_sel_hi:[1,0]
	v_pk_mul_f32 v[26:27], v[26:27], s[4:5] op_sel_hi:[1,0]
	v_pk_mul_f32 v[28:29], v[28:29], s[4:5] op_sel_hi:[1,0]
	v_cvt_pk_bf16_f32 v22, v22, v23
	v_cvt_pk_bf16_f32 v23, v24, v25
	v_pk_fma_f32 v[20:21], v[82:83], v[20:21], v[4:5]
	v_pk_fma_f32 v[18:19], v[84:85], v[18:19], v[2:3]
	v_readlane_b32 s4, v98, 11
	global_store_dwordx2 v[34:35], v[22:23], off offset:1024
	v_cvt_pk_bf16_f32 v18, v18, v19
	v_cvt_pk_bf16_f32 v19, v20, v21
	s_add_i32 s38, s16, 0x107fb
	s_waitcnt vmcnt(6)
	v_pk_mul_f32 v[20:21], v[78:79], s[4:5] op_sel_hi:[1,0]
	v_pk_mul_f32 v[22:23], v[80:81], s[4:5] op_sel_hi:[1,0]
	s_lshl_b64 s[10:11], s[38:39], 11
	v_pk_fma_f32 v[22:23], v[94:95], v[22:23], v[16:17]
	v_pk_fma_f32 v[20:21], v[96:97], v[20:21], v[14:15]
	global_store_dwordx2 v[34:35], v[18:19], off offset:1536
	v_lshl_add_u64 v[18:19], v[150:151], 0, s[10:11]
	v_cvt_pk_bf16_f32 v20, v20, v21
	v_cvt_pk_bf16_f32 v21, v22, v23
	global_store_dwordx2 v[18:19], v[20:21], off
	s_waitcnt vmcnt(7)
	v_pk_mul_f32 v[20:21], v[74:75], s[4:5] op_sel_hi:[1,0]
	v_pk_mul_f32 v[22:23], v[76:77], s[4:5] op_sel_hi:[1,0]
	v_pk_fma_f32 v[20:21], v[92:93], v[20:21], v[10:11]
	v_pk_fma_f32 v[22:23], v[90:91], v[22:23], v[12:13]
	v_cvt_pk_bf16_f32 v20, v20, v21
	v_cvt_pk_bf16_f32 v21, v22, v23
	global_store_dwordx2 v[18:19], v[20:21], off offset:512
	s_waitcnt vmcnt(7)
	v_pk_mul_f32 v[20:21], v[70:71], s[4:5] op_sel_hi:[1,0]
	v_pk_mul_f32 v[22:23], v[72:73], s[4:5] op_sel_hi:[1,0]
	v_pk_fma_f32 v[20:21], v[88:89], v[20:21], v[6:7]
	v_pk_fma_f32 v[22:23], v[86:87], v[22:23], v[8:9]
	v_cvt_pk_bf16_f32 v20, v20, v21
	v_cvt_pk_bf16_f32 v21, v22, v23
	global_store_dwordx2 v[18:19], v[20:21], off offset:1024
	s_waitcnt vmcnt(7)
	v_pk_mul_f32 v[20:21], v[66:67], s[4:5] op_sel_hi:[1,0]
	v_pk_mul_f32 v[22:23], v[68:69], s[4:5] op_sel_hi:[1,0]
	v_pk_fma_f32 v[20:21], v[84:85], v[20:21], v[2:3]
	v_pk_fma_f32 v[22:23], v[82:83], v[22:23], v[4:5]
	s_cmpk_lt_i32 s21, 0x1ff4
	v_cvt_pk_bf16_f32 v20, v20, v21
	v_cvt_pk_bf16_f32 v21, v22, v23
	s_cselect_b64 vcc, -1, 0
	global_store_dwordx2 v[18:19], v[20:21], off offset:1536
	v_cndmask_b32_e32 v18, v170, v169, vcc
	v_add_u32_e32 v18, s20, v18
	v_add_u32_e32 v18, 0x107fc, v18
	v_pk_fma_f32 v[62:63], v[96:97], v[62:63], v[14:15]
	v_pk_fma_f32 v[60:61], v[90:91], v[60:61], v[12:13]
	v_pk_fma_f32 v[58:59], v[92:93], v[58:59], v[10:11]
	v_pk_fma_f32 v[56:57], v[86:87], v[56:57], v[8:9]
	v_pk_fma_f32 v[54:55], v[88:89], v[54:55], v[6:7]
	v_pk_fma_f32 v[48:49], v[94:95], v[48:49], v[16:17]
	v_pk_fma_f32 v[46:47], v[96:97], v[46:47], v[14:15]
	v_pk_fma_f32 v[44:45], v[90:91], v[44:45], v[12:13]
	v_pk_fma_f32 v[42:43], v[92:93], v[42:43], v[10:11]
	v_pk_fma_f32 v[40:41], v[86:87], v[40:41], v[8:9]
	v_pk_fma_f32 v[38:39], v[88:89], v[38:39], v[6:7]
	v_pk_fma_f32 v[32:33], v[94:95], v[32:33], v[16:17]
	v_pk_fma_f32 v[30:31], v[96:97], v[30:31], v[14:15]
	v_pk_fma_f32 v[28:29], v[90:91], v[28:29], v[12:13]
	v_pk_fma_f32 v[26:27], v[92:93], v[26:27], v[10:11]
	s_and_b64 s[4:5], vcc, exec
	v_ashrrev_i32_e32 v19, 31, v18
	v_cvt_pk_bf16_f32 v62, v62, v63
	v_cvt_pk_bf16_f32 v63, v64, v65
	v_cvt_pk_bf16_f32 v58, v58, v59
	v_cvt_pk_bf16_f32 v59, v60, v61
	v_cvt_pk_bf16_f32 v54, v54, v55
	v_cvt_pk_bf16_f32 v55, v56, v57
	v_cvt_pk_bf16_f32 v46, v46, v47
	v_cvt_pk_bf16_f32 v47, v48, v49
	v_cvt_pk_bf16_f32 v42, v42, v43
	v_cvt_pk_bf16_f32 v43, v44, v45
	v_cvt_pk_bf16_f32 v38, v38, v39
	v_cvt_pk_bf16_f32 v39, v40, v41
	v_cvt_pk_bf16_f32 v30, v30, v31
	v_cvt_pk_bf16_f32 v31, v32, v33
	v_cvt_pk_bf16_f32 v26, v26, v27
; __device__ __forceinline__ unsigned cvtpk(float lo, float hi) { f32x2 v = {lo, hi}; bf16x2_t b = __builtin_convertvector(v, bf16x2_t); return __builtin_bit_cast(unsigned, b); }
; __device__ __forceinline__ float* xrow_ptr(float* xl, float* xc, int b, int t) { return (t < SEQ) ? xl + ((size_t)(b * SEQ + t)) * DM : xc + ((size_t)(b * CTXL + (t - SEQ))) * DM; }
; #define xl OUTP(launder(kargs))
; __device__ __forceinline__ void norm2_block(float* xl, float* xc, const float* MOD, const float* gn, const float* WP, bf16_t* H, float* AFF, int L, int row0, int nrows, int lane) {
;     ...
;     for (int r4 = 0; r4 < 4; ++r4) {
;         if (r4 * 4 < nrows) {
;             f32x4 v[4][4];
; #pragma unroll
;             for (int k = 0; k < 4; ++k) { const float* xq = xrow_ptr(xl, xc, b, t0 + r4 * 4 + k);
; #pragma unroll
;                 for (int j = 0; j < 4; ++j) v[k][j] = *(const f32x4*)(xq + 256 * j + 4 * lane); }
; #pragma unroll
;             for (int k = 0; k < 4; ++k) { const float rs = __builtin_bit_cast(float, __builtin_amdgcn_readlane(__builtin_bit_cast(int, rstd), r4 * 4 + k));
;                 bf16_t* hr = H + (size_t)(row0 + r4 * 4 + k) * DM;
; #pragma unroll
;                 for (int j = 0; j < 4; ++j) { const f32x4 h = (v[k][j] * rs) * mg[j] + sf[j]; u32x2 w; w.x = cvtpk(h[0], h[1]); w.y = cvtpk(h[2], h[3]); *(u32x2*)(hr + 256 * j + 4 * lane) = w; } }
;             asm volatile("" ::: "memory");
	v_cvt_pk_bf16_f32 v27, v28, v29
	s_cselect_b32 s5, s9, s7
	s_cselect_b32 s4, s8, s6
	v_lshlrev_b64 v[18:19], 12, v[18:19]
	global_store_dwordx2 v[100:101], v[62:63], off
	global_store_dwordx2 v[100:101], v[58:59], off offset:512
	global_store_dwordx2 v[100:101], v[54:55], off offset:1024
	global_store_dwordx2 v[50:51], v[46:47], off
	global_store_dwordx2 v[50:51], v[42:43], off offset:512
	global_store_dwordx2 v[50:51], v[38:39], off offset:1024
	global_store_dwordx2 v[34:35], v[30:31], off
	global_store_dwordx2 v[34:35], v[26:27], off offset:512
	v_lshl_add_u64 v[18:19], s[4:5], 0, v[18:19]
	s_cmpk_lt_i32 s21, 0x1ff3
	v_lshl_add_u64 v[18:19], v[18:19], 0, v[152:153]
	s_cselect_b64 vcc, -1, 0
	global_load_dwordx4 v[62:65], v[18:19], off
	global_load_dwordx4 v[58:61], v[18:19], off offset:1024
	global_load_dwordx4 v[54:57], v[18:19], off offset:2048
	global_load_dwordx4 v[50:53], v[18:19], off offset:3072
	v_cndmask_b32_e32 v18, v170, v169, vcc
	v_add_u32_e32 v18, s20, v18
	v_add_u32_e32 v18, 0x107fd, v18
	s_and_b64 s[4:5], vcc, exec
	v_ashrrev_i32_e32 v19, 31, v18
	s_cselect_b32 s5, s9, s7
	s_cselect_b32 s4, s8, s6
	v_lshlrev_b64 v[18:19], 12, v[18:19]
	v_lshl_add_u64 v[18:19], s[4:5], 0, v[18:19]
	s_cmpk_lt_i32 s21, 0x1ff2
	v_lshl_add_u64 v[18:19], v[18:19], 0, v[152:153]
	s_cselect_b64 vcc, -1, 0
	global_load_dwordx4 v[46:49], v[18:19], off
	global_load_dwordx4 v[42:45], v[18:19], off offset:1024
	global_load_dwordx4 v[38:41], v[18:19], off offset:2048
	global_load_dwordx4 v[34:37], v[18:19], off offset:3072
	v_cndmask_b32_e32 v18, v170, v169, vcc
	v_add_u32_e32 v18, s20, v18
	v_add_u32_e32 v18, 0x107fe, v18
	s_and_b64 s[4:5], vcc, exec
	s_cselect_b32 s5, s9, s7
	s_cselect_b32 s4, s8, s6
	v_ashrrev_i32_e32 v19, 31, v18
	s_cmpk_lt_i32 s21, 0x1ff1
	v_lshlrev_b64 v[18:19], 12, v[18:19]
	s_cselect_b64 vcc, -1, 0
	v_lshl_add_u64 v[18:19], s[4:5], 0, v[18:19]
	v_cndmask_b32_e32 v66, v170, v169, vcc
	v_lshl_add_u64 v[18:19], v[18:19], 0, v[152:153]
	v_add_u32_e32 v66, s20, v66
	global_load_dwordx4 v[30:33], v[18:19], off
	global_load_dwordx4 v[26:29], v[18:19], off offset:1024
	global_load_dwordx4 v[22:25], v[18:19], off offset:2048
	s_nop 0
	global_load_dwordx4 v[18:21], v[18:19], off offset:3072
	v_add_u32_e32 v66, 0x107ff, v66
	s_and_b64 s[4:5], vcc, exec
	v_ashrrev_i32_e32 v67, 31, v66
	s_cselect_b32 s5, s9, s7
	s_cselect_b32 s4, s8, s6
	v_lshlrev_b64 v[66:67], 12, v[66:67]
	v_lshl_add_u64 v[66:67], s[4:5], 0, v[66:67]
	v_lshl_add_u64 v[66:67], v[66:67], 0, v[152:153]
	global_load_dwordx4 v[78:81], v[66:67], off
	global_load_dwordx4 v[74:77], v[66:67], off offset:1024
	global_load_dwordx4 v[70:73], v[66:67], off offset:2048
	s_nop 0
	global_load_dwordx4 v[66:69], v[66:67], off offset:3072
	v_readlane_b32 s4, v98, 12
	s_add_i32 s38, s16, 0x107fc
	s_lshl_b64 s[10:11], s[38:39], 11
	s_add_i32 s38, s16, 0x107fd
	v_lshl_add_u64 v[100:101], v[150:151], 0, s[10:11]
	s_lshl_b64 s[10:11], s[38:39], 11
	s_add_i32 s38, s16, 0x107fe
	s_waitcnt vmcnt(15)
	v_pk_mul_f32 v[62:63], v[62:63], s[4:5] op_sel_hi:[1,0]
	v_pk_mul_f32 v[64:65], v[64:65], s[4:5] op_sel_hi:[1,0]
	s_waitcnt vmcnt(14)
	v_pk_mul_f32 v[58:59], v[58:59], s[4:5] op_sel_hi:[1,0]
	v_pk_mul_f32 v[60:61], v[60:61], s[4:5] op_sel_hi:[1,0]
	s_waitcnt vmcnt(13)
	v_pk_mul_f32 v[54:55], v[54:55], s[4:5] op_sel_hi:[1,0]
	v_pk_mul_f32 v[56:57], v[56:57], s[4:5] op_sel_hi:[1,0]
	s_waitcnt vmcnt(12)
	v_pk_mul_f32 v[50:51], v[50:51], s[4:5] op_sel_hi:[1,0]
	v_pk_mul_f32 v[52:53], v[52:53], s[4:5] op_sel_hi:[1,0]
	v_readlane_b32 s4, v98, 13
	v_pk_fma_f32 v[52:53], v[82:83], v[52:53], v[4:5]
	v_pk_fma_f32 v[50:51], v[84:85], v[50:51], v[2:3]
	v_pk_fma_f32 v[64:65], v[94:95], v[64:65], v[16:17]
	v_cvt_pk_bf16_f32 v50, v50, v51
	s_waitcnt vmcnt(11)
	v_pk_mul_f32 v[46:47], v[46:47], s[4:5] op_sel_hi:[1,0]
	v_pk_mul_f32 v[48:49], v[48:49], s[4:5] op_sel_hi:[1,0]
	s_waitcnt vmcnt(10)
	v_pk_mul_f32 v[42:43], v[42:43], s[4:5] op_sel_hi:[1,0]
	v_pk_mul_f32 v[44:45], v[44:45], s[4:5] op_sel_hi:[1,0]
	s_waitcnt vmcnt(9)
	v_pk_mul_f32 v[38:39], v[38:39], s[4:5] op_sel_hi:[1,0]
	v_pk_mul_f32 v[40:41], v[40:41], s[4:5] op_sel_hi:[1,0]
	s_waitcnt vmcnt(8)
	v_pk_mul_f32 v[34:35], v[34:35], s[4:5] op_sel_hi:[1,0]
	v_pk_mul_f32 v[36:37], v[36:37], s[4:5] op_sel_hi:[1,0]
	v_readlane_b32 s4, v98, 14
	v_cvt_pk_bf16_f32 v51, v52, v53
	v_pk_fma_f32 v[36:37], v[82:83], v[36:37], v[4:5]
	v_pk_fma_f32 v[34:35], v[84:85], v[34:35], v[2:3]
	global_store_dwordx2 v[100:101], v[50:51], off offset:1536
	v_lshl_add_u64 v[50:51], v[150:151], 0, s[10:11]
	v_cvt_pk_bf16_f32 v34, v34, v35
	v_cvt_pk_bf16_f32 v35, v36, v37
	s_lshl_b64 s[10:11], s[38:39], 11
	s_waitcnt vmcnt(6)
; __device__ __forceinline__ unsigned cvtpk(float lo, float hi) { f32x2 v = {lo, hi}; bf16x2_t b = __builtin_convertvector(v, bf16x2_t); return __builtin_bit_cast(unsigned, b); }
; __device__ __forceinline__ float* xrow_ptr(float* xl, float* xc, int b, int t) { return (t < SEQ) ? xl + ((size_t)(b * SEQ + t)) * DM : xc + ((size_t)(b * CTXL + (t - SEQ))) * DM; }
; #define xl OUTP(launder(kargs))
; __device__ __forceinline__ void norm2_block(float* xl, float* xc, const float* MOD, const float* gn, const float* WP, bf16_t* H, float* AFF, int L, int row0, int nrows, int lane) {
;     ...
;     for (int r4 = 0; r4 < 4; ++r4) {
;         if (r4 * 4 < nrows) {
;             f32x4 v[4][4];
; #pragma unroll
;             for (int k = 0; k < 4; ++k) { const float* xq = xrow_ptr(xl, xc, b, t0 + r4 * 4 + k);
; #pragma unroll
;                 for (int j = 0; j < 4; ++j) v[k][j] = *(const f32x4*)(xq + 256 * j + 4 * lane); }
; #pragma unroll
;             for (int k = 0; k < 4; ++k) { const float rs = __builtin_bit_cast(float, __builtin_amdgcn_readlane(__builtin_bit_cast(int, rstd), r4 * 4 + k));
;                 bf16_t* hr = H + (size_t)(row0 + r4 * 4 + k) * DM;
; #pragma unroll
;                 for (int j = 0; j < 4; ++j) { const f32x4 h = (v[k][j] * rs) * mg[j] + sf[j]; u32x2 w; w.x = cvtpk(h[0], h[1]); w.y = cvtpk(h[2], h[3]); *(u32x2*)(hr + 256 * j + 4 * lane) = w; } }
;             asm volatile("" ::: "memory");
	v_pk_mul_f32 v[22:23], v[22:23], s[4:5] op_sel_hi:[1,0]
	v_pk_mul_f32 v[24:25], v[24:25], s[4:5] op_sel_hi:[1,0]
	v_pk_fma_f32 v[22:23], v[88:89], v[22:23], v[6:7]
	v_pk_fma_f32 v[24:25], v[86:87], v[24:25], v[8:9]
	s_waitcnt vmcnt(5)
	v_pk_mul_f32 v[18:19], v[18:19], s[4:5] op_sel_hi:[1,0]
	v_pk_mul_f32 v[20:21], v[20:21], s[4:5] op_sel_hi:[1,0]
	global_store_dwordx2 v[50:51], v[34:35], off offset:1536
	v_lshl_add_u64 v[34:35], v[150:151], 0, s[10:11]
	v_pk_mul_f32 v[30:31], v[30:31], s[4:5] op_sel_hi:[1,0]
	v_pk_mul_f32 v[32:33], v[32:33], s[4:5] op_sel_hi:[1,0]
	v_pk_mul_f32 v[26:27], v[26:27], s[4:5] op_sel_hi:[1,0]
	v_pk_mul_f32 v[28:29], v[28:29], s[4:5] op_sel_hi:[1,0]
	v_cvt_pk_bf16_f32 v22, v22, v23
	v_cvt_pk_bf16_f32 v23, v24, v25
	v_pk_fma_f32 v[20:21], v[82:83], v[20:21], v[4:5]
	v_pk_fma_f32 v[18:19], v[84:85], v[18:19], v[2:3]
	v_readlane_b32 s4, v98, 15
	global_store_dwordx2 v[34:35], v[22:23], off offset:1024
	v_cvt_pk_bf16_f32 v18, v18, v19
	v_cvt_pk_bf16_f32 v19, v20, v21
	s_add_i32 s38, s16, 0x107ff
	s_waitcnt vmcnt(6)
	v_pk_mul_f32 v[20:21], v[78:79], s[4:5] op_sel_hi:[1,0]
	v_pk_mul_f32 v[22:23], v[80:81], s[4:5] op_sel_hi:[1,0]
	v_pk_fma_f32 v[62:63], v[96:97], v[62:63], v[14:15]
	v_pk_fma_f32 v[48:49], v[94:95], v[48:49], v[16:17]
	v_pk_fma_f32 v[46:47], v[96:97], v[46:47], v[14:15]
	v_pk_fma_f32 v[32:33], v[94:95], v[32:33], v[16:17]
	v_pk_fma_f32 v[30:31], v[96:97], v[30:31], v[14:15]
	s_lshl_b64 s[10:11], s[38:39], 11
	v_pk_fma_f32 v[16:17], v[94:95], v[22:23], v[16:17]
	v_pk_fma_f32 v[14:15], v[96:97], v[20:21], v[14:15]
	global_store_dwordx2 v[34:35], v[18:19], off offset:1536
	v_lshl_add_u64 v[18:19], v[150:151], 0, s[10:11]
	v_cvt_pk_bf16_f32 v14, v14, v15
	v_cvt_pk_bf16_f32 v15, v16, v17
	global_store_dwordx2 v[18:19], v[14:15], off
	s_waitcnt vmcnt(7)
	v_pk_mul_f32 v[14:15], v[74:75], s[4:5] op_sel_hi:[1,0]
	v_pk_mul_f32 v[16:17], v[76:77], s[4:5] op_sel_hi:[1,0]
	v_pk_fma_f32 v[60:61], v[90:91], v[60:61], v[12:13]
	v_pk_fma_f32 v[58:59], v[92:93], v[58:59], v[10:11]
	v_pk_fma_f32 v[44:45], v[90:91], v[44:45], v[12:13]
	v_pk_fma_f32 v[42:43], v[92:93], v[42:43], v[10:11]
	v_pk_fma_f32 v[28:29], v[90:91], v[28:29], v[12:13]
	v_pk_fma_f32 v[26:27], v[92:93], v[26:27], v[10:11]
	v_pk_fma_f32 v[12:13], v[90:91], v[16:17], v[12:13]
	v_pk_fma_f32 v[10:11], v[92:93], v[14:15], v[10:11]
	v_pk_fma_f32 v[56:57], v[86:87], v[56:57], v[8:9]
	v_cvt_pk_bf16_f32 v10, v10, v11
	v_cvt_pk_bf16_f32 v11, v12, v13
	global_store_dwordx2 v[18:19], v[10:11], off offset:512
	s_waitcnt vmcnt(7)
	v_pk_mul_f32 v[10:11], v[70:71], s[4:5] op_sel_hi:[1,0]
	v_pk_mul_f32 v[12:13], v[72:73], s[4:5] op_sel_hi:[1,0]
	v_pk_fma_f32 v[54:55], v[88:89], v[54:55], v[6:7]
	v_pk_fma_f32 v[40:41], v[86:87], v[40:41], v[8:9]
	v_pk_fma_f32 v[38:39], v[88:89], v[38:39], v[6:7]
	v_pk_fma_f32 v[8:9], v[86:87], v[12:13], v[8:9]
	v_pk_fma_f32 v[6:7], v[88:89], v[10:11], v[6:7]
	v_cvt_pk_bf16_f32 v62, v62, v63
	v_cvt_pk_bf16_f32 v6, v6, v7
	v_cvt_pk_bf16_f32 v7, v8, v9
	global_store_dwordx2 v[18:19], v[6:7], off offset:1024
	s_waitcnt vmcnt(7)
	v_pk_mul_f32 v[6:7], v[66:67], s[4:5] op_sel_hi:[1,0]
	v_pk_mul_f32 v[8:9], v[68:69], s[4:5] op_sel_hi:[1,0]
	v_pk_fma_f32 v[2:3], v[84:85], v[6:7], v[2:3]
	v_pk_fma_f32 v[4:5], v[82:83], v[8:9], v[4:5]
	v_cvt_pk_bf16_f32 v63, v64, v65
	v_cvt_pk_bf16_f32 v58, v58, v59
	v_cvt_pk_bf16_f32 v59, v60, v61
	v_cvt_pk_bf16_f32 v54, v54, v55
	v_cvt_pk_bf16_f32 v55, v56, v57
	v_cvt_pk_bf16_f32 v46, v46, v47
	v_cvt_pk_bf16_f32 v47, v48, v49
	v_cvt_pk_bf16_f32 v42, v42, v43
	v_cvt_pk_bf16_f32 v43, v44, v45
	v_cvt_pk_bf16_f32 v38, v38, v39
	v_cvt_pk_bf16_f32 v39, v40, v41
	v_cvt_pk_bf16_f32 v30, v30, v31
	v_cvt_pk_bf16_f32 v31, v32, v33
	v_cvt_pk_bf16_f32 v26, v26, v27
	v_cvt_pk_bf16_f32 v27, v28, v29
	v_cvt_pk_bf16_f32 v2, v2, v3
	v_cvt_pk_bf16_f32 v3, v4, v5
	global_store_dwordx2 v[100:101], v[62:63], off
	global_store_dwordx2 v[100:101], v[58:59], off offset:512
	global_store_dwordx2 v[100:101], v[54:55], off offset:1024
	global_store_dwordx2 v[50:51], v[46:47], off
	global_store_dwordx2 v[50:51], v[42:43], off offset:512
	global_store_dwordx2 v[50:51], v[38:39], off offset:1024
	global_store_dwordx2 v[34:35], v[30:31], off
	global_store_dwordx2 v[34:35], v[26:27], off offset:512
	global_store_dwordx2 v[18:19], v[2:3], off offset:1536
